# attention main loop unrolled x4 with the LDS ring slot as an immediate offset (no per-tile address VALU/SALU) and separate loop copies for lead / non-lead waves (no per-tile role branches)
# speedup vs baseline: 1.0190x; 1.0098x over previous
; __device__ __forceinline__ int v_rd_base(int lane) { return ((lane & 3) << 3) | (((lane >> 2) & 3) << 6) | (((lane >> 4) & 1) << 5) | (((lane >> 5) & 1) << 8); }
; #define ATT_WAIT_BAR() asm volatile("s_waitcnt vmcnt(0) lgkmcnt(0)\n\ts_barrier" ::: "memory")
; __device__ __forceinline__ void attn_dma_body(const bf16_t* __restrict__ Qb, int ldq, int tpos0, const float* __restrict__ rope, const float* __restrict__ qgain, ...
;     ...
;   ATT_WAIT_BAR();
;   if (2 < NT) ATT_DMA(2, 2);
;   const int vb0 = (int)(uintptr_t)lds + 16384 + v_rd_base(lane);
;   f32x16 pA0, pA1, pB0, pB1; float mnA, mnB, alA, alB; bf16x8 pa0, pa1, pa2, pa3;
;   qkt(pA0, pA1, (const bf16_t*)lds, qr, r32, hi); partialSM(pA0, pA1, m_reg, mnA, alA);
;   const bool lead = __builtin_amdgcn_readfirstlane(wid) < 4;
;     ...
;   for (int j = 1; j + 1 < NT; j += 2) {
.Lf16_noprio:
	s_waitcnt vmcnt(0) lgkmcnt(0)
	s_barrier
	s_add_u32 s2, s38, 0x8000
	s_addc_u32 s3, s39, 0
	s_add_u32 s4, s40, 0x8000
	s_addc_u32 s5, s41, 0
	s_add_i32 s6, s96, 0x10000
	s_mov_b32 m0, s6
	s_nop 0
	global_load_lds_dwordx4 v170, s[2:3]
	s_add_i32 m0, s6, 0x2000
	s_nop 0
	global_load_lds_dwordx4 v172, s[2:3]
	s_add_i32 m0, s6, 0x4000
	s_nop 0
	global_load_lds_dwordx4 v171, s[4:5]
	s_add_i32 m0, s6, 0x6000
	s_nop 0
	global_load_lds_dwordx4 v173, s[4:5]
	s_add_u32 s2, s2, 0x4000
	s_addc_u32 s3, s3, 0
	s_add_u32 s4, s4, 0x4000
	s_addc_u32 s5, s5, 0
	v_add_u32_e32 v187, 0x10000, v183
	v_add_u32_e32 v188, 0x10000, v184
	v_add_u32_e32 v189, 0x10000, v185
	v_add_u32_e32 v190, 0x10000, v186
	v_add_u32_e32 v180, 0x10000, v191
	v_add_u32_e32 v181, 0x10000, v192
	s_mov_b32 s36, 0
	ds_read_b128 v[146:149], v183 offset:0
	ds_read_b128 v[150:153], v183 offset:4096
	ds_read_b128 v[154:157], v183 offset:8192
	ds_read_b128 v[158:161], v183 offset:12288
	ds_read_b128 v[198:201], v184 offset:0
	ds_read_b128 v[202:205], v184 offset:4096
	ds_read_b128 v[206:209], v184 offset:8192
	ds_read_b128 v[210:213], v184 offset:12288
	s_waitcnt lgkmcnt(7)
	v_mfma_f32_16x16x32_bf16 v[66:69], v[146:149], v[98:101], 0
	v_mfma_f32_16x16x32_bf16 v[70:73], v[146:149], v[114:117], 0
	ds_read_b128 v[146:149], v185 offset:0
	s_waitcnt lgkmcnt(7)
	v_mfma_f32_16x16x32_bf16 v[74:77], v[150:153], v[98:101], 0
	v_mfma_f32_16x16x32_bf16 v[78:81], v[150:153], v[114:117], 0
	ds_read_b128 v[150:153], v185 offset:4096
	s_waitcnt lgkmcnt(7)
	v_mfma_f32_16x16x32_bf16 v[82:85], v[154:157], v[98:101], 0
	v_mfma_f32_16x16x32_bf16 v[86:89], v[154:157], v[114:117], 0
	ds_read_b128 v[154:157], v185 offset:8192
	s_waitcnt lgkmcnt(7)
	v_mfma_f32_16x16x32_bf16 v[90:93], v[158:161], v[98:101], 0
	v_mfma_f32_16x16x32_bf16 v[94:97], v[158:161], v[114:117], 0
	ds_read_b128 v[158:161], v185 offset:12288
	s_waitcnt lgkmcnt(7)
	v_mfma_f32_16x16x32_bf16 v[66:69], v[198:201], v[102:105], v[66:69]
	v_mfma_f32_16x16x32_bf16 v[70:73], v[198:201], v[118:121], v[70:73]
	ds_read_b128 v[198:201], v186 offset:0
	s_waitcnt lgkmcnt(7)
	v_mfma_f32_16x16x32_bf16 v[74:77], v[202:205], v[102:105], v[74:77]
	v_mfma_f32_16x16x32_bf16 v[78:81], v[202:205], v[118:121], v[78:81]
	ds_read_b128 v[202:205], v186 offset:4096
	s_waitcnt lgkmcnt(7)
	v_mfma_f32_16x16x32_bf16 v[82:85], v[206:209], v[102:105], v[82:85]
	v_mfma_f32_16x16x32_bf16 v[86:89], v[206:209], v[118:121], v[86:89]
	ds_read_b128 v[206:209], v186 offset:8192
	s_waitcnt lgkmcnt(7)
	v_mfma_f32_16x16x32_bf16 v[90:93], v[210:213], v[102:105], v[90:93]
	v_mfma_f32_16x16x32_bf16 v[94:97], v[210:213], v[118:121], v[94:97]
	ds_read_b128 v[210:213], v186 offset:12288
	s_waitcnt lgkmcnt(7)
	v_mfma_f32_16x16x32_bf16 v[66:69], v[146:149], v[106:109], v[66:69]
	v_mfma_f32_16x16x32_bf16 v[70:73], v[146:149], v[122:125], v[70:73]
	s_waitcnt lgkmcnt(6)
	v_mfma_f32_16x16x32_bf16 v[74:77], v[150:153], v[106:109], v[74:77]
	v_mfma_f32_16x16x32_bf16 v[78:81], v[150:153], v[122:125], v[78:81]
	s_waitcnt lgkmcnt(5)
	v_mfma_f32_16x16x32_bf16 v[82:85], v[154:157], v[106:109], v[82:85]
	v_mfma_f32_16x16x32_bf16 v[86:89], v[154:157], v[122:125], v[86:89]
	s_waitcnt lgkmcnt(4)
	v_mfma_f32_16x16x32_bf16 v[90:93], v[158:161], v[106:109], v[90:93]
	v_mfma_f32_16x16x32_bf16 v[94:97], v[158:161], v[122:125], v[94:97]
	s_waitcnt lgkmcnt(3)
	v_mfma_f32_16x16x32_bf16 v[66:69], v[198:201], v[110:113], v[66:69]
	v_mfma_f32_16x16x32_bf16 v[70:73], v[198:201], v[126:129], v[70:73]
	s_waitcnt lgkmcnt(2)
	v_mfma_f32_16x16x32_bf16 v[74:77], v[202:205], v[110:113], v[74:77]
	v_mfma_f32_16x16x32_bf16 v[78:81], v[202:205], v[126:129], v[78:81]
	s_waitcnt lgkmcnt(1)
	v_mfma_f32_16x16x32_bf16 v[82:85], v[206:209], v[110:113], v[82:85]
	v_mfma_f32_16x16x32_bf16 v[86:89], v[206:209], v[126:129], v[86:89]
	s_waitcnt lgkmcnt(0)
	v_mfma_f32_16x16x32_bf16 v[90:93], v[210:213], v[110:113], v[90:93]
	v_mfma_f32_16x16x32_bf16 v[94:97], v[210:213], v[126:129], v[94:97]
	s_nop 7
	v_exp_f32_e32 v66, v66
	v_exp_f32_e32 v67, v67
	v_exp_f32_e32 v68, v68
	v_exp_f32_e32 v69, v69
	v_exp_f32_e32 v70, v70
	v_exp_f32_e32 v71, v71
	v_exp_f32_e32 v72, v72
	v_exp_f32_e32 v73, v73
	v_exp_f32_e32 v74, v74
	v_exp_f32_e32 v75, v75
	v_exp_f32_e32 v76, v76
	v_exp_f32_e32 v77, v77
	v_exp_f32_e32 v78, v78
	v_exp_f32_e32 v79, v79
	v_exp_f32_e32 v80, v80
	v_exp_f32_e32 v81, v81
	v_exp_f32_e32 v82, v82
	v_exp_f32_e32 v83, v83
	v_exp_f32_e32 v84, v84
	v_exp_f32_e32 v85, v85
	v_exp_f32_e32 v86, v86
	v_exp_f32_e32 v87, v87
	v_exp_f32_e32 v88, v88
	v_exp_f32_e32 v89, v89
	v_exp_f32_e32 v90, v90
	v_exp_f32_e32 v91, v91
	v_exp_f32_e32 v92, v92
	v_exp_f32_e32 v93, v93
	v_exp_f32_e32 v94, v94
	v_exp_f32_e32 v95, v95
	v_exp_f32_e32 v96, v96
	v_exp_f32_e32 v97, v97
	v_cvt_pk_bf16_f32 v130, v66, v67
	v_cvt_pk_bf16_f32 v131, v68, v69
	v_cvt_pk_bf16_f32 v132, v74, v75
	v_cvt_pk_bf16_f32 v133, v76, v77
	v_cvt_pk_bf16_f32 v134, v82, v83
	v_cvt_pk_bf16_f32 v135, v84, v85
	v_cvt_pk_bf16_f32 v136, v90, v91
	v_cvt_pk_bf16_f32 v137, v92, v93
	v_cvt_pk_bf16_f32 v138, v70, v71
	v_cvt_pk_bf16_f32 v139, v72, v73
	v_cvt_pk_bf16_f32 v140, v78, v79
	v_cvt_pk_bf16_f32 v141, v80, v81
	v_cvt_pk_bf16_f32 v142, v86, v87
	v_cvt_pk_bf16_f32 v143, v88, v89
	v_cvt_pk_bf16_f32 v144, v94, v95
	v_cvt_pk_bf16_f32 v145, v96, v97
	s_mov_b32 s97, 1
	s_cmp_lt_u32 s42, 4
	s_cbranch_scc1 .Lf16_L_loop
	.p2align 6
; #define SBAR() __builtin_amdgcn_sched_barrier(0)
; #define RESC(a) do { if (__any((a) < 1.f)) { if (hi == 0) al_l[r32] = (a); asm volatile("s_waitcnt lgkmcnt(0)" ::: "memory"); \
;     for (int d = 0; d < 4; ++d) for (int r = 0; r < 16; ++r) o[d][r] *= al_l[crow(r, hi)]; } } while (0)
; #define ATT_SYNC(jn) do { ATT_WAIT_BAR(); if ((jn) < NT) ATT_DMA((jn), (jn) & 3); } while (0)
; template <int D0> __device__ __forceinline__ void pv_rd(s16x4 (&r)[8], int vb) {
;   r[0] = tr_read<v_rd_off(D0, 0, 0)>(vb); r[1] = tr_read<v_rd_off(D0, 0, 1)>(vb); r[2] = tr_read<v_rd_off(D0, 1, 0)>(vb); r[3] = tr_read<v_rd_off(D0, 1, 1)>(vb);
;   r[4] = tr_read<v_rd_off(D0, 2, 0)>(vb); r[5] = tr_read<v_rd_off(D0, 2, 1)>(vb); r[6] = tr_read<v_rd_off(D0, 3, 0)>(vb); r[7] = tr_read<v_rd_off(D0, 3, 1)>(vb);
; }
; __device__ __forceinline__ void pv_mm(f32x16& od, const s16x4 (&r)[8], bf16x8 pa0, bf16x8 pa1, bf16x8 pa2, bf16x8 pa3) {
;     ...
;   od = __builtin_amdgcn_mfma_f32_32x32x16_bf16(pa0, PK(r[0], r[1]), od, 0, 0, 0);
;   od = __builtin_amdgcn_mfma_f32_32x32x16_bf16(pa1, PK(r[2], r[3]), od, 0, 0, 0);
;   od = __builtin_amdgcn_mfma_f32_32x32x16_bf16(pa2, PK(r[4], r[5]), od, 0, 0, 0);
;   od = __builtin_amdgcn_mfma_f32_32x32x16_bf16(pa3, PK(r[6], r[7]), od, 0, 0, 0);
;     ...
; }
; __device__ __forceinline__ void attn_dma_body(const bf16_t* __restrict__ Qb, int ldq, int tpos0, const float* __restrict__ rope, const float* __restrict__ qgain, ...
;     ...
;   for (int j = 1; j + 1 < NT; j += 2) {
;     { SBAR(); qkt(pB0, pB1, (const bf16_t*)(lds + (j & 3) * SHM_SLOT), qr, r32, hi);
;       finishSM(pA0, pA1, alA, l_reg, pa0, pa1, pa2, pa3); s16x4 va[8]; pv_rd<0>(va, vb0 + ((j - 1) & 3) * (int)SHM_SLOT); SBAR();
;       if (!lead) ATT_SYNC(j + 2);
;       pv_d0_pre(o, vb0 + ((j - 1) & 3) * (int)SHM_SLOT, va, pa0, pa1, pa2, pa3); partialSM(pB0, pB1, m_reg, mnB, alB);
;       if (lead) ATT_SYNC(j + 2);
;       RESC(alB); }
;     { SBAR(); qkt(pA0, pA1, (const bf16_t*)(lds + ((j + 1) & 3) * SHM_SLOT), qr, r32, hi);
;       finishSM(pB0, pB1, alB, l_reg, pa0, pa1, pa2, pa3); s16x4 va[8]; pv_rd<0>(va, vb0 + (j & 3) * (int)SHM_SLOT); SBAR();
;       if (!lead) ATT_SYNC(j + 3);
;       pv_d0_pre(o, vb0 + (j & 3) * (int)SHM_SLOT, va, pa0, pa1, pa2, pa3); partialSM(pA0, pA1, m_reg, mnA, alA);
;       if (lead) ATT_SYNC(j + 3);
;       RESC(alA); }
;   }
.Lf16_N_loop:
	ds_read_b128 v[146:149], v183 offset:32768
	ds_read_b128 v[150:153], v183 offset:36864
	ds_read_b128 v[154:157], v183 offset:40960
	ds_read_b128 v[158:161], v183 offset:45056
	ds_read_b128 v[198:201], v184 offset:32768
	ds_read_b128 v[202:205], v184 offset:36864
	ds_read_b128 v[206:209], v184 offset:40960
	ds_read_b128 v[210:213], v184 offset:45056
	s_waitcnt lgkmcnt(7)
	v_mfma_f32_16x16x32_bf16 v[66:69], v[146:149], v[98:101], 0
	v_mfma_f32_16x16x32_bf16 v[70:73], v[146:149], v[114:117], 0
	ds_read_b128 v[146:149], v185 offset:32768
	s_waitcnt lgkmcnt(7)
	v_mfma_f32_16x16x32_bf16 v[74:77], v[150:153], v[98:101], 0
	v_mfma_f32_16x16x32_bf16 v[78:81], v[150:153], v[114:117], 0
	ds_read_b128 v[150:153], v185 offset:36864
	s_waitcnt lgkmcnt(7)
	v_mfma_f32_16x16x32_bf16 v[82:85], v[154:157], v[98:101], 0
	v_mfma_f32_16x16x32_bf16 v[86:89], v[154:157], v[114:117], 0
	ds_read_b128 v[154:157], v185 offset:40960
	s_waitcnt lgkmcnt(7)
	v_mfma_f32_16x16x32_bf16 v[90:93], v[158:161], v[98:101], 0
	v_mfma_f32_16x16x32_bf16 v[94:97], v[158:161], v[114:117], 0
	ds_read_b128 v[158:161], v185 offset:45056
	s_waitcnt lgkmcnt(7)
	v_mfma_f32_16x16x32_bf16 v[66:69], v[198:201], v[102:105], v[66:69]
	v_mfma_f32_16x16x32_bf16 v[70:73], v[198:201], v[118:121], v[70:73]
	ds_read_b128 v[198:201], v186 offset:32768
	s_waitcnt lgkmcnt(7)
	v_mfma_f32_16x16x32_bf16 v[74:77], v[202:205], v[102:105], v[74:77]
	v_mfma_f32_16x16x32_bf16 v[78:81], v[202:205], v[118:121], v[78:81]
	ds_read_b128 v[202:205], v186 offset:36864
	s_waitcnt lgkmcnt(7)
	v_mfma_f32_16x16x32_bf16 v[82:85], v[206:209], v[102:105], v[82:85]
	v_mfma_f32_16x16x32_bf16 v[86:89], v[206:209], v[118:121], v[86:89]
	ds_read_b128 v[206:209], v186 offset:40960
	s_waitcnt lgkmcnt(7)
	v_mfma_f32_16x16x32_bf16 v[90:93], v[210:213], v[102:105], v[90:93]
	v_mfma_f32_16x16x32_bf16 v[94:97], v[210:213], v[118:121], v[94:97]
	ds_read_b128 v[210:213], v186 offset:45056
	s_waitcnt lgkmcnt(7)
	v_mfma_f32_16x16x32_bf16 v[66:69], v[146:149], v[106:109], v[66:69]
	v_mfma_f32_16x16x32_bf16 v[70:73], v[146:149], v[122:125], v[70:73]
	s_waitcnt lgkmcnt(6)
	v_mfma_f32_16x16x32_bf16 v[74:77], v[150:153], v[106:109], v[74:77]
	v_mfma_f32_16x16x32_bf16 v[78:81], v[150:153], v[122:125], v[78:81]
	s_waitcnt lgkmcnt(5)
	v_mfma_f32_16x16x32_bf16 v[82:85], v[154:157], v[106:109], v[82:85]
	v_mfma_f32_16x16x32_bf16 v[86:89], v[154:157], v[122:125], v[86:89]
	s_waitcnt lgkmcnt(4)
	v_mfma_f32_16x16x32_bf16 v[90:93], v[158:161], v[106:109], v[90:93]
	v_mfma_f32_16x16x32_bf16 v[94:97], v[158:161], v[122:125], v[94:97]
	s_waitcnt lgkmcnt(3)
	v_mfma_f32_16x16x32_bf16 v[66:69], v[198:201], v[110:113], v[66:69]
	v_mfma_f32_16x16x32_bf16 v[70:73], v[198:201], v[126:129], v[70:73]
	ds_read_b64_tr_b16 v[214:215], v191 offset:0
	ds_read_b64_tr_b16 v[216:217], v191 offset:4096
	ds_read_b64_tr_b16 v[218:219], v192 offset:0
	ds_read_b64_tr_b16 v[220:221], v192 offset:4096
	ds_read_b64_tr_b16 v[222:223], v191 offset:512
	ds_read_b64_tr_b16 v[224:225], v191 offset:4608
	ds_read_b64_tr_b16 v[226:227], v192 offset:512
	ds_read_b64_tr_b16 v[228:229], v192 offset:4608
	s_waitcnt lgkmcnt(10)
	v_mfma_f32_16x16x32_bf16 v[74:77], v[202:205], v[110:113], v[74:77]
	v_mfma_f32_16x16x32_bf16 v[78:81], v[202:205], v[126:129], v[78:81]
	s_waitcnt lgkmcnt(9)
	v_mfma_f32_16x16x32_bf16 v[82:85], v[206:209], v[110:113], v[82:85]
	v_mfma_f32_16x16x32_bf16 v[86:89], v[206:209], v[126:129], v[86:89]
	s_waitcnt lgkmcnt(8)
	v_mfma_f32_16x16x32_bf16 v[90:93], v[210:213], v[110:113], v[90:93]
	v_mfma_f32_16x16x32_bf16 v[94:97], v[210:213], v[126:129], v[94:97]
	s_cmp_ge_u32 s97, 131
	s_cbranch_scc1 .Lf16_se_N0
	s_waitcnt vmcnt(0) lgkmcnt(0)
	s_barrier
	s_cmp_ge_u32 s97, 130
	s_cbranch_scc1 .Lf16_se_N0
	s_add_i32 s6, s96, 0x18000
	s_mov_b32 m0, s6
	s_nop 0
	global_load_lds_dwordx4 v170, s[2:3]
	s_add_i32 m0, s6, 0x2000
	s_nop 0
	global_load_lds_dwordx4 v172, s[2:3]
	s_add_i32 m0, s6, 0x4000
	s_nop 0
	global_load_lds_dwordx4 v171, s[4:5]
	s_add_i32 m0, s6, 0x6000
	s_nop 0
	global_load_lds_dwordx4 v173, s[4:5]
	s_add_u32 s2, s2, 0x4000
	s_addc_u32 s3, s3, 0
	s_add_u32 s4, s4, 0x4000
	s_addc_u32 s5, s5, 0
.Lf16_se_N0:
	s_waitcnt lgkmcnt(6)
	v_mfma_f32_16x16x32_bf16 v[2:5], v[214:217], v[130:133], v[2:5]
	v_exp_f32_e32 v66, v66
	v_mfma_f32_16x16x32_bf16 v[6:9], v[214:217], v[138:141], v[6:9]
	v_exp_f32_e32 v67, v67
	ds_read_b64_tr_b16 v[230:231], v191 offset:1024
	ds_read_b64_tr_b16 v[232:233], v191 offset:5120
	s_waitcnt lgkmcnt(6)
	v_mfma_f32_16x16x32_bf16 v[10:13], v[218:221], v[130:133], v[10:13]
	v_exp_f32_e32 v68, v68
	v_mfma_f32_16x16x32_bf16 v[14:17], v[218:221], v[138:141], v[14:17]
	v_exp_f32_e32 v69, v69
	ds_read_b64_tr_b16 v[234:235], v192 offset:1024
	ds_read_b64_tr_b16 v[236:237], v192 offset:5120
	s_waitcnt lgkmcnt(6)
	v_mfma_f32_16x16x32_bf16 v[18:21], v[222:225], v[130:133], v[18:21]
	v_exp_f32_e32 v70, v70
	v_mfma_f32_16x16x32_bf16 v[22:25], v[222:225], v[138:141], v[22:25]
	v_exp_f32_e32 v71, v71
	ds_read_b64_tr_b16 v[238:239], v191 offset:1536
	ds_read_b64_tr_b16 v[240:241], v191 offset:5632
	s_waitcnt lgkmcnt(6)
	v_mfma_f32_16x16x32_bf16 v[26:29], v[226:229], v[130:133], v[26:29]
	v_exp_f32_e32 v72, v72
	v_mfma_f32_16x16x32_bf16 v[30:33], v[226:229], v[138:141], v[30:33]
	v_exp_f32_e32 v73, v73
	v_mfma_f32_16x16x32_bf16 v[246:249], v[194:197], v[130:133], v[246:249]
	ds_read_b64_tr_b16 v[242:243], v192 offset:1536
	ds_read_b64_tr_b16 v[244:245], v192 offset:5632
	s_waitcnt lgkmcnt(6)
	v_mfma_f32_16x16x32_bf16 v[34:37], v[230:233], v[130:133], v[34:37]
	v_exp_f32_e32 v74, v74
	v_mfma_f32_16x16x32_bf16 v[38:41], v[230:233], v[138:141], v[38:41]
	v_exp_f32_e32 v75, v75
	ds_read_b64_tr_b16 v[214:215], v191 offset:8192
	ds_read_b64_tr_b16 v[216:217], v191 offset:12288
	s_waitcnt lgkmcnt(6)
; __device__ __forceinline__ void finishSM(f32x16& p0, f32x16& p1, float alpha, float& l_reg, bf16x8& pa0, bf16x8& pa1, bf16x8& pa2, bf16x8& pa3) {
;   for (int r = 0; r < 16; ++r) p1[r] = __builtin_amdgcn_exp2f(p1[r]);
;   float ps = 0; for (int r = 0; r < 16; ++r) ps += p0[r]; for (int r = 0; r < 16; ++r) ps += p1[r];
;   { auto rr = __builtin_amdgcn_permlane32_swap(__float_as_uint(ps), __float_as_uint(ps), false, false);
;     ps = __uint_as_float(rr[0]) + __uint_as_float(rr[1]); }
;   l_reg = l_reg * alpha + ps;
;     ...
;   PK4(p0, 0, pa0); PK4(p0, 8, pa1); PK4(p1, 0, pa2); PK4(p1, 8, pa3);
; template <int D0> __device__ __forceinline__ void pv_rd(s16x4 (&r)[8], int vb) {
;   r[0] = tr_read<v_rd_off(D0, 0, 0)>(vb); r[1] = tr_read<v_rd_off(D0, 0, 1)>(vb); r[2] = tr_read<v_rd_off(D0, 1, 0)>(vb); r[3] = tr_read<v_rd_off(D0, 1, 1)>(vb);
;   r[4] = tr_read<v_rd_off(D0, 2, 0)>(vb); r[5] = tr_read<v_rd_off(D0, 2, 1)>(vb); r[6] = tr_read<v_rd_off(D0, 3, 0)>(vb); r[7] = tr_read<v_rd_off(D0, 3, 1)>(vb);
; }
; __device__ __forceinline__ void pv_mm(f32x16& od, const s16x4 (&r)[8], bf16x8 pa0, bf16x8 pa1, bf16x8 pa2, bf16x8 pa3) {
;     ...
;   od = __builtin_amdgcn_mfma_f32_32x32x16_bf16(pa0, PK(r[0], r[1]), od, 0, 0, 0);
;   od = __builtin_amdgcn_mfma_f32_32x32x16_bf16(pa1, PK(r[2], r[3]), od, 0, 0, 0);
; __device__ __forceinline__ void attn_dma_body(const bf16_t* __restrict__ Qb, int ldq, int tpos0, const float* __restrict__ rope, const float* __restrict__ qgain, ...
;     ...
;   for (int j = 1; j + 1 < NT; j += 2) {
;     { SBAR(); qkt(pB0, pB1, (const bf16_t*)(lds + (j & 3) * SHM_SLOT), qr, r32, hi);
;       finishSM(pA0, pA1, alA, l_reg, pa0, pa1, pa2, pa3); s16x4 va[8]; pv_rd<0>(va, vb0 + ((j - 1) & 3) * (int)SHM_SLOT); SBAR();
;       if (!lead) ATT_SYNC(j + 2);
;       pv_d0_pre(o, vb0 + ((j - 1) & 3) * (int)SHM_SLOT, va, pa0, pa1, pa2, pa3); partialSM(pB0, pB1, m_reg, mnB, alB);
;       if (lead) ATT_SYNC(j + 2);
;       RESC(alB); }
;     { SBAR(); qkt(pA0, pA1, (const bf16_t*)(lds + ((j + 1) & 3) * SHM_SLOT), qr, r32, hi);
;       finishSM(pB0, pB1, alB, l_reg, pa0, pa1, pa2, pa3); s16x4 va[8]; pv_rd<0>(va, vb0 + (j & 3) * (int)SHM_SLOT); SBAR();
;       if (!lead) ATT_SYNC(j + 3);
;       pv_d0_pre(o, vb0 + (j & 3) * (int)SHM_SLOT, va, pa0, pa1, pa2, pa3); partialSM(pA0, pA1, m_reg, mnA, alA);
;       if (lead) ATT_SYNC(j + 3);
;       RESC(alA); }
;   }
	v_mfma_f32_16x16x32_bf16 v[42:45], v[234:237], v[130:133], v[42:45]
	v_exp_f32_e32 v76, v76
	v_mfma_f32_16x16x32_bf16 v[46:49], v[234:237], v[138:141], v[46:49]
	v_exp_f32_e32 v77, v77
	ds_read_b64_tr_b16 v[218:219], v192 offset:8192
	ds_read_b64_tr_b16 v[220:221], v192 offset:12288
	s_waitcnt lgkmcnt(6)
	v_mfma_f32_16x16x32_bf16 v[50:53], v[238:241], v[130:133], v[50:53]
	v_exp_f32_e32 v78, v78
	v_mfma_f32_16x16x32_bf16 v[54:57], v[238:241], v[138:141], v[54:57]
	v_exp_f32_e32 v79, v79
	ds_read_b64_tr_b16 v[222:223], v191 offset:8704
	ds_read_b64_tr_b16 v[224:225], v191 offset:12800
	s_waitcnt lgkmcnt(6)
	v_mfma_f32_16x16x32_bf16 v[58:61], v[242:245], v[130:133], v[58:61]
	v_exp_f32_e32 v80, v80
	v_mfma_f32_16x16x32_bf16 v[62:65], v[242:245], v[138:141], v[62:65]
	v_exp_f32_e32 v81, v81
	v_mfma_f32_16x16x32_bf16 v[252:255], v[194:197], v[138:141], v[252:255]
	ds_read_b64_tr_b16 v[226:227], v192 offset:8704
	ds_read_b64_tr_b16 v[228:229], v192 offset:12800
	s_waitcnt lgkmcnt(6)
	v_mfma_f32_16x16x32_bf16 v[2:5], v[214:217], v[134:137], v[2:5]
	v_exp_f32_e32 v82, v82
	v_mfma_f32_16x16x32_bf16 v[6:9], v[214:217], v[142:145], v[6:9]
	v_exp_f32_e32 v83, v83
	ds_read_b64_tr_b16 v[230:231], v191 offset:9216
	ds_read_b64_tr_b16 v[232:233], v191 offset:13312
	s_waitcnt lgkmcnt(6)
	v_mfma_f32_16x16x32_bf16 v[10:13], v[218:221], v[134:137], v[10:13]
	v_exp_f32_e32 v84, v84
	v_mfma_f32_16x16x32_bf16 v[14:17], v[218:221], v[142:145], v[14:17]
	v_exp_f32_e32 v85, v85
	ds_read_b64_tr_b16 v[234:235], v192 offset:9216
	ds_read_b64_tr_b16 v[236:237], v192 offset:13312
	s_waitcnt lgkmcnt(6)
	v_mfma_f32_16x16x32_bf16 v[18:21], v[222:225], v[134:137], v[18:21]
	v_exp_f32_e32 v86, v86
	v_mfma_f32_16x16x32_bf16 v[22:25], v[222:225], v[142:145], v[22:25]
	v_exp_f32_e32 v87, v87
	ds_read_b64_tr_b16 v[238:239], v191 offset:9728
	ds_read_b64_tr_b16 v[240:241], v191 offset:13824
	s_waitcnt lgkmcnt(6)
	v_mfma_f32_16x16x32_bf16 v[26:29], v[226:229], v[134:137], v[26:29]
	v_exp_f32_e32 v88, v88
	v_mfma_f32_16x16x32_bf16 v[30:33], v[226:229], v[142:145], v[30:33]
	v_exp_f32_e32 v89, v89
	v_mfma_f32_16x16x32_bf16 v[246:249], v[194:197], v[134:137], v[246:249]
	ds_read_b64_tr_b16 v[242:243], v192 offset:9728
	ds_read_b64_tr_b16 v[244:245], v192 offset:13824
	s_waitcnt lgkmcnt(6)
	v_mfma_f32_16x16x32_bf16 v[34:37], v[230:233], v[134:137], v[34:37]
	v_exp_f32_e32 v90, v90
	v_mfma_f32_16x16x32_bf16 v[38:41], v[230:233], v[142:145], v[38:41]
	v_exp_f32_e32 v91, v91
	s_waitcnt lgkmcnt(4)
	v_mfma_f32_16x16x32_bf16 v[42:45], v[234:237], v[134:137], v[42:45]
	v_exp_f32_e32 v92, v92
	v_mfma_f32_16x16x32_bf16 v[46:49], v[234:237], v[142:145], v[46:49]
	v_exp_f32_e32 v93, v93
	s_waitcnt lgkmcnt(2)
	v_mfma_f32_16x16x32_bf16 v[50:53], v[238:241], v[134:137], v[50:53]
	v_exp_f32_e32 v94, v94
	v_mfma_f32_16x16x32_bf16 v[54:57], v[238:241], v[142:145], v[54:57]
	v_exp_f32_e32 v95, v95
	s_waitcnt lgkmcnt(0)
	v_mfma_f32_16x16x32_bf16 v[58:61], v[242:245], v[134:137], v[58:61]
	v_exp_f32_e32 v96, v96
	v_mfma_f32_16x16x32_bf16 v[62:65], v[242:245], v[142:145], v[62:65]
	v_exp_f32_e32 v97, v97
	v_mfma_f32_16x16x32_bf16 v[252:255], v[194:197], v[142:145], v[252:255]
	v_cvt_pk_bf16_f32 v130, v66, v67
	v_cvt_pk_bf16_f32 v131, v68, v69
	v_cvt_pk_bf16_f32 v132, v74, v75
	v_cvt_pk_bf16_f32 v133, v76, v77
	v_cvt_pk_bf16_f32 v134, v82, v83
	v_cvt_pk_bf16_f32 v135, v84, v85
	v_cvt_pk_bf16_f32 v136, v90, v91
	v_cvt_pk_bf16_f32 v137, v92, v93
	v_cvt_pk_bf16_f32 v138, v70, v71
	v_cvt_pk_bf16_f32 v139, v72, v73
	v_cvt_pk_bf16_f32 v140, v78, v79
	v_cvt_pk_bf16_f32 v141, v80, v81
	v_cvt_pk_bf16_f32 v142, v86, v87
	v_cvt_pk_bf16_f32 v143, v88, v89
	v_cvt_pk_bf16_f32 v144, v94, v95
	v_cvt_pk_bf16_f32 v145, v96, v97
	s_add_i32 s97, s97, 1
	s_cmp_lt_u32 s97, 132
	s_cbranch_scc0 .Lf16_done
	ds_read_b128 v[146:149], v187 offset:0
	ds_read_b128 v[150:153], v187 offset:4096
	ds_read_b128 v[154:157], v187 offset:8192
	ds_read_b128 v[158:161], v187 offset:12288
	ds_read_b128 v[198:201], v188 offset:0
	ds_read_b128 v[202:205], v188 offset:4096
	ds_read_b128 v[206:209], v188 offset:8192
	ds_read_b128 v[210:213], v188 offset:12288
	s_waitcnt lgkmcnt(7)
	v_mfma_f32_16x16x32_bf16 v[66:69], v[146:149], v[98:101], 0
	v_mfma_f32_16x16x32_bf16 v[70:73], v[146:149], v[114:117], 0
	ds_read_b128 v[146:149], v189 offset:0
	s_waitcnt lgkmcnt(7)
	v_mfma_f32_16x16x32_bf16 v[74:77], v[150:153], v[98:101], 0
	v_mfma_f32_16x16x32_bf16 v[78:81], v[150:153], v[114:117], 0
	ds_read_b128 v[150:153], v189 offset:4096
	s_waitcnt lgkmcnt(7)
	v_mfma_f32_16x16x32_bf16 v[82:85], v[154:157], v[98:101], 0
	v_mfma_f32_16x16x32_bf16 v[86:89], v[154:157], v[114:117], 0
	ds_read_b128 v[154:157], v189 offset:8192
	s_waitcnt lgkmcnt(7)
	v_mfma_f32_16x16x32_bf16 v[90:93], v[158:161], v[98:101], 0
	v_mfma_f32_16x16x32_bf16 v[94:97], v[158:161], v[114:117], 0
	ds_read_b128 v[158:161], v189 offset:12288
	s_waitcnt lgkmcnt(7)
	v_mfma_f32_16x16x32_bf16 v[66:69], v[198:201], v[102:105], v[66:69]
	v_mfma_f32_16x16x32_bf16 v[70:73], v[198:201], v[118:121], v[70:73]
	ds_read_b128 v[198:201], v190 offset:0
	s_waitcnt lgkmcnt(7)
	v_mfma_f32_16x16x32_bf16 v[74:77], v[202:205], v[102:105], v[74:77]
	v_mfma_f32_16x16x32_bf16 v[78:81], v[202:205], v[118:121], v[78:81]
	ds_read_b128 v[202:205], v190 offset:4096
	s_waitcnt lgkmcnt(7)
	v_mfma_f32_16x16x32_bf16 v[82:85], v[206:209], v[102:105], v[82:85]
	v_mfma_f32_16x16x32_bf16 v[86:89], v[206:209], v[118:121], v[86:89]
	ds_read_b128 v[206:209], v190 offset:8192
	s_waitcnt lgkmcnt(7)
	v_mfma_f32_16x16x32_bf16 v[90:93], v[210:213], v[102:105], v[90:93]
	v_mfma_f32_16x16x32_bf16 v[94:97], v[210:213], v[118:121], v[94:97]
	ds_read_b128 v[210:213], v190 offset:12288
	s_waitcnt lgkmcnt(7)
; #define SBAR() __builtin_amdgcn_sched_barrier(0)
; #define RESC(a) do { if (__any((a) < 1.f)) { if (hi == 0) al_l[r32] = (a); asm volatile("s_waitcnt lgkmcnt(0)" ::: "memory"); \
;     for (int d = 0; d < 4; ++d) for (int r = 0; r < 16; ++r) o[d][r] *= al_l[crow(r, hi)]; } } while (0)
; #define ATT_SYNC(jn) do { ATT_WAIT_BAR(); if ((jn) < NT) ATT_DMA((jn), (jn) & 3); } while (0)
; template <int D0> __device__ __forceinline__ void pv_rd(s16x4 (&r)[8], int vb) {
;   r[0] = tr_read<v_rd_off(D0, 0, 0)>(vb); r[1] = tr_read<v_rd_off(D0, 0, 1)>(vb); r[2] = tr_read<v_rd_off(D0, 1, 0)>(vb); r[3] = tr_read<v_rd_off(D0, 1, 1)>(vb);
;   r[4] = tr_read<v_rd_off(D0, 2, 0)>(vb); r[5] = tr_read<v_rd_off(D0, 2, 1)>(vb); r[6] = tr_read<v_rd_off(D0, 3, 0)>(vb); r[7] = tr_read<v_rd_off(D0, 3, 1)>(vb);
; }
; __device__ __forceinline__ void pv_mm(f32x16& od, const s16x4 (&r)[8], bf16x8 pa0, bf16x8 pa1, bf16x8 pa2, bf16x8 pa3) {
;     ...
;   od = __builtin_amdgcn_mfma_f32_32x32x16_bf16(pa0, PK(r[0], r[1]), od, 0, 0, 0);
;   od = __builtin_amdgcn_mfma_f32_32x32x16_bf16(pa1, PK(r[2], r[3]), od, 0, 0, 0);
;   od = __builtin_amdgcn_mfma_f32_32x32x16_bf16(pa2, PK(r[4], r[5]), od, 0, 0, 0);
;   od = __builtin_amdgcn_mfma_f32_32x32x16_bf16(pa3, PK(r[6], r[7]), od, 0, 0, 0);
;     ...
; }
; __device__ __forceinline__ void attn_dma_body(const bf16_t* __restrict__ Qb, int ldq, int tpos0, const float* __restrict__ rope, const float* __restrict__ qgain, ...
;     ...
;   for (int j = 1; j + 1 < NT; j += 2) {
;     { SBAR(); qkt(pB0, pB1, (const bf16_t*)(lds + (j & 3) * SHM_SLOT), qr, r32, hi);
;       finishSM(pA0, pA1, alA, l_reg, pa0, pa1, pa2, pa3); s16x4 va[8]; pv_rd<0>(va, vb0 + ((j - 1) & 3) * (int)SHM_SLOT); SBAR();
;       if (!lead) ATT_SYNC(j + 2);
;       pv_d0_pre(o, vb0 + ((j - 1) & 3) * (int)SHM_SLOT, va, pa0, pa1, pa2, pa3); partialSM(pB0, pB1, m_reg, mnB, alB);
;       if (lead) ATT_SYNC(j + 2);
;       RESC(alB); }
;     { SBAR(); qkt(pA0, pA1, (const bf16_t*)(lds + ((j + 1) & 3) * SHM_SLOT), qr, r32, hi);
;       finishSM(pB0, pB1, alB, l_reg, pa0, pa1, pa2, pa3); s16x4 va[8]; pv_rd<0>(va, vb0 + (j & 3) * (int)SHM_SLOT); SBAR();
;       if (!lead) ATT_SYNC(j + 3);
;       pv_d0_pre(o, vb0 + (j & 3) * (int)SHM_SLOT, va, pa0, pa1, pa2, pa3); partialSM(pA0, pA1, m_reg, mnA, alA);
;       if (lead) ATT_SYNC(j + 3);
;       RESC(alA); }
;   }
	v_mfma_f32_16x16x32_bf16 v[66:69], v[146:149], v[106:109], v[66:69]
	v_mfma_f32_16x16x32_bf16 v[70:73], v[146:149], v[122:125], v[70:73]
	s_waitcnt lgkmcnt(6)
	v_mfma_f32_16x16x32_bf16 v[74:77], v[150:153], v[106:109], v[74:77]
	v_mfma_f32_16x16x32_bf16 v[78:81], v[150:153], v[122:125], v[78:81]
	s_waitcnt lgkmcnt(5)
	v_mfma_f32_16x16x32_bf16 v[82:85], v[154:157], v[106:109], v[82:85]
	v_mfma_f32_16x16x32_bf16 v[86:89], v[154:157], v[122:125], v[86:89]
	s_waitcnt lgkmcnt(4)
	v_mfma_f32_16x16x32_bf16 v[90:93], v[158:161], v[106:109], v[90:93]
	v_mfma_f32_16x16x32_bf16 v[94:97], v[158:161], v[122:125], v[94:97]
	s_waitcnt lgkmcnt(3)
	v_mfma_f32_16x16x32_bf16 v[66:69], v[198:201], v[110:113], v[66:69]
	v_mfma_f32_16x16x32_bf16 v[70:73], v[198:201], v[126:129], v[70:73]
	ds_read_b64_tr_b16 v[214:215], v191 offset:32768
	ds_read_b64_tr_b16 v[216:217], v191 offset:36864
	ds_read_b64_tr_b16 v[218:219], v192 offset:32768
	ds_read_b64_tr_b16 v[220:221], v192 offset:36864
	ds_read_b64_tr_b16 v[222:223], v191 offset:33280
	ds_read_b64_tr_b16 v[224:225], v191 offset:37376
	ds_read_b64_tr_b16 v[226:227], v192 offset:33280
	ds_read_b64_tr_b16 v[228:229], v192 offset:37376
	s_waitcnt lgkmcnt(10)
	v_mfma_f32_16x16x32_bf16 v[74:77], v[202:205], v[110:113], v[74:77]
	v_mfma_f32_16x16x32_bf16 v[78:81], v[202:205], v[126:129], v[78:81]
	s_waitcnt lgkmcnt(9)
	v_mfma_f32_16x16x32_bf16 v[82:85], v[206:209], v[110:113], v[82:85]
	v_mfma_f32_16x16x32_bf16 v[86:89], v[206:209], v[126:129], v[86:89]
	s_waitcnt lgkmcnt(8)
	v_mfma_f32_16x16x32_bf16 v[90:93], v[210:213], v[110:113], v[90:93]
	v_mfma_f32_16x16x32_bf16 v[94:97], v[210:213], v[126:129], v[94:97]
	s_cmp_ge_u32 s97, 131
	s_cbranch_scc1 .Lf16_se_N1
	s_waitcnt vmcnt(0) lgkmcnt(0)
	s_barrier
	s_cmp_ge_u32 s97, 130
	s_cbranch_scc1 .Lf16_se_N1
	s_add_i32 s6, s96, 0x0
	s_mov_b32 m0, s6
	s_nop 0
	global_load_lds_dwordx4 v170, s[2:3]
	s_add_i32 m0, s6, 0x2000
	s_nop 0
	global_load_lds_dwordx4 v172, s[2:3]
	s_add_i32 m0, s6, 0x4000
	s_nop 0
	global_load_lds_dwordx4 v171, s[4:5]
	s_add_i32 m0, s6, 0x6000
	s_nop 0
	global_load_lds_dwordx4 v173, s[4:5]
	s_add_u32 s2, s2, 0x4000
	s_addc_u32 s3, s3, 0
	s_add_u32 s4, s4, 0x4000
	s_addc_u32 s5, s5, 0
.Lf16_se_N1:
	s_waitcnt lgkmcnt(6)
	v_mfma_f32_16x16x32_bf16 v[2:5], v[214:217], v[130:133], v[2:5]
	v_exp_f32_e32 v66, v66
	v_mfma_f32_16x16x32_bf16 v[6:9], v[214:217], v[138:141], v[6:9]
	v_exp_f32_e32 v67, v67
	ds_read_b64_tr_b16 v[230:231], v191 offset:33792
	ds_read_b64_tr_b16 v[232:233], v191 offset:37888
	s_waitcnt lgkmcnt(6)
	v_mfma_f32_16x16x32_bf16 v[10:13], v[218:221], v[130:133], v[10:13]
	v_exp_f32_e32 v68, v68
	v_mfma_f32_16x16x32_bf16 v[14:17], v[218:221], v[138:141], v[14:17]
	v_exp_f32_e32 v69, v69
	ds_read_b64_tr_b16 v[234:235], v192 offset:33792
	ds_read_b64_tr_b16 v[236:237], v192 offset:37888
	s_waitcnt lgkmcnt(6)
	v_mfma_f32_16x16x32_bf16 v[18:21], v[222:225], v[130:133], v[18:21]
	v_exp_f32_e32 v70, v70
	v_mfma_f32_16x16x32_bf16 v[22:25], v[222:225], v[138:141], v[22:25]
	v_exp_f32_e32 v71, v71
	ds_read_b64_tr_b16 v[238:239], v191 offset:34304
	ds_read_b64_tr_b16 v[240:241], v191 offset:38400
	s_waitcnt lgkmcnt(6)
	v_mfma_f32_16x16x32_bf16 v[26:29], v[226:229], v[130:133], v[26:29]
	v_exp_f32_e32 v72, v72
	v_mfma_f32_16x16x32_bf16 v[30:33], v[226:229], v[138:141], v[30:33]
	v_exp_f32_e32 v73, v73
	v_mfma_f32_16x16x32_bf16 v[246:249], v[194:197], v[130:133], v[246:249]
	ds_read_b64_tr_b16 v[242:243], v192 offset:34304
	ds_read_b64_tr_b16 v[244:245], v192 offset:38400
	s_waitcnt lgkmcnt(6)
	v_mfma_f32_16x16x32_bf16 v[34:37], v[230:233], v[130:133], v[34:37]
	v_exp_f32_e32 v74, v74
	v_mfma_f32_16x16x32_bf16 v[38:41], v[230:233], v[138:141], v[38:41]
	v_exp_f32_e32 v75, v75
	ds_read_b64_tr_b16 v[214:215], v191 offset:40960
	ds_read_b64_tr_b16 v[216:217], v191 offset:45056
	s_waitcnt lgkmcnt(6)
	v_mfma_f32_16x16x32_bf16 v[42:45], v[234:237], v[130:133], v[42:45]
	v_exp_f32_e32 v76, v76
	v_mfma_f32_16x16x32_bf16 v[46:49], v[234:237], v[138:141], v[46:49]
	v_exp_f32_e32 v77, v77
	ds_read_b64_tr_b16 v[218:219], v192 offset:40960
	ds_read_b64_tr_b16 v[220:221], v192 offset:45056
	s_waitcnt lgkmcnt(6)
	v_mfma_f32_16x16x32_bf16 v[50:53], v[238:241], v[130:133], v[50:53]
	v_exp_f32_e32 v78, v78
	v_mfma_f32_16x16x32_bf16 v[54:57], v[238:241], v[138:141], v[54:57]
	v_exp_f32_e32 v79, v79
	ds_read_b64_tr_b16 v[222:223], v191 offset:41472
	ds_read_b64_tr_b16 v[224:225], v191 offset:45568
	s_waitcnt lgkmcnt(6)
	v_mfma_f32_16x16x32_bf16 v[58:61], v[242:245], v[130:133], v[58:61]
	v_exp_f32_e32 v80, v80
	v_mfma_f32_16x16x32_bf16 v[62:65], v[242:245], v[138:141], v[62:65]
	v_exp_f32_e32 v81, v81
	v_mfma_f32_16x16x32_bf16 v[252:255], v[194:197], v[138:141], v[252:255]
	ds_read_b64_tr_b16 v[226:227], v192 offset:41472
	ds_read_b64_tr_b16 v[228:229], v192 offset:45568
	s_waitcnt lgkmcnt(6)
	v_mfma_f32_16x16x32_bf16 v[2:5], v[214:217], v[134:137], v[2:5]
	v_exp_f32_e32 v82, v82
	v_mfma_f32_16x16x32_bf16 v[6:9], v[214:217], v[142:145], v[6:9]
	v_exp_f32_e32 v83, v83
	ds_read_b64_tr_b16 v[230:231], v191 offset:41984
	ds_read_b64_tr_b16 v[232:233], v191 offset:46080
	s_waitcnt lgkmcnt(6)
	v_mfma_f32_16x16x32_bf16 v[10:13], v[218:221], v[134:137], v[10:13]
	v_exp_f32_e32 v84, v84
	v_mfma_f32_16x16x32_bf16 v[14:17], v[218:221], v[142:145], v[14:17]
	v_exp_f32_e32 v85, v85
	ds_read_b64_tr_b16 v[234:235], v192 offset:41984
	ds_read_b64_tr_b16 v[236:237], v192 offset:46080
	s_waitcnt lgkmcnt(6)
	v_mfma_f32_16x16x32_bf16 v[18:21], v[222:225], v[134:137], v[18:21]
	v_exp_f32_e32 v86, v86
	v_mfma_f32_16x16x32_bf16 v[22:25], v[222:225], v[142:145], v[22:25]
	v_exp_f32_e32 v87, v87
	ds_read_b64_tr_b16 v[238:239], v191 offset:42496
	ds_read_b64_tr_b16 v[240:241], v191 offset:46592
	s_waitcnt lgkmcnt(6)
; #define SBAR() __builtin_amdgcn_sched_barrier(0)
; #define RESC(a) do { if (__any((a) < 1.f)) { if (hi == 0) al_l[r32] = (a); asm volatile("s_waitcnt lgkmcnt(0)" ::: "memory"); \
;     for (int d = 0; d < 4; ++d) for (int r = 0; r < 16; ++r) o[d][r] *= al_l[crow(r, hi)]; } } while (0)
; #define ATT_SYNC(jn) do { ATT_WAIT_BAR(); if ((jn) < NT) ATT_DMA((jn), (jn) & 3); } while (0)
; template <int D0> __device__ __forceinline__ void pv_rd(s16x4 (&r)[8], int vb) {
;   r[0] = tr_read<v_rd_off(D0, 0, 0)>(vb); r[1] = tr_read<v_rd_off(D0, 0, 1)>(vb); r[2] = tr_read<v_rd_off(D0, 1, 0)>(vb); r[3] = tr_read<v_rd_off(D0, 1, 1)>(vb);
;   r[4] = tr_read<v_rd_off(D0, 2, 0)>(vb); r[5] = tr_read<v_rd_off(D0, 2, 1)>(vb); r[6] = tr_read<v_rd_off(D0, 3, 0)>(vb); r[7] = tr_read<v_rd_off(D0, 3, 1)>(vb);
; }
; __device__ __forceinline__ void pv_mm(f32x16& od, const s16x4 (&r)[8], bf16x8 pa0, bf16x8 pa1, bf16x8 pa2, bf16x8 pa3) {
;     ...
;   od = __builtin_amdgcn_mfma_f32_32x32x16_bf16(pa0, PK(r[0], r[1]), od, 0, 0, 0);
;   od = __builtin_amdgcn_mfma_f32_32x32x16_bf16(pa1, PK(r[2], r[3]), od, 0, 0, 0);
;   od = __builtin_amdgcn_mfma_f32_32x32x16_bf16(pa2, PK(r[4], r[5]), od, 0, 0, 0);
;   od = __builtin_amdgcn_mfma_f32_32x32x16_bf16(pa3, PK(r[6], r[7]), od, 0, 0, 0);
;     ...
; }
; __device__ __forceinline__ void attn_dma_body(const bf16_t* __restrict__ Qb, int ldq, int tpos0, const float* __restrict__ rope, const float* __restrict__ qgain, ...
;     ...
;   for (int j = 1; j + 1 < NT; j += 2) {
;     { SBAR(); qkt(pB0, pB1, (const bf16_t*)(lds + (j & 3) * SHM_SLOT), qr, r32, hi);
;       finishSM(pA0, pA1, alA, l_reg, pa0, pa1, pa2, pa3); s16x4 va[8]; pv_rd<0>(va, vb0 + ((j - 1) & 3) * (int)SHM_SLOT); SBAR();
;       if (!lead) ATT_SYNC(j + 2);
;       pv_d0_pre(o, vb0 + ((j - 1) & 3) * (int)SHM_SLOT, va, pa0, pa1, pa2, pa3); partialSM(pB0, pB1, m_reg, mnB, alB);
;       if (lead) ATT_SYNC(j + 2);
;       RESC(alB); }
;     { SBAR(); qkt(pA0, pA1, (const bf16_t*)(lds + ((j + 1) & 3) * SHM_SLOT), qr, r32, hi);
;       finishSM(pB0, pB1, alB, l_reg, pa0, pa1, pa2, pa3); s16x4 va[8]; pv_rd<0>(va, vb0 + (j & 3) * (int)SHM_SLOT); SBAR();
;       if (!lead) ATT_SYNC(j + 3);
;       pv_d0_pre(o, vb0 + (j & 3) * (int)SHM_SLOT, va, pa0, pa1, pa2, pa3); partialSM(pA0, pA1, m_reg, mnA, alA);
;       if (lead) ATT_SYNC(j + 3);
;       RESC(alA); }
;   }
	v_mfma_f32_16x16x32_bf16 v[26:29], v[226:229], v[134:137], v[26:29]
	v_exp_f32_e32 v88, v88
	v_mfma_f32_16x16x32_bf16 v[30:33], v[226:229], v[142:145], v[30:33]
	v_exp_f32_e32 v89, v89
	v_mfma_f32_16x16x32_bf16 v[246:249], v[194:197], v[134:137], v[246:249]
	ds_read_b64_tr_b16 v[242:243], v192 offset:42496
	ds_read_b64_tr_b16 v[244:245], v192 offset:46592
	s_waitcnt lgkmcnt(6)
	v_mfma_f32_16x16x32_bf16 v[34:37], v[230:233], v[134:137], v[34:37]
	v_exp_f32_e32 v90, v90
	v_mfma_f32_16x16x32_bf16 v[38:41], v[230:233], v[142:145], v[38:41]
	v_exp_f32_e32 v91, v91
	s_waitcnt lgkmcnt(4)
	v_mfma_f32_16x16x32_bf16 v[42:45], v[234:237], v[134:137], v[42:45]
	v_exp_f32_e32 v92, v92
	v_mfma_f32_16x16x32_bf16 v[46:49], v[234:237], v[142:145], v[46:49]
	v_exp_f32_e32 v93, v93
	s_waitcnt lgkmcnt(2)
	v_mfma_f32_16x16x32_bf16 v[50:53], v[238:241], v[134:137], v[50:53]
	v_exp_f32_e32 v94, v94
	v_mfma_f32_16x16x32_bf16 v[54:57], v[238:241], v[142:145], v[54:57]
	v_exp_f32_e32 v95, v95
	s_waitcnt lgkmcnt(0)
	v_mfma_f32_16x16x32_bf16 v[58:61], v[242:245], v[134:137], v[58:61]
	v_exp_f32_e32 v96, v96
	v_mfma_f32_16x16x32_bf16 v[62:65], v[242:245], v[142:145], v[62:65]
	v_exp_f32_e32 v97, v97
	v_mfma_f32_16x16x32_bf16 v[252:255], v[194:197], v[142:145], v[252:255]
	v_cvt_pk_bf16_f32 v130, v66, v67
	v_cvt_pk_bf16_f32 v131, v68, v69
	v_cvt_pk_bf16_f32 v132, v74, v75
	v_cvt_pk_bf16_f32 v133, v76, v77
	v_cvt_pk_bf16_f32 v134, v82, v83
	v_cvt_pk_bf16_f32 v135, v84, v85
	v_cvt_pk_bf16_f32 v136, v90, v91
	v_cvt_pk_bf16_f32 v137, v92, v93
	v_cvt_pk_bf16_f32 v138, v70, v71
	v_cvt_pk_bf16_f32 v139, v72, v73
	v_cvt_pk_bf16_f32 v140, v78, v79
	v_cvt_pk_bf16_f32 v141, v80, v81
	v_cvt_pk_bf16_f32 v142, v86, v87
	v_cvt_pk_bf16_f32 v143, v88, v89
	v_cvt_pk_bf16_f32 v144, v94, v95
	v_cvt_pk_bf16_f32 v145, v96, v97
	s_add_i32 s97, s97, 1
	s_cmp_lt_u32 s97, 132
	s_cbranch_scc0 .Lf16_done
	ds_read_b128 v[146:149], v187 offset:32768
	ds_read_b128 v[150:153], v187 offset:36864
	ds_read_b128 v[154:157], v187 offset:40960
	ds_read_b128 v[158:161], v187 offset:45056
	ds_read_b128 v[198:201], v188 offset:32768
	ds_read_b128 v[202:205], v188 offset:36864
	ds_read_b128 v[206:209], v188 offset:40960
	ds_read_b128 v[210:213], v188 offset:45056
	s_waitcnt lgkmcnt(7)
	v_mfma_f32_16x16x32_bf16 v[66:69], v[146:149], v[98:101], 0
	v_mfma_f32_16x16x32_bf16 v[70:73], v[146:149], v[114:117], 0
	ds_read_b128 v[146:149], v189 offset:32768
	s_waitcnt lgkmcnt(7)
	v_mfma_f32_16x16x32_bf16 v[74:77], v[150:153], v[98:101], 0
	v_mfma_f32_16x16x32_bf16 v[78:81], v[150:153], v[114:117], 0
	ds_read_b128 v[150:153], v189 offset:36864
	s_waitcnt lgkmcnt(7)
	v_mfma_f32_16x16x32_bf16 v[82:85], v[154:157], v[98:101], 0
	v_mfma_f32_16x16x32_bf16 v[86:89], v[154:157], v[114:117], 0
	ds_read_b128 v[154:157], v189 offset:40960
	s_waitcnt lgkmcnt(7)
	v_mfma_f32_16x16x32_bf16 v[90:93], v[158:161], v[98:101], 0
	v_mfma_f32_16x16x32_bf16 v[94:97], v[158:161], v[114:117], 0
	ds_read_b128 v[158:161], v189 offset:45056
	s_waitcnt lgkmcnt(7)
	v_mfma_f32_16x16x32_bf16 v[66:69], v[198:201], v[102:105], v[66:69]
	v_mfma_f32_16x16x32_bf16 v[70:73], v[198:201], v[118:121], v[70:73]
	ds_read_b128 v[198:201], v190 offset:32768
	s_waitcnt lgkmcnt(7)
	v_mfma_f32_16x16x32_bf16 v[74:77], v[202:205], v[102:105], v[74:77]
	v_mfma_f32_16x16x32_bf16 v[78:81], v[202:205], v[118:121], v[78:81]
	ds_read_b128 v[202:205], v190 offset:36864
	s_waitcnt lgkmcnt(7)
	v_mfma_f32_16x16x32_bf16 v[82:85], v[206:209], v[102:105], v[82:85]
	v_mfma_f32_16x16x32_bf16 v[86:89], v[206:209], v[118:121], v[86:89]
	ds_read_b128 v[206:209], v190 offset:40960
	s_waitcnt lgkmcnt(7)
	v_mfma_f32_16x16x32_bf16 v[90:93], v[210:213], v[102:105], v[90:93]
	v_mfma_f32_16x16x32_bf16 v[94:97], v[210:213], v[118:121], v[94:97]
	ds_read_b128 v[210:213], v190 offset:45056
	s_waitcnt lgkmcnt(7)
	v_mfma_f32_16x16x32_bf16 v[66:69], v[146:149], v[106:109], v[66:69]
	v_mfma_f32_16x16x32_bf16 v[70:73], v[146:149], v[122:125], v[70:73]
	s_waitcnt lgkmcnt(6)
	v_mfma_f32_16x16x32_bf16 v[74:77], v[150:153], v[106:109], v[74:77]
	v_mfma_f32_16x16x32_bf16 v[78:81], v[150:153], v[122:125], v[78:81]
	s_waitcnt lgkmcnt(5)
	v_mfma_f32_16x16x32_bf16 v[82:85], v[154:157], v[106:109], v[82:85]
	v_mfma_f32_16x16x32_bf16 v[86:89], v[154:157], v[122:125], v[86:89]
	s_waitcnt lgkmcnt(4)
	v_mfma_f32_16x16x32_bf16 v[90:93], v[158:161], v[106:109], v[90:93]
	v_mfma_f32_16x16x32_bf16 v[94:97], v[158:161], v[122:125], v[94:97]
	s_waitcnt lgkmcnt(3)
	v_mfma_f32_16x16x32_bf16 v[66:69], v[198:201], v[110:113], v[66:69]
	v_mfma_f32_16x16x32_bf16 v[70:73], v[198:201], v[126:129], v[70:73]
	ds_read_b64_tr_b16 v[214:215], v180 offset:0
	ds_read_b64_tr_b16 v[216:217], v180 offset:4096
	ds_read_b64_tr_b16 v[218:219], v181 offset:0
	ds_read_b64_tr_b16 v[220:221], v181 offset:4096
	ds_read_b64_tr_b16 v[222:223], v180 offset:512
	ds_read_b64_tr_b16 v[224:225], v180 offset:4608
	ds_read_b64_tr_b16 v[226:227], v181 offset:512
	ds_read_b64_tr_b16 v[228:229], v181 offset:4608
	s_waitcnt lgkmcnt(10)
	v_mfma_f32_16x16x32_bf16 v[74:77], v[202:205], v[110:113], v[74:77]
	v_mfma_f32_16x16x32_bf16 v[78:81], v[202:205], v[126:129], v[78:81]
	s_waitcnt lgkmcnt(9)
	v_mfma_f32_16x16x32_bf16 v[82:85], v[206:209], v[110:113], v[82:85]
	v_mfma_f32_16x16x32_bf16 v[86:89], v[206:209], v[126:129], v[86:89]
	s_waitcnt lgkmcnt(8)
	v_mfma_f32_16x16x32_bf16 v[90:93], v[210:213], v[110:113], v[90:93]
	v_mfma_f32_16x16x32_bf16 v[94:97], v[210:213], v[126:129], v[94:97]
	s_cmp_ge_u32 s97, 131
	s_cbranch_scc1 .Lf16_se_N2
	s_waitcnt vmcnt(0) lgkmcnt(0)
	s_barrier
	s_cmp_ge_u32 s97, 130
	s_cbranch_scc1 .Lf16_se_N2
	s_add_i32 s6, s96, 0x8000
	s_mov_b32 m0, s6
	s_nop 0
	global_load_lds_dwordx4 v170, s[2:3]
	s_add_i32 m0, s6, 0x2000
	s_nop 0
	global_load_lds_dwordx4 v172, s[2:3]
	s_add_i32 m0, s6, 0x4000
	s_nop 0
	global_load_lds_dwordx4 v171, s[4:5]
	s_add_i32 m0, s6, 0x6000
	s_nop 0
	global_load_lds_dwordx4 v173, s[4:5]
	s_add_u32 s2, s2, 0x4000
	s_addc_u32 s3, s3, 0
	s_add_u32 s4, s4, 0x4000
	s_addc_u32 s5, s5, 0
; __device__ __forceinline__ void finishSM(f32x16& p0, f32x16& p1, float alpha, float& l_reg, bf16x8& pa0, bf16x8& pa1, bf16x8& pa2, bf16x8& pa3) {
;   for (int r = 0; r < 16; ++r) p1[r] = __builtin_amdgcn_exp2f(p1[r]);
;   float ps = 0; for (int r = 0; r < 16; ++r) ps += p0[r]; for (int r = 0; r < 16; ++r) ps += p1[r];
;   { auto rr = __builtin_amdgcn_permlane32_swap(__float_as_uint(ps), __float_as_uint(ps), false, false);
;     ps = __uint_as_float(rr[0]) + __uint_as_float(rr[1]); }
;   l_reg = l_reg * alpha + ps;
;     ...
;   PK4(p0, 0, pa0); PK4(p0, 8, pa1); PK4(p1, 0, pa2); PK4(p1, 8, pa3);
; template <int D0> __device__ __forceinline__ void pv_rd(s16x4 (&r)[8], int vb) {
;   r[0] = tr_read<v_rd_off(D0, 0, 0)>(vb); r[1] = tr_read<v_rd_off(D0, 0, 1)>(vb); r[2] = tr_read<v_rd_off(D0, 1, 0)>(vb); r[3] = tr_read<v_rd_off(D0, 1, 1)>(vb);
;   r[4] = tr_read<v_rd_off(D0, 2, 0)>(vb); r[5] = tr_read<v_rd_off(D0, 2, 1)>(vb); r[6] = tr_read<v_rd_off(D0, 3, 0)>(vb); r[7] = tr_read<v_rd_off(D0, 3, 1)>(vb);
; }
; __device__ __forceinline__ void pv_mm(f32x16& od, const s16x4 (&r)[8], bf16x8 pa0, bf16x8 pa1, bf16x8 pa2, bf16x8 pa3) {
;     ...
;   od = __builtin_amdgcn_mfma_f32_32x32x16_bf16(pa0, PK(r[0], r[1]), od, 0, 0, 0);
;   od = __builtin_amdgcn_mfma_f32_32x32x16_bf16(pa1, PK(r[2], r[3]), od, 0, 0, 0);
; __device__ __forceinline__ void attn_dma_body(const bf16_t* __restrict__ Qb, int ldq, int tpos0, const float* __restrict__ rope, const float* __restrict__ qgain, ...
;     ...
;   for (int j = 1; j + 1 < NT; j += 2) {
;     { SBAR(); qkt(pB0, pB1, (const bf16_t*)(lds + (j & 3) * SHM_SLOT), qr, r32, hi);
;       finishSM(pA0, pA1, alA, l_reg, pa0, pa1, pa2, pa3); s16x4 va[8]; pv_rd<0>(va, vb0 + ((j - 1) & 3) * (int)SHM_SLOT); SBAR();
;       if (!lead) ATT_SYNC(j + 2);
;       pv_d0_pre(o, vb0 + ((j - 1) & 3) * (int)SHM_SLOT, va, pa0, pa1, pa2, pa3); partialSM(pB0, pB1, m_reg, mnB, alB);
;       if (lead) ATT_SYNC(j + 2);
;       RESC(alB); }
;     { SBAR(); qkt(pA0, pA1, (const bf16_t*)(lds + ((j + 1) & 3) * SHM_SLOT), qr, r32, hi);
;       finishSM(pB0, pB1, alB, l_reg, pa0, pa1, pa2, pa3); s16x4 va[8]; pv_rd<0>(va, vb0 + (j & 3) * (int)SHM_SLOT); SBAR();
;       if (!lead) ATT_SYNC(j + 3);
;       pv_d0_pre(o, vb0 + (j & 3) * (int)SHM_SLOT, va, pa0, pa1, pa2, pa3); partialSM(pA0, pA1, m_reg, mnA, alA);
;       if (lead) ATT_SYNC(j + 3);
;       RESC(alA); }
;   }
.Lf16_se_N2:
	s_waitcnt lgkmcnt(6)
	v_mfma_f32_16x16x32_bf16 v[2:5], v[214:217], v[130:133], v[2:5]
	v_exp_f32_e32 v66, v66
	v_mfma_f32_16x16x32_bf16 v[6:9], v[214:217], v[138:141], v[6:9]
	v_exp_f32_e32 v67, v67
	ds_read_b64_tr_b16 v[230:231], v180 offset:1024
	ds_read_b64_tr_b16 v[232:233], v180 offset:5120
	s_waitcnt lgkmcnt(6)
	v_mfma_f32_16x16x32_bf16 v[10:13], v[218:221], v[130:133], v[10:13]
	v_exp_f32_e32 v68, v68
	v_mfma_f32_16x16x32_bf16 v[14:17], v[218:221], v[138:141], v[14:17]
	v_exp_f32_e32 v69, v69
	ds_read_b64_tr_b16 v[234:235], v181 offset:1024
	ds_read_b64_tr_b16 v[236:237], v181 offset:5120
	s_waitcnt lgkmcnt(6)
	v_mfma_f32_16x16x32_bf16 v[18:21], v[222:225], v[130:133], v[18:21]
	v_exp_f32_e32 v70, v70
	v_mfma_f32_16x16x32_bf16 v[22:25], v[222:225], v[138:141], v[22:25]
	v_exp_f32_e32 v71, v71
	ds_read_b64_tr_b16 v[238:239], v180 offset:1536
	ds_read_b64_tr_b16 v[240:241], v180 offset:5632
	s_waitcnt lgkmcnt(6)
	v_mfma_f32_16x16x32_bf16 v[26:29], v[226:229], v[130:133], v[26:29]
	v_exp_f32_e32 v72, v72
	v_mfma_f32_16x16x32_bf16 v[30:33], v[226:229], v[138:141], v[30:33]
	v_exp_f32_e32 v73, v73
	v_mfma_f32_16x16x32_bf16 v[246:249], v[194:197], v[130:133], v[246:249]
	ds_read_b64_tr_b16 v[242:243], v181 offset:1536
	ds_read_b64_tr_b16 v[244:245], v181 offset:5632
	s_waitcnt lgkmcnt(6)
	v_mfma_f32_16x16x32_bf16 v[34:37], v[230:233], v[130:133], v[34:37]
	v_exp_f32_e32 v74, v74
	v_mfma_f32_16x16x32_bf16 v[38:41], v[230:233], v[138:141], v[38:41]
	v_exp_f32_e32 v75, v75
	ds_read_b64_tr_b16 v[214:215], v180 offset:8192
	ds_read_b64_tr_b16 v[216:217], v180 offset:12288
	s_waitcnt lgkmcnt(6)
	v_mfma_f32_16x16x32_bf16 v[42:45], v[234:237], v[130:133], v[42:45]
	v_exp_f32_e32 v76, v76
	v_mfma_f32_16x16x32_bf16 v[46:49], v[234:237], v[138:141], v[46:49]
	v_exp_f32_e32 v77, v77
	ds_read_b64_tr_b16 v[218:219], v181 offset:8192
	ds_read_b64_tr_b16 v[220:221], v181 offset:12288
	s_waitcnt lgkmcnt(6)
	v_mfma_f32_16x16x32_bf16 v[50:53], v[238:241], v[130:133], v[50:53]
	v_exp_f32_e32 v78, v78
	v_mfma_f32_16x16x32_bf16 v[54:57], v[238:241], v[138:141], v[54:57]
	v_exp_f32_e32 v79, v79
	ds_read_b64_tr_b16 v[222:223], v180 offset:8704
	ds_read_b64_tr_b16 v[224:225], v180 offset:12800
	s_waitcnt lgkmcnt(6)
	v_mfma_f32_16x16x32_bf16 v[58:61], v[242:245], v[130:133], v[58:61]
	v_exp_f32_e32 v80, v80
	v_mfma_f32_16x16x32_bf16 v[62:65], v[242:245], v[138:141], v[62:65]
	v_exp_f32_e32 v81, v81
	v_mfma_f32_16x16x32_bf16 v[252:255], v[194:197], v[138:141], v[252:255]
	ds_read_b64_tr_b16 v[226:227], v181 offset:8704
	ds_read_b64_tr_b16 v[228:229], v181 offset:12800
	s_waitcnt lgkmcnt(6)
	v_mfma_f32_16x16x32_bf16 v[2:5], v[214:217], v[134:137], v[2:5]
	v_exp_f32_e32 v82, v82
	v_mfma_f32_16x16x32_bf16 v[6:9], v[214:217], v[142:145], v[6:9]
	v_exp_f32_e32 v83, v83
	ds_read_b64_tr_b16 v[230:231], v180 offset:9216
	ds_read_b64_tr_b16 v[232:233], v180 offset:13312
	s_waitcnt lgkmcnt(6)
	v_mfma_f32_16x16x32_bf16 v[10:13], v[218:221], v[134:137], v[10:13]
	v_exp_f32_e32 v84, v84
	v_mfma_f32_16x16x32_bf16 v[14:17], v[218:221], v[142:145], v[14:17]
	v_exp_f32_e32 v85, v85
	ds_read_b64_tr_b16 v[234:235], v181 offset:9216
	ds_read_b64_tr_b16 v[236:237], v181 offset:13312
	s_waitcnt lgkmcnt(6)
	v_mfma_f32_16x16x32_bf16 v[18:21], v[222:225], v[134:137], v[18:21]
	v_exp_f32_e32 v86, v86
	v_mfma_f32_16x16x32_bf16 v[22:25], v[222:225], v[142:145], v[22:25]
	v_exp_f32_e32 v87, v87
	ds_read_b64_tr_b16 v[238:239], v180 offset:9728
	ds_read_b64_tr_b16 v[240:241], v180 offset:13824
	s_waitcnt lgkmcnt(6)
	v_mfma_f32_16x16x32_bf16 v[26:29], v[226:229], v[134:137], v[26:29]
	v_exp_f32_e32 v88, v88
	v_mfma_f32_16x16x32_bf16 v[30:33], v[226:229], v[142:145], v[30:33]
	v_exp_f32_e32 v89, v89
	v_mfma_f32_16x16x32_bf16 v[246:249], v[194:197], v[134:137], v[246:249]
	ds_read_b64_tr_b16 v[242:243], v181 offset:9728
	ds_read_b64_tr_b16 v[244:245], v181 offset:13824
	s_waitcnt lgkmcnt(6)
	v_mfma_f32_16x16x32_bf16 v[34:37], v[230:233], v[134:137], v[34:37]
	v_exp_f32_e32 v90, v90
	v_mfma_f32_16x16x32_bf16 v[38:41], v[230:233], v[142:145], v[38:41]
	v_exp_f32_e32 v91, v91
	s_waitcnt lgkmcnt(4)
	v_mfma_f32_16x16x32_bf16 v[42:45], v[234:237], v[134:137], v[42:45]
	v_exp_f32_e32 v92, v92
	v_mfma_f32_16x16x32_bf16 v[46:49], v[234:237], v[142:145], v[46:49]
	v_exp_f32_e32 v93, v93
	s_waitcnt lgkmcnt(2)
	v_mfma_f32_16x16x32_bf16 v[50:53], v[238:241], v[134:137], v[50:53]
	v_exp_f32_e32 v94, v94
	v_mfma_f32_16x16x32_bf16 v[54:57], v[238:241], v[142:145], v[54:57]
	v_exp_f32_e32 v95, v95
	s_waitcnt lgkmcnt(0)
	v_mfma_f32_16x16x32_bf16 v[58:61], v[242:245], v[134:137], v[58:61]
	v_exp_f32_e32 v96, v96
	v_mfma_f32_16x16x32_bf16 v[62:65], v[242:245], v[142:145], v[62:65]
	v_exp_f32_e32 v97, v97
	v_mfma_f32_16x16x32_bf16 v[252:255], v[194:197], v[142:145], v[252:255]
	v_cvt_pk_bf16_f32 v130, v66, v67
	v_cvt_pk_bf16_f32 v131, v68, v69
	v_cvt_pk_bf16_f32 v132, v74, v75
	v_cvt_pk_bf16_f32 v133, v76, v77
	v_cvt_pk_bf16_f32 v134, v82, v83
	v_cvt_pk_bf16_f32 v135, v84, v85
	v_cvt_pk_bf16_f32 v136, v90, v91
	v_cvt_pk_bf16_f32 v137, v92, v93
	v_cvt_pk_bf16_f32 v138, v70, v71
	v_cvt_pk_bf16_f32 v139, v72, v73
	v_cvt_pk_bf16_f32 v140, v78, v79
	v_cvt_pk_bf16_f32 v141, v80, v81
	v_cvt_pk_bf16_f32 v142, v86, v87
	v_cvt_pk_bf16_f32 v143, v88, v89
	v_cvt_pk_bf16_f32 v144, v94, v95
	v_cvt_pk_bf16_f32 v145, v96, v97
	s_add_i32 s97, s97, 1
	s_cmp_lt_u32 s97, 132
	s_cbranch_scc0 .Lf16_done
; #define SBAR() __builtin_amdgcn_sched_barrier(0)
; #define RESC(a) do { if (__any((a) < 1.f)) { if (hi == 0) al_l[r32] = (a); asm volatile("s_waitcnt lgkmcnt(0)" ::: "memory"); \
;     for (int d = 0; d < 4; ++d) for (int r = 0; r < 16; ++r) o[d][r] *= al_l[crow(r, hi)]; } } while (0)
; #define ATT_SYNC(jn) do { ATT_WAIT_BAR(); if ((jn) < NT) ATT_DMA((jn), (jn) & 3); } while (0)
; template <int D0> __device__ __forceinline__ void pv_rd(s16x4 (&r)[8], int vb) {
;   r[0] = tr_read<v_rd_off(D0, 0, 0)>(vb); r[1] = tr_read<v_rd_off(D0, 0, 1)>(vb); r[2] = tr_read<v_rd_off(D0, 1, 0)>(vb); r[3] = tr_read<v_rd_off(D0, 1, 1)>(vb);
;   r[4] = tr_read<v_rd_off(D0, 2, 0)>(vb); r[5] = tr_read<v_rd_off(D0, 2, 1)>(vb); r[6] = tr_read<v_rd_off(D0, 3, 0)>(vb); r[7] = tr_read<v_rd_off(D0, 3, 1)>(vb);
; }
; __device__ __forceinline__ void pv_mm(f32x16& od, const s16x4 (&r)[8], bf16x8 pa0, bf16x8 pa1, bf16x8 pa2, bf16x8 pa3) {
;     ...
;   od = __builtin_amdgcn_mfma_f32_32x32x16_bf16(pa0, PK(r[0], r[1]), od, 0, 0, 0);
;   od = __builtin_amdgcn_mfma_f32_32x32x16_bf16(pa1, PK(r[2], r[3]), od, 0, 0, 0);
;   od = __builtin_amdgcn_mfma_f32_32x32x16_bf16(pa2, PK(r[4], r[5]), od, 0, 0, 0);
;   od = __builtin_amdgcn_mfma_f32_32x32x16_bf16(pa3, PK(r[6], r[7]), od, 0, 0, 0);
;     ...
; }
; __device__ __forceinline__ void attn_dma_body(const bf16_t* __restrict__ Qb, int ldq, int tpos0, const float* __restrict__ rope, const float* __restrict__ qgain, ...
;     ...
;   for (int j = 1; j + 1 < NT; j += 2) {
;     { SBAR(); qkt(pB0, pB1, (const bf16_t*)(lds + (j & 3) * SHM_SLOT), qr, r32, hi);
;       finishSM(pA0, pA1, alA, l_reg, pa0, pa1, pa2, pa3); s16x4 va[8]; pv_rd<0>(va, vb0 + ((j - 1) & 3) * (int)SHM_SLOT); SBAR();
;       if (!lead) ATT_SYNC(j + 2);
;       pv_d0_pre(o, vb0 + ((j - 1) & 3) * (int)SHM_SLOT, va, pa0, pa1, pa2, pa3); partialSM(pB0, pB1, m_reg, mnB, alB);
;       if (lead) ATT_SYNC(j + 2);
;       RESC(alB); }
;     { SBAR(); qkt(pA0, pA1, (const bf16_t*)(lds + ((j + 1) & 3) * SHM_SLOT), qr, r32, hi);
;       finishSM(pB0, pB1, alB, l_reg, pa0, pa1, pa2, pa3); s16x4 va[8]; pv_rd<0>(va, vb0 + (j & 3) * (int)SHM_SLOT); SBAR();
;       if (!lead) ATT_SYNC(j + 3);
;       pv_d0_pre(o, vb0 + (j & 3) * (int)SHM_SLOT, va, pa0, pa1, pa2, pa3); partialSM(pA0, pA1, m_reg, mnA, alA);
;       if (lead) ATT_SYNC(j + 3);
;       RESC(alA); }
;   }
	ds_read_b128 v[146:149], v183 offset:0
	ds_read_b128 v[150:153], v183 offset:4096
	ds_read_b128 v[154:157], v183 offset:8192
	ds_read_b128 v[158:161], v183 offset:12288
	ds_read_b128 v[198:201], v184 offset:0
	ds_read_b128 v[202:205], v184 offset:4096
	ds_read_b128 v[206:209], v184 offset:8192
	ds_read_b128 v[210:213], v184 offset:12288
	s_waitcnt lgkmcnt(7)
	v_mfma_f32_16x16x32_bf16 v[66:69], v[146:149], v[98:101], 0
	v_mfma_f32_16x16x32_bf16 v[70:73], v[146:149], v[114:117], 0
	ds_read_b128 v[146:149], v185 offset:0
	s_waitcnt lgkmcnt(7)
	v_mfma_f32_16x16x32_bf16 v[74:77], v[150:153], v[98:101], 0
	v_mfma_f32_16x16x32_bf16 v[78:81], v[150:153], v[114:117], 0
	ds_read_b128 v[150:153], v185 offset:4096
	s_waitcnt lgkmcnt(7)
	v_mfma_f32_16x16x32_bf16 v[82:85], v[154:157], v[98:101], 0
	v_mfma_f32_16x16x32_bf16 v[86:89], v[154:157], v[114:117], 0
	ds_read_b128 v[154:157], v185 offset:8192
	s_waitcnt lgkmcnt(7)
	v_mfma_f32_16x16x32_bf16 v[90:93], v[158:161], v[98:101], 0
	v_mfma_f32_16x16x32_bf16 v[94:97], v[158:161], v[114:117], 0
	ds_read_b128 v[158:161], v185 offset:12288
	s_waitcnt lgkmcnt(7)
	v_mfma_f32_16x16x32_bf16 v[66:69], v[198:201], v[102:105], v[66:69]
	v_mfma_f32_16x16x32_bf16 v[70:73], v[198:201], v[118:121], v[70:73]
	ds_read_b128 v[198:201], v186 offset:0
	s_waitcnt lgkmcnt(7)
	v_mfma_f32_16x16x32_bf16 v[74:77], v[202:205], v[102:105], v[74:77]
	v_mfma_f32_16x16x32_bf16 v[78:81], v[202:205], v[118:121], v[78:81]
	ds_read_b128 v[202:205], v186 offset:4096
	s_waitcnt lgkmcnt(7)
	v_mfma_f32_16x16x32_bf16 v[82:85], v[206:209], v[102:105], v[82:85]
	v_mfma_f32_16x16x32_bf16 v[86:89], v[206:209], v[118:121], v[86:89]
	ds_read_b128 v[206:209], v186 offset:8192
	s_waitcnt lgkmcnt(7)
	v_mfma_f32_16x16x32_bf16 v[90:93], v[210:213], v[102:105], v[90:93]
	v_mfma_f32_16x16x32_bf16 v[94:97], v[210:213], v[118:121], v[94:97]
	ds_read_b128 v[210:213], v186 offset:12288
	s_waitcnt lgkmcnt(7)
	v_mfma_f32_16x16x32_bf16 v[66:69], v[146:149], v[106:109], v[66:69]
	v_mfma_f32_16x16x32_bf16 v[70:73], v[146:149], v[122:125], v[70:73]
	s_waitcnt lgkmcnt(6)
	v_mfma_f32_16x16x32_bf16 v[74:77], v[150:153], v[106:109], v[74:77]
	v_mfma_f32_16x16x32_bf16 v[78:81], v[150:153], v[122:125], v[78:81]
	s_waitcnt lgkmcnt(5)
	v_mfma_f32_16x16x32_bf16 v[82:85], v[154:157], v[106:109], v[82:85]
	v_mfma_f32_16x16x32_bf16 v[86:89], v[154:157], v[122:125], v[86:89]
	s_waitcnt lgkmcnt(4)
	v_mfma_f32_16x16x32_bf16 v[90:93], v[158:161], v[106:109], v[90:93]
	v_mfma_f32_16x16x32_bf16 v[94:97], v[158:161], v[122:125], v[94:97]
	s_waitcnt lgkmcnt(3)
	v_mfma_f32_16x16x32_bf16 v[66:69], v[198:201], v[110:113], v[66:69]
	v_mfma_f32_16x16x32_bf16 v[70:73], v[198:201], v[126:129], v[70:73]
	ds_read_b64_tr_b16 v[214:215], v180 offset:32768
	ds_read_b64_tr_b16 v[216:217], v180 offset:36864
	ds_read_b64_tr_b16 v[218:219], v181 offset:32768
	ds_read_b64_tr_b16 v[220:221], v181 offset:36864
	ds_read_b64_tr_b16 v[222:223], v180 offset:33280
	ds_read_b64_tr_b16 v[224:225], v180 offset:37376
	ds_read_b64_tr_b16 v[226:227], v181 offset:33280
	ds_read_b64_tr_b16 v[228:229], v181 offset:37376
	s_waitcnt lgkmcnt(10)
	v_mfma_f32_16x16x32_bf16 v[74:77], v[202:205], v[110:113], v[74:77]
	v_mfma_f32_16x16x32_bf16 v[78:81], v[202:205], v[126:129], v[78:81]
	s_waitcnt lgkmcnt(9)
	v_mfma_f32_16x16x32_bf16 v[82:85], v[206:209], v[110:113], v[82:85]
	v_mfma_f32_16x16x32_bf16 v[86:89], v[206:209], v[126:129], v[86:89]
	s_waitcnt lgkmcnt(8)
	v_mfma_f32_16x16x32_bf16 v[90:93], v[210:213], v[110:113], v[90:93]
	v_mfma_f32_16x16x32_bf16 v[94:97], v[210:213], v[126:129], v[94:97]
	s_cmp_ge_u32 s97, 131
	s_cbranch_scc1 .Lf16_se_N3
	s_waitcnt vmcnt(0) lgkmcnt(0)
	s_barrier
	s_cmp_ge_u32 s97, 130
	s_cbranch_scc1 .Lf16_se_N3
	s_add_i32 s6, s96, 0x10000
	s_mov_b32 m0, s6
	s_nop 0
	global_load_lds_dwordx4 v170, s[2:3]
	s_add_i32 m0, s6, 0x2000
	s_nop 0
	global_load_lds_dwordx4 v172, s[2:3]
	s_add_i32 m0, s6, 0x4000
	s_nop 0
	global_load_lds_dwordx4 v171, s[4:5]
	s_add_i32 m0, s6, 0x6000
	s_nop 0
	global_load_lds_dwordx4 v173, s[4:5]
	s_add_u32 s2, s2, 0x4000
	s_addc_u32 s3, s3, 0
	s_add_u32 s4, s4, 0x4000
	s_addc_u32 s5, s5, 0
.Lf16_se_N3:
	s_waitcnt lgkmcnt(6)
	v_mfma_f32_16x16x32_bf16 v[2:5], v[214:217], v[130:133], v[2:5]
	v_exp_f32_e32 v66, v66
	v_mfma_f32_16x16x32_bf16 v[6:9], v[214:217], v[138:141], v[6:9]
	v_exp_f32_e32 v67, v67
	ds_read_b64_tr_b16 v[230:231], v180 offset:33792
	ds_read_b64_tr_b16 v[232:233], v180 offset:37888
	s_waitcnt lgkmcnt(6)
	v_mfma_f32_16x16x32_bf16 v[10:13], v[218:221], v[130:133], v[10:13]
	v_exp_f32_e32 v68, v68
	v_mfma_f32_16x16x32_bf16 v[14:17], v[218:221], v[138:141], v[14:17]
	v_exp_f32_e32 v69, v69
	ds_read_b64_tr_b16 v[234:235], v181 offset:33792
	ds_read_b64_tr_b16 v[236:237], v181 offset:37888
	s_waitcnt lgkmcnt(6)
	v_mfma_f32_16x16x32_bf16 v[18:21], v[222:225], v[130:133], v[18:21]
	v_exp_f32_e32 v70, v70
	v_mfma_f32_16x16x32_bf16 v[22:25], v[222:225], v[138:141], v[22:25]
	v_exp_f32_e32 v71, v71
	ds_read_b64_tr_b16 v[238:239], v180 offset:34304
	ds_read_b64_tr_b16 v[240:241], v180 offset:38400
	s_waitcnt lgkmcnt(6)
	v_mfma_f32_16x16x32_bf16 v[26:29], v[226:229], v[130:133], v[26:29]
	v_exp_f32_e32 v72, v72
	v_mfma_f32_16x16x32_bf16 v[30:33], v[226:229], v[138:141], v[30:33]
	v_exp_f32_e32 v73, v73
	v_mfma_f32_16x16x32_bf16 v[246:249], v[194:197], v[130:133], v[246:249]
	ds_read_b64_tr_b16 v[242:243], v181 offset:34304
	ds_read_b64_tr_b16 v[244:245], v181 offset:38400
	s_waitcnt lgkmcnt(6)
	v_mfma_f32_16x16x32_bf16 v[34:37], v[230:233], v[130:133], v[34:37]
	v_exp_f32_e32 v74, v74
	v_mfma_f32_16x16x32_bf16 v[38:41], v[230:233], v[138:141], v[38:41]
	v_exp_f32_e32 v75, v75
	ds_read_b64_tr_b16 v[214:215], v180 offset:40960
	ds_read_b64_tr_b16 v[216:217], v180 offset:45056
	s_waitcnt lgkmcnt(6)
; #define SBAR() __builtin_amdgcn_sched_barrier(0)
; #define RESC(a) do { if (__any((a) < 1.f)) { if (hi == 0) al_l[r32] = (a); asm volatile("s_waitcnt lgkmcnt(0)" ::: "memory"); \
;     for (int d = 0; d < 4; ++d) for (int r = 0; r < 16; ++r) o[d][r] *= al_l[crow(r, hi)]; } } while (0)
; #define RESC(a) do { if (__any((a) < 1.f)) { if (hi == 0) al_l[r32] = (a); asm volatile("s_waitcnt lgkmcnt(0)" ::: "memory"); \
;     for (int d = 0; d < 4; ++d) for (int r = 0; r < 16; ++r) o[d][r] *= al_l[crow(r, hi)]; } } while (0)
; #define ATT_SYNC(jn) do { ATT_WAIT_BAR(); if ((jn) < NT) ATT_DMA((jn), (jn) & 3); } while (0)
; __device__ __forceinline__ void attn_dma_body(const bf16_t* __restrict__ Qb, int ldq, int tpos0, const float* __restrict__ rope, const float* __restrict__ qgain, ...
;     ...
;   for (int j = 1; j + 1 < NT; j += 2) {
;     { SBAR(); qkt(pB0, pB1, (const bf16_t*)(lds + (j & 3) * SHM_SLOT), qr, r32, hi);
;       finishSM(pA0, pA1, alA, l_reg, pa0, pa1, pa2, pa3); s16x4 va[8]; pv_rd<0>(va, vb0 + ((j - 1) & 3) * (int)SHM_SLOT); SBAR();
;       if (!lead) ATT_SYNC(j + 2);
;       pv_d0_pre(o, vb0 + ((j - 1) & 3) * (int)SHM_SLOT, va, pa0, pa1, pa2, pa3); partialSM(pB0, pB1, m_reg, mnB, alB);
;       if (lead) ATT_SYNC(j + 2);
;       RESC(alB); }
;     { SBAR(); qkt(pA0, pA1, (const bf16_t*)(lds + ((j + 1) & 3) * SHM_SLOT), qr, r32, hi);
;       finishSM(pB0, pB1, alB, l_reg, pa0, pa1, pa2, pa3); s16x4 va[8]; pv_rd<0>(va, vb0 + (j & 3) * (int)SHM_SLOT); SBAR();
;       if (!lead) ATT_SYNC(j + 3);
;       pv_d0_pre(o, vb0 + (j & 3) * (int)SHM_SLOT, va, pa0, pa1, pa2, pa3); partialSM(pA0, pA1, m_reg, mnA, alA);
;       if (lead) ATT_SYNC(j + 3);
;       RESC(alA); }
;   }
	v_mfma_f32_16x16x32_bf16 v[42:45], v[234:237], v[130:133], v[42:45]
	v_exp_f32_e32 v76, v76
	v_mfma_f32_16x16x32_bf16 v[46:49], v[234:237], v[138:141], v[46:49]
	v_exp_f32_e32 v77, v77
	ds_read_b64_tr_b16 v[218:219], v181 offset:40960
	ds_read_b64_tr_b16 v[220:221], v181 offset:45056
	s_waitcnt lgkmcnt(6)
	v_mfma_f32_16x16x32_bf16 v[50:53], v[238:241], v[130:133], v[50:53]
	v_exp_f32_e32 v78, v78
	v_mfma_f32_16x16x32_bf16 v[54:57], v[238:241], v[138:141], v[54:57]
	v_exp_f32_e32 v79, v79
	ds_read_b64_tr_b16 v[222:223], v180 offset:41472
	ds_read_b64_tr_b16 v[224:225], v180 offset:45568
	s_waitcnt lgkmcnt(6)
	v_mfma_f32_16x16x32_bf16 v[58:61], v[242:245], v[130:133], v[58:61]
	v_exp_f32_e32 v80, v80
	v_mfma_f32_16x16x32_bf16 v[62:65], v[242:245], v[138:141], v[62:65]
	v_exp_f32_e32 v81, v81
	v_mfma_f32_16x16x32_bf16 v[252:255], v[194:197], v[138:141], v[252:255]
	ds_read_b64_tr_b16 v[226:227], v181 offset:41472
	ds_read_b64_tr_b16 v[228:229], v181 offset:45568
	s_waitcnt lgkmcnt(6)
	v_mfma_f32_16x16x32_bf16 v[2:5], v[214:217], v[134:137], v[2:5]
	v_exp_f32_e32 v82, v82
	v_mfma_f32_16x16x32_bf16 v[6:9], v[214:217], v[142:145], v[6:9]
	v_exp_f32_e32 v83, v83
	ds_read_b64_tr_b16 v[230:231], v180 offset:41984
	ds_read_b64_tr_b16 v[232:233], v180 offset:46080
	s_waitcnt lgkmcnt(6)
	v_mfma_f32_16x16x32_bf16 v[10:13], v[218:221], v[134:137], v[10:13]
	v_exp_f32_e32 v84, v84
	v_mfma_f32_16x16x32_bf16 v[14:17], v[218:221], v[142:145], v[14:17]
	v_exp_f32_e32 v85, v85
	ds_read_b64_tr_b16 v[234:235], v181 offset:41984
	ds_read_b64_tr_b16 v[236:237], v181 offset:46080
	s_waitcnt lgkmcnt(6)
	v_mfma_f32_16x16x32_bf16 v[18:21], v[222:225], v[134:137], v[18:21]
	v_exp_f32_e32 v86, v86
	v_mfma_f32_16x16x32_bf16 v[22:25], v[222:225], v[142:145], v[22:25]
	v_exp_f32_e32 v87, v87
	ds_read_b64_tr_b16 v[238:239], v180 offset:42496
	ds_read_b64_tr_b16 v[240:241], v180 offset:46592
	s_waitcnt lgkmcnt(6)
	v_mfma_f32_16x16x32_bf16 v[26:29], v[226:229], v[134:137], v[26:29]
	v_exp_f32_e32 v88, v88
	v_mfma_f32_16x16x32_bf16 v[30:33], v[226:229], v[142:145], v[30:33]
	v_exp_f32_e32 v89, v89
	v_mfma_f32_16x16x32_bf16 v[246:249], v[194:197], v[134:137], v[246:249]
	ds_read_b64_tr_b16 v[242:243], v181 offset:42496
	ds_read_b64_tr_b16 v[244:245], v181 offset:46592
	s_waitcnt lgkmcnt(6)
	v_mfma_f32_16x16x32_bf16 v[34:37], v[230:233], v[134:137], v[34:37]
	v_exp_f32_e32 v90, v90
	v_mfma_f32_16x16x32_bf16 v[38:41], v[230:233], v[142:145], v[38:41]
	v_exp_f32_e32 v91, v91
	s_waitcnt lgkmcnt(4)
	v_mfma_f32_16x16x32_bf16 v[42:45], v[234:237], v[134:137], v[42:45]
	v_exp_f32_e32 v92, v92
	v_mfma_f32_16x16x32_bf16 v[46:49], v[234:237], v[142:145], v[46:49]
	v_exp_f32_e32 v93, v93
	s_waitcnt lgkmcnt(2)
	v_mfma_f32_16x16x32_bf16 v[50:53], v[238:241], v[134:137], v[50:53]
	v_exp_f32_e32 v94, v94
	v_mfma_f32_16x16x32_bf16 v[54:57], v[238:241], v[142:145], v[54:57]
	v_exp_f32_e32 v95, v95
	s_waitcnt lgkmcnt(0)
	v_mfma_f32_16x16x32_bf16 v[58:61], v[242:245], v[134:137], v[58:61]
	v_exp_f32_e32 v96, v96
	v_mfma_f32_16x16x32_bf16 v[62:65], v[242:245], v[142:145], v[62:65]
	v_exp_f32_e32 v97, v97
	v_mfma_f32_16x16x32_bf16 v[252:255], v[194:197], v[142:145], v[252:255]
	v_cvt_pk_bf16_f32 v130, v66, v67
	v_cvt_pk_bf16_f32 v131, v68, v69
	v_cvt_pk_bf16_f32 v132, v74, v75
	v_cvt_pk_bf16_f32 v133, v76, v77
	v_cvt_pk_bf16_f32 v134, v82, v83
	v_cvt_pk_bf16_f32 v135, v84, v85
	v_cvt_pk_bf16_f32 v136, v90, v91
	v_cvt_pk_bf16_f32 v137, v92, v93
	v_cvt_pk_bf16_f32 v138, v70, v71
	v_cvt_pk_bf16_f32 v139, v72, v73
	v_cvt_pk_bf16_f32 v140, v78, v79
	v_cvt_pk_bf16_f32 v141, v80, v81
	v_cvt_pk_bf16_f32 v142, v86, v87
	v_cvt_pk_bf16_f32 v143, v88, v89
	v_cvt_pk_bf16_f32 v144, v94, v95
	v_cvt_pk_bf16_f32 v145, v96, v97
	s_add_i32 s97, s97, 1
	s_cmp_lt_u32 s97, 132
	s_cbranch_scc0 .Lf16_done
	s_branch .Lf16_N_loop
	.p2align 6
.Lf16_L_loop:
	ds_read_b128 v[146:149], v183 offset:32768
	ds_read_b128 v[150:153], v183 offset:36864
	ds_read_b128 v[154:157], v183 offset:40960
	ds_read_b128 v[158:161], v183 offset:45056
	ds_read_b128 v[198:201], v184 offset:32768
	ds_read_b128 v[202:205], v184 offset:36864
	ds_read_b128 v[206:209], v184 offset:40960
	ds_read_b128 v[210:213], v184 offset:45056
	s_waitcnt lgkmcnt(7)
	v_mfma_f32_16x16x32_bf16 v[66:69], v[146:149], v[98:101], 0
	v_mfma_f32_16x16x32_bf16 v[70:73], v[146:149], v[114:117], 0
	ds_read_b128 v[146:149], v185 offset:32768
	s_waitcnt lgkmcnt(7)
	v_mfma_f32_16x16x32_bf16 v[74:77], v[150:153], v[98:101], 0
	v_mfma_f32_16x16x32_bf16 v[78:81], v[150:153], v[114:117], 0
	ds_read_b128 v[150:153], v185 offset:36864
	s_waitcnt lgkmcnt(7)
	v_mfma_f32_16x16x32_bf16 v[82:85], v[154:157], v[98:101], 0
	v_mfma_f32_16x16x32_bf16 v[86:89], v[154:157], v[114:117], 0
	ds_read_b128 v[154:157], v185 offset:40960
	s_waitcnt lgkmcnt(7)
	v_mfma_f32_16x16x32_bf16 v[90:93], v[158:161], v[98:101], 0
	v_mfma_f32_16x16x32_bf16 v[94:97], v[158:161], v[114:117], 0
	ds_read_b128 v[158:161], v185 offset:45056
	s_waitcnt lgkmcnt(7)
	v_mfma_f32_16x16x32_bf16 v[66:69], v[198:201], v[102:105], v[66:69]
	v_mfma_f32_16x16x32_bf16 v[70:73], v[198:201], v[118:121], v[70:73]
	ds_read_b128 v[198:201], v186 offset:32768
	s_waitcnt lgkmcnt(7)
	v_mfma_f32_16x16x32_bf16 v[74:77], v[202:205], v[102:105], v[74:77]
	v_mfma_f32_16x16x32_bf16 v[78:81], v[202:205], v[118:121], v[78:81]
	ds_read_b128 v[202:205], v186 offset:36864
	s_waitcnt lgkmcnt(7)
	v_mfma_f32_16x16x32_bf16 v[82:85], v[206:209], v[102:105], v[82:85]
	v_mfma_f32_16x16x32_bf16 v[86:89], v[206:209], v[118:121], v[86:89]
	ds_read_b128 v[206:209], v186 offset:40960
	s_waitcnt lgkmcnt(7)
; #define SBAR() __builtin_amdgcn_sched_barrier(0)
; #define RESC(a) do { if (__any((a) < 1.f)) { if (hi == 0) al_l[r32] = (a); asm volatile("s_waitcnt lgkmcnt(0)" ::: "memory"); \
;     for (int d = 0; d < 4; ++d) for (int r = 0; r < 16; ++r) o[d][r] *= al_l[crow(r, hi)]; } } while (0)
; #define RESC(a) do { if (__any((a) < 1.f)) { if (hi == 0) al_l[r32] = (a); asm volatile("s_waitcnt lgkmcnt(0)" ::: "memory"); \
;     for (int d = 0; d < 4; ++d) for (int r = 0; r < 16; ++r) o[d][r] *= al_l[crow(r, hi)]; } } while (0)
; #define ATT_SYNC(jn) do { ATT_WAIT_BAR(); if ((jn) < NT) ATT_DMA((jn), (jn) & 3); } while (0)
; __device__ __forceinline__ void attn_dma_body(const bf16_t* __restrict__ Qb, int ldq, int tpos0, const float* __restrict__ rope, const float* __restrict__ qgain, ...
;     ...
;   for (int j = 1; j + 1 < NT; j += 2) {
;     { SBAR(); qkt(pB0, pB1, (const bf16_t*)(lds + (j & 3) * SHM_SLOT), qr, r32, hi);
;       finishSM(pA0, pA1, alA, l_reg, pa0, pa1, pa2, pa3); s16x4 va[8]; pv_rd<0>(va, vb0 + ((j - 1) & 3) * (int)SHM_SLOT); SBAR();
;       if (!lead) ATT_SYNC(j + 2);
;       pv_d0_pre(o, vb0 + ((j - 1) & 3) * (int)SHM_SLOT, va, pa0, pa1, pa2, pa3); partialSM(pB0, pB1, m_reg, mnB, alB);
;       if (lead) ATT_SYNC(j + 2);
;       RESC(alB); }
;     { SBAR(); qkt(pA0, pA1, (const bf16_t*)(lds + ((j + 1) & 3) * SHM_SLOT), qr, r32, hi);
;       finishSM(pB0, pB1, alB, l_reg, pa0, pa1, pa2, pa3); s16x4 va[8]; pv_rd<0>(va, vb0 + (j & 3) * (int)SHM_SLOT); SBAR();
;       if (!lead) ATT_SYNC(j + 3);
;       pv_d0_pre(o, vb0 + (j & 3) * (int)SHM_SLOT, va, pa0, pa1, pa2, pa3); partialSM(pA0, pA1, m_reg, mnA, alA);
;       if (lead) ATT_SYNC(j + 3);
;       RESC(alA); }
;   }
	v_mfma_f32_16x16x32_bf16 v[90:93], v[210:213], v[102:105], v[90:93]
	v_mfma_f32_16x16x32_bf16 v[94:97], v[210:213], v[118:121], v[94:97]
	ds_read_b128 v[210:213], v186 offset:45056
	s_waitcnt lgkmcnt(7)
	v_mfma_f32_16x16x32_bf16 v[66:69], v[146:149], v[106:109], v[66:69]
	v_mfma_f32_16x16x32_bf16 v[70:73], v[146:149], v[122:125], v[70:73]
	s_waitcnt lgkmcnt(6)
	v_mfma_f32_16x16x32_bf16 v[74:77], v[150:153], v[106:109], v[74:77]
	v_mfma_f32_16x16x32_bf16 v[78:81], v[150:153], v[122:125], v[78:81]
	s_waitcnt lgkmcnt(5)
	v_mfma_f32_16x16x32_bf16 v[82:85], v[154:157], v[106:109], v[82:85]
	v_mfma_f32_16x16x32_bf16 v[86:89], v[154:157], v[122:125], v[86:89]
	s_waitcnt lgkmcnt(4)
	v_mfma_f32_16x16x32_bf16 v[90:93], v[158:161], v[106:109], v[90:93]
	v_mfma_f32_16x16x32_bf16 v[94:97], v[158:161], v[122:125], v[94:97]
	s_waitcnt lgkmcnt(3)
	v_mfma_f32_16x16x32_bf16 v[66:69], v[198:201], v[110:113], v[66:69]
	v_mfma_f32_16x16x32_bf16 v[70:73], v[198:201], v[126:129], v[70:73]
	ds_read_b64_tr_b16 v[214:215], v191 offset:0
	ds_read_b64_tr_b16 v[216:217], v191 offset:4096
	ds_read_b64_tr_b16 v[218:219], v192 offset:0
	ds_read_b64_tr_b16 v[220:221], v192 offset:4096
	ds_read_b64_tr_b16 v[222:223], v191 offset:512
	ds_read_b64_tr_b16 v[224:225], v191 offset:4608
	ds_read_b64_tr_b16 v[226:227], v192 offset:512
	ds_read_b64_tr_b16 v[228:229], v192 offset:4608
	s_waitcnt lgkmcnt(10)
	v_mfma_f32_16x16x32_bf16 v[74:77], v[202:205], v[110:113], v[74:77]
	v_mfma_f32_16x16x32_bf16 v[78:81], v[202:205], v[126:129], v[78:81]
	s_waitcnt lgkmcnt(9)
	v_mfma_f32_16x16x32_bf16 v[82:85], v[206:209], v[110:113], v[82:85]
	v_mfma_f32_16x16x32_bf16 v[86:89], v[206:209], v[126:129], v[86:89]
	s_waitcnt lgkmcnt(8)
	v_mfma_f32_16x16x32_bf16 v[90:93], v[210:213], v[110:113], v[90:93]
	v_mfma_f32_16x16x32_bf16 v[94:97], v[210:213], v[126:129], v[94:97]
	s_waitcnt lgkmcnt(6)
	v_mfma_f32_16x16x32_bf16 v[2:5], v[214:217], v[130:133], v[2:5]
	v_exp_f32_e32 v66, v66
	v_mfma_f32_16x16x32_bf16 v[6:9], v[214:217], v[138:141], v[6:9]
	v_exp_f32_e32 v67, v67
	ds_read_b64_tr_b16 v[230:231], v191 offset:1024
	ds_read_b64_tr_b16 v[232:233], v191 offset:5120
	s_waitcnt lgkmcnt(6)
	v_mfma_f32_16x16x32_bf16 v[10:13], v[218:221], v[130:133], v[10:13]
	v_exp_f32_e32 v68, v68
	v_mfma_f32_16x16x32_bf16 v[14:17], v[218:221], v[138:141], v[14:17]
	v_exp_f32_e32 v69, v69
	ds_read_b64_tr_b16 v[234:235], v192 offset:1024
	ds_read_b64_tr_b16 v[236:237], v192 offset:5120
	s_waitcnt lgkmcnt(6)
	v_mfma_f32_16x16x32_bf16 v[18:21], v[222:225], v[130:133], v[18:21]
	v_exp_f32_e32 v70, v70
	v_mfma_f32_16x16x32_bf16 v[22:25], v[222:225], v[138:141], v[22:25]
	v_exp_f32_e32 v71, v71
	ds_read_b64_tr_b16 v[238:239], v191 offset:1536
	ds_read_b64_tr_b16 v[240:241], v191 offset:5632
	s_waitcnt lgkmcnt(6)
	v_mfma_f32_16x16x32_bf16 v[26:29], v[226:229], v[130:133], v[26:29]
	v_exp_f32_e32 v72, v72
	v_mfma_f32_16x16x32_bf16 v[30:33], v[226:229], v[138:141], v[30:33]
	v_exp_f32_e32 v73, v73
	v_mfma_f32_16x16x32_bf16 v[246:249], v[194:197], v[130:133], v[246:249]
	ds_read_b64_tr_b16 v[242:243], v192 offset:1536
	ds_read_b64_tr_b16 v[244:245], v192 offset:5632
	s_waitcnt lgkmcnt(6)
	v_mfma_f32_16x16x32_bf16 v[34:37], v[230:233], v[130:133], v[34:37]
	v_exp_f32_e32 v74, v74
	v_mfma_f32_16x16x32_bf16 v[38:41], v[230:233], v[138:141], v[38:41]
	v_exp_f32_e32 v75, v75
	ds_read_b64_tr_b16 v[214:215], v191 offset:8192
	ds_read_b64_tr_b16 v[216:217], v191 offset:12288
	s_waitcnt lgkmcnt(6)
	v_mfma_f32_16x16x32_bf16 v[42:45], v[234:237], v[130:133], v[42:45]
	v_exp_f32_e32 v76, v76
	v_mfma_f32_16x16x32_bf16 v[46:49], v[234:237], v[138:141], v[46:49]
	v_exp_f32_e32 v77, v77
	ds_read_b64_tr_b16 v[218:219], v192 offset:8192
	ds_read_b64_tr_b16 v[220:221], v192 offset:12288
	s_waitcnt lgkmcnt(6)
	v_mfma_f32_16x16x32_bf16 v[50:53], v[238:241], v[130:133], v[50:53]
	v_exp_f32_e32 v78, v78
	v_mfma_f32_16x16x32_bf16 v[54:57], v[238:241], v[138:141], v[54:57]
	v_exp_f32_e32 v79, v79
	ds_read_b64_tr_b16 v[222:223], v191 offset:8704
	ds_read_b64_tr_b16 v[224:225], v191 offset:12800
	s_waitcnt lgkmcnt(6)
	v_mfma_f32_16x16x32_bf16 v[58:61], v[242:245], v[130:133], v[58:61]
	v_exp_f32_e32 v80, v80
	v_mfma_f32_16x16x32_bf16 v[62:65], v[242:245], v[138:141], v[62:65]
	v_exp_f32_e32 v81, v81
	v_mfma_f32_16x16x32_bf16 v[252:255], v[194:197], v[138:141], v[252:255]
	ds_read_b64_tr_b16 v[226:227], v192 offset:8704
	ds_read_b64_tr_b16 v[228:229], v192 offset:12800
	s_waitcnt lgkmcnt(6)
	v_mfma_f32_16x16x32_bf16 v[2:5], v[214:217], v[134:137], v[2:5]
	v_exp_f32_e32 v82, v82
	v_mfma_f32_16x16x32_bf16 v[6:9], v[214:217], v[142:145], v[6:9]
	v_exp_f32_e32 v83, v83
	ds_read_b64_tr_b16 v[230:231], v191 offset:9216
	ds_read_b64_tr_b16 v[232:233], v191 offset:13312
	s_waitcnt lgkmcnt(6)
	v_mfma_f32_16x16x32_bf16 v[10:13], v[218:221], v[134:137], v[10:13]
	v_exp_f32_e32 v84, v84
	v_mfma_f32_16x16x32_bf16 v[14:17], v[218:221], v[142:145], v[14:17]
	v_exp_f32_e32 v85, v85
	ds_read_b64_tr_b16 v[234:235], v192 offset:9216
	ds_read_b64_tr_b16 v[236:237], v192 offset:13312
	s_waitcnt lgkmcnt(6)
	v_mfma_f32_16x16x32_bf16 v[18:21], v[222:225], v[134:137], v[18:21]
	v_exp_f32_e32 v86, v86
	v_mfma_f32_16x16x32_bf16 v[22:25], v[222:225], v[142:145], v[22:25]
	v_exp_f32_e32 v87, v87
	ds_read_b64_tr_b16 v[238:239], v191 offset:9728
	ds_read_b64_tr_b16 v[240:241], v191 offset:13824
	s_waitcnt lgkmcnt(6)
	v_mfma_f32_16x16x32_bf16 v[26:29], v[226:229], v[134:137], v[26:29]
	v_exp_f32_e32 v88, v88
	v_mfma_f32_16x16x32_bf16 v[30:33], v[226:229], v[142:145], v[30:33]
	v_exp_f32_e32 v89, v89
	v_mfma_f32_16x16x32_bf16 v[246:249], v[194:197], v[134:137], v[246:249]
	ds_read_b64_tr_b16 v[242:243], v192 offset:9728
	ds_read_b64_tr_b16 v[244:245], v192 offset:13824
	s_waitcnt lgkmcnt(6)
	v_mfma_f32_16x16x32_bf16 v[34:37], v[230:233], v[134:137], v[34:37]
	v_exp_f32_e32 v90, v90
	v_mfma_f32_16x16x32_bf16 v[38:41], v[230:233], v[142:145], v[38:41]
	v_exp_f32_e32 v91, v91
	s_waitcnt lgkmcnt(4)
	v_mfma_f32_16x16x32_bf16 v[42:45], v[234:237], v[134:137], v[42:45]
	v_exp_f32_e32 v92, v92
	v_mfma_f32_16x16x32_bf16 v[46:49], v[234:237], v[142:145], v[46:49]
	v_exp_f32_e32 v93, v93
	s_waitcnt lgkmcnt(2)
	v_mfma_f32_16x16x32_bf16 v[50:53], v[238:241], v[134:137], v[50:53]
	v_exp_f32_e32 v94, v94
	v_mfma_f32_16x16x32_bf16 v[54:57], v[238:241], v[142:145], v[54:57]
	v_exp_f32_e32 v95, v95
	s_waitcnt lgkmcnt(0)
	v_mfma_f32_16x16x32_bf16 v[58:61], v[242:245], v[134:137], v[58:61]
	v_exp_f32_e32 v96, v96
	v_mfma_f32_16x16x32_bf16 v[62:65], v[242:245], v[142:145], v[62:65]
	v_exp_f32_e32 v97, v97
	v_mfma_f32_16x16x32_bf16 v[252:255], v[194:197], v[142:145], v[252:255]
	s_cmp_ge_u32 s97, 131
	s_cbranch_scc1 .Lf16_se_L0
; #define SBAR() __builtin_amdgcn_sched_barrier(0)
; #define RESC(a) do { if (__any((a) < 1.f)) { if (hi == 0) al_l[r32] = (a); asm volatile("s_waitcnt lgkmcnt(0)" ::: "memory"); \
;     for (int d = 0; d < 4; ++d) for (int r = 0; r < 16; ++r) o[d][r] *= al_l[crow(r, hi)]; } } while (0)
; #define RESC(a) do { if (__any((a) < 1.f)) { if (hi == 0) al_l[r32] = (a); asm volatile("s_waitcnt lgkmcnt(0)" ::: "memory"); \
;     for (int d = 0; d < 4; ++d) for (int r = 0; r < 16; ++r) o[d][r] *= al_l[crow(r, hi)]; } } while (0)
; #define ATT_SYNC(jn) do { ATT_WAIT_BAR(); if ((jn) < NT) ATT_DMA((jn), (jn) & 3); } while (0)
; __device__ __forceinline__ void attn_dma_body(const bf16_t* __restrict__ Qb, int ldq, int tpos0, const float* __restrict__ rope, const float* __restrict__ qgain, ...
;     ...
;   for (int j = 1; j + 1 < NT; j += 2) {
;     { SBAR(); qkt(pB0, pB1, (const bf16_t*)(lds + (j & 3) * SHM_SLOT), qr, r32, hi);
;       finishSM(pA0, pA1, alA, l_reg, pa0, pa1, pa2, pa3); s16x4 va[8]; pv_rd<0>(va, vb0 + ((j - 1) & 3) * (int)SHM_SLOT); SBAR();
;       if (!lead) ATT_SYNC(j + 2);
;       pv_d0_pre(o, vb0 + ((j - 1) & 3) * (int)SHM_SLOT, va, pa0, pa1, pa2, pa3); partialSM(pB0, pB1, m_reg, mnB, alB);
;       if (lead) ATT_SYNC(j + 2);
;       RESC(alB); }
;     { SBAR(); qkt(pA0, pA1, (const bf16_t*)(lds + ((j + 1) & 3) * SHM_SLOT), qr, r32, hi);
;       finishSM(pB0, pB1, alB, l_reg, pa0, pa1, pa2, pa3); s16x4 va[8]; pv_rd<0>(va, vb0 + (j & 3) * (int)SHM_SLOT); SBAR();
;       if (!lead) ATT_SYNC(j + 3);
;       pv_d0_pre(o, vb0 + (j & 3) * (int)SHM_SLOT, va, pa0, pa1, pa2, pa3); partialSM(pA0, pA1, m_reg, mnA, alA);
;       if (lead) ATT_SYNC(j + 3);
;       RESC(alA); }
;   }
	s_waitcnt vmcnt(0) lgkmcnt(0)
	s_barrier
	s_cmp_ge_u32 s97, 130
	s_cbranch_scc1 .Lf16_se_L0
	s_add_i32 s6, s96, 0x18000
	s_mov_b32 m0, s6
	s_nop 0
	global_load_lds_dwordx4 v170, s[2:3]
	s_add_i32 m0, s6, 0x2000
	s_nop 0
	global_load_lds_dwordx4 v172, s[2:3]
	s_add_i32 m0, s6, 0x4000
	s_nop 0
	global_load_lds_dwordx4 v171, s[4:5]
	s_add_i32 m0, s6, 0x6000
	s_nop 0
	global_load_lds_dwordx4 v173, s[4:5]
	s_add_u32 s2, s2, 0x4000
	s_addc_u32 s3, s3, 0
	s_add_u32 s4, s4, 0x4000
	s_addc_u32 s5, s5, 0
.Lf16_se_L0:
	v_cvt_pk_bf16_f32 v130, v66, v67
	v_cvt_pk_bf16_f32 v131, v68, v69
	v_cvt_pk_bf16_f32 v132, v74, v75
	v_cvt_pk_bf16_f32 v133, v76, v77
	v_cvt_pk_bf16_f32 v134, v82, v83
	v_cvt_pk_bf16_f32 v135, v84, v85
	v_cvt_pk_bf16_f32 v136, v90, v91
	v_cvt_pk_bf16_f32 v137, v92, v93
	v_cvt_pk_bf16_f32 v138, v70, v71
	v_cvt_pk_bf16_f32 v139, v72, v73
	v_cvt_pk_bf16_f32 v140, v78, v79
	v_cvt_pk_bf16_f32 v141, v80, v81
	v_cvt_pk_bf16_f32 v142, v86, v87
	v_cvt_pk_bf16_f32 v143, v88, v89
	v_cvt_pk_bf16_f32 v144, v94, v95
	v_cvt_pk_bf16_f32 v145, v96, v97
	s_add_i32 s97, s97, 1
	s_cmp_lt_u32 s97, 132
	s_cbranch_scc0 .Lf16_done
	ds_read_b128 v[146:149], v187 offset:0
	ds_read_b128 v[150:153], v187 offset:4096
	ds_read_b128 v[154:157], v187 offset:8192
	ds_read_b128 v[158:161], v187 offset:12288
	ds_read_b128 v[198:201], v188 offset:0
	ds_read_b128 v[202:205], v188 offset:4096
	ds_read_b128 v[206:209], v188 offset:8192
	ds_read_b128 v[210:213], v188 offset:12288
	s_waitcnt lgkmcnt(7)
	v_mfma_f32_16x16x32_bf16 v[66:69], v[146:149], v[98:101], 0
	v_mfma_f32_16x16x32_bf16 v[70:73], v[146:149], v[114:117], 0
	ds_read_b128 v[146:149], v189 offset:0
	s_waitcnt lgkmcnt(7)
	v_mfma_f32_16x16x32_bf16 v[74:77], v[150:153], v[98:101], 0
	v_mfma_f32_16x16x32_bf16 v[78:81], v[150:153], v[114:117], 0
	ds_read_b128 v[150:153], v189 offset:4096
	s_waitcnt lgkmcnt(7)
	v_mfma_f32_16x16x32_bf16 v[82:85], v[154:157], v[98:101], 0
	v_mfma_f32_16x16x32_bf16 v[86:89], v[154:157], v[114:117], 0
	ds_read_b128 v[154:157], v189 offset:8192
	s_waitcnt lgkmcnt(7)
	v_mfma_f32_16x16x32_bf16 v[90:93], v[158:161], v[98:101], 0
	v_mfma_f32_16x16x32_bf16 v[94:97], v[158:161], v[114:117], 0
	ds_read_b128 v[158:161], v189 offset:12288
	s_waitcnt lgkmcnt(7)
	v_mfma_f32_16x16x32_bf16 v[66:69], v[198:201], v[102:105], v[66:69]
	v_mfma_f32_16x16x32_bf16 v[70:73], v[198:201], v[118:121], v[70:73]
	ds_read_b128 v[198:201], v190 offset:0
	s_waitcnt lgkmcnt(7)
	v_mfma_f32_16x16x32_bf16 v[74:77], v[202:205], v[102:105], v[74:77]
	v_mfma_f32_16x16x32_bf16 v[78:81], v[202:205], v[118:121], v[78:81]
	ds_read_b128 v[202:205], v190 offset:4096
	s_waitcnt lgkmcnt(7)
	v_mfma_f32_16x16x32_bf16 v[82:85], v[206:209], v[102:105], v[82:85]
	v_mfma_f32_16x16x32_bf16 v[86:89], v[206:209], v[118:121], v[86:89]
	ds_read_b128 v[206:209], v190 offset:8192
	s_waitcnt lgkmcnt(7)
	v_mfma_f32_16x16x32_bf16 v[90:93], v[210:213], v[102:105], v[90:93]
	v_mfma_f32_16x16x32_bf16 v[94:97], v[210:213], v[118:121], v[94:97]
	ds_read_b128 v[210:213], v190 offset:12288
	s_waitcnt lgkmcnt(7)
	v_mfma_f32_16x16x32_bf16 v[66:69], v[146:149], v[106:109], v[66:69]
	v_mfma_f32_16x16x32_bf16 v[70:73], v[146:149], v[122:125], v[70:73]
	s_waitcnt lgkmcnt(6)
	v_mfma_f32_16x16x32_bf16 v[74:77], v[150:153], v[106:109], v[74:77]
	v_mfma_f32_16x16x32_bf16 v[78:81], v[150:153], v[122:125], v[78:81]
	s_waitcnt lgkmcnt(5)
	v_mfma_f32_16x16x32_bf16 v[82:85], v[154:157], v[106:109], v[82:85]
	v_mfma_f32_16x16x32_bf16 v[86:89], v[154:157], v[122:125], v[86:89]
	s_waitcnt lgkmcnt(4)
	v_mfma_f32_16x16x32_bf16 v[90:93], v[158:161], v[106:109], v[90:93]
	v_mfma_f32_16x16x32_bf16 v[94:97], v[158:161], v[122:125], v[94:97]
	s_waitcnt lgkmcnt(3)
	v_mfma_f32_16x16x32_bf16 v[66:69], v[198:201], v[110:113], v[66:69]
	v_mfma_f32_16x16x32_bf16 v[70:73], v[198:201], v[126:129], v[70:73]
	ds_read_b64_tr_b16 v[214:215], v191 offset:32768
	ds_read_b64_tr_b16 v[216:217], v191 offset:36864
	ds_read_b64_tr_b16 v[218:219], v192 offset:32768
	ds_read_b64_tr_b16 v[220:221], v192 offset:36864
	ds_read_b64_tr_b16 v[222:223], v191 offset:33280
	ds_read_b64_tr_b16 v[224:225], v191 offset:37376
	ds_read_b64_tr_b16 v[226:227], v192 offset:33280
	ds_read_b64_tr_b16 v[228:229], v192 offset:37376
	s_waitcnt lgkmcnt(10)
	v_mfma_f32_16x16x32_bf16 v[74:77], v[202:205], v[110:113], v[74:77]
	v_mfma_f32_16x16x32_bf16 v[78:81], v[202:205], v[126:129], v[78:81]
	s_waitcnt lgkmcnt(9)
	v_mfma_f32_16x16x32_bf16 v[82:85], v[206:209], v[110:113], v[82:85]
	v_mfma_f32_16x16x32_bf16 v[86:89], v[206:209], v[126:129], v[86:89]
	s_waitcnt lgkmcnt(8)
	v_mfma_f32_16x16x32_bf16 v[90:93], v[210:213], v[110:113], v[90:93]
	v_mfma_f32_16x16x32_bf16 v[94:97], v[210:213], v[126:129], v[94:97]
	s_waitcnt lgkmcnt(6)
	v_mfma_f32_16x16x32_bf16 v[2:5], v[214:217], v[130:133], v[2:5]
	v_exp_f32_e32 v66, v66
	v_mfma_f32_16x16x32_bf16 v[6:9], v[214:217], v[138:141], v[6:9]
	v_exp_f32_e32 v67, v67
	ds_read_b64_tr_b16 v[230:231], v191 offset:33792
	ds_read_b64_tr_b16 v[232:233], v191 offset:37888
	s_waitcnt lgkmcnt(6)
	v_mfma_f32_16x16x32_bf16 v[10:13], v[218:221], v[130:133], v[10:13]
	v_exp_f32_e32 v68, v68
	v_mfma_f32_16x16x32_bf16 v[14:17], v[218:221], v[138:141], v[14:17]
	v_exp_f32_e32 v69, v69
	ds_read_b64_tr_b16 v[234:235], v192 offset:33792
	ds_read_b64_tr_b16 v[236:237], v192 offset:37888
	s_waitcnt lgkmcnt(6)
	v_mfma_f32_16x16x32_bf16 v[18:21], v[222:225], v[130:133], v[18:21]
	v_exp_f32_e32 v70, v70
	v_mfma_f32_16x16x32_bf16 v[22:25], v[222:225], v[138:141], v[22:25]
	v_exp_f32_e32 v71, v71
	ds_read_b64_tr_b16 v[238:239], v191 offset:34304
	ds_read_b64_tr_b16 v[240:241], v191 offset:38400
	s_waitcnt lgkmcnt(6)
; #define SBAR() __builtin_amdgcn_sched_barrier(0)
; #define RESC(a) do { if (__any((a) < 1.f)) { if (hi == 0) al_l[r32] = (a); asm volatile("s_waitcnt lgkmcnt(0)" ::: "memory"); \
;     for (int d = 0; d < 4; ++d) for (int r = 0; r < 16; ++r) o[d][r] *= al_l[crow(r, hi)]; } } while (0)
; #define ATT_SYNC(jn) do { ATT_WAIT_BAR(); if ((jn) < NT) ATT_DMA((jn), (jn) & 3); } while (0)
; template <int D0> __device__ __forceinline__ void pv_rd(s16x4 (&r)[8], int vb) {
;   r[0] = tr_read<v_rd_off(D0, 0, 0)>(vb); r[1] = tr_read<v_rd_off(D0, 0, 1)>(vb); r[2] = tr_read<v_rd_off(D0, 1, 0)>(vb); r[3] = tr_read<v_rd_off(D0, 1, 1)>(vb);
;   r[4] = tr_read<v_rd_off(D0, 2, 0)>(vb); r[5] = tr_read<v_rd_off(D0, 2, 1)>(vb); r[6] = tr_read<v_rd_off(D0, 3, 0)>(vb); r[7] = tr_read<v_rd_off(D0, 3, 1)>(vb);
; }
; __device__ __forceinline__ void pv_mm(f32x16& od, const s16x4 (&r)[8], bf16x8 pa0, bf16x8 pa1, bf16x8 pa2, bf16x8 pa3) {
;     ...
;   od = __builtin_amdgcn_mfma_f32_32x32x16_bf16(pa0, PK(r[0], r[1]), od, 0, 0, 0);
;   od = __builtin_amdgcn_mfma_f32_32x32x16_bf16(pa1, PK(r[2], r[3]), od, 0, 0, 0);
;   od = __builtin_amdgcn_mfma_f32_32x32x16_bf16(pa2, PK(r[4], r[5]), od, 0, 0, 0);
;   od = __builtin_amdgcn_mfma_f32_32x32x16_bf16(pa3, PK(r[6], r[7]), od, 0, 0, 0);
;     ...
; }
; __device__ __forceinline__ void attn_dma_body(const bf16_t* __restrict__ Qb, int ldq, int tpos0, const float* __restrict__ rope, const float* __restrict__ qgain, ...
;     ...
;   for (int j = 1; j + 1 < NT; j += 2) {
;     { SBAR(); qkt(pB0, pB1, (const bf16_t*)(lds + (j & 3) * SHM_SLOT), qr, r32, hi);
;       finishSM(pA0, pA1, alA, l_reg, pa0, pa1, pa2, pa3); s16x4 va[8]; pv_rd<0>(va, vb0 + ((j - 1) & 3) * (int)SHM_SLOT); SBAR();
;       if (!lead) ATT_SYNC(j + 2);
;       pv_d0_pre(o, vb0 + ((j - 1) & 3) * (int)SHM_SLOT, va, pa0, pa1, pa2, pa3); partialSM(pB0, pB1, m_reg, mnB, alB);
;       if (lead) ATT_SYNC(j + 2);
;       RESC(alB); }
;     { SBAR(); qkt(pA0, pA1, (const bf16_t*)(lds + ((j + 1) & 3) * SHM_SLOT), qr, r32, hi);
;       finishSM(pB0, pB1, alB, l_reg, pa0, pa1, pa2, pa3); s16x4 va[8]; pv_rd<0>(va, vb0 + (j & 3) * (int)SHM_SLOT); SBAR();
;       if (!lead) ATT_SYNC(j + 3);
;       pv_d0_pre(o, vb0 + (j & 3) * (int)SHM_SLOT, va, pa0, pa1, pa2, pa3); partialSM(pA0, pA1, m_reg, mnA, alA);
;       if (lead) ATT_SYNC(j + 3);
;       RESC(alA); }
;   }
	v_mfma_f32_16x16x32_bf16 v[26:29], v[226:229], v[130:133], v[26:29]
	v_exp_f32_e32 v72, v72
	v_mfma_f32_16x16x32_bf16 v[30:33], v[226:229], v[138:141], v[30:33]
	v_exp_f32_e32 v73, v73
	v_mfma_f32_16x16x32_bf16 v[246:249], v[194:197], v[130:133], v[246:249]
	ds_read_b64_tr_b16 v[242:243], v192 offset:34304
	ds_read_b64_tr_b16 v[244:245], v192 offset:38400
	s_waitcnt lgkmcnt(6)
	v_mfma_f32_16x16x32_bf16 v[34:37], v[230:233], v[130:133], v[34:37]
	v_exp_f32_e32 v74, v74
	v_mfma_f32_16x16x32_bf16 v[38:41], v[230:233], v[138:141], v[38:41]
	v_exp_f32_e32 v75, v75
	ds_read_b64_tr_b16 v[214:215], v191 offset:40960
	ds_read_b64_tr_b16 v[216:217], v191 offset:45056
	s_waitcnt lgkmcnt(6)
	v_mfma_f32_16x16x32_bf16 v[42:45], v[234:237], v[130:133], v[42:45]
	v_exp_f32_e32 v76, v76
	v_mfma_f32_16x16x32_bf16 v[46:49], v[234:237], v[138:141], v[46:49]
	v_exp_f32_e32 v77, v77
	ds_read_b64_tr_b16 v[218:219], v192 offset:40960
	ds_read_b64_tr_b16 v[220:221], v192 offset:45056
	s_waitcnt lgkmcnt(6)
	v_mfma_f32_16x16x32_bf16 v[50:53], v[238:241], v[130:133], v[50:53]
	v_exp_f32_e32 v78, v78
	v_mfma_f32_16x16x32_bf16 v[54:57], v[238:241], v[138:141], v[54:57]
	v_exp_f32_e32 v79, v79
	ds_read_b64_tr_b16 v[222:223], v191 offset:41472
	ds_read_b64_tr_b16 v[224:225], v191 offset:45568
	s_waitcnt lgkmcnt(6)
	v_mfma_f32_16x16x32_bf16 v[58:61], v[242:245], v[130:133], v[58:61]
	v_exp_f32_e32 v80, v80
	v_mfma_f32_16x16x32_bf16 v[62:65], v[242:245], v[138:141], v[62:65]
	v_exp_f32_e32 v81, v81
	v_mfma_f32_16x16x32_bf16 v[252:255], v[194:197], v[138:141], v[252:255]
	ds_read_b64_tr_b16 v[226:227], v192 offset:41472
	ds_read_b64_tr_b16 v[228:229], v192 offset:45568
	s_waitcnt lgkmcnt(6)
	v_mfma_f32_16x16x32_bf16 v[2:5], v[214:217], v[134:137], v[2:5]
	v_exp_f32_e32 v82, v82
	v_mfma_f32_16x16x32_bf16 v[6:9], v[214:217], v[142:145], v[6:9]
	v_exp_f32_e32 v83, v83
	ds_read_b64_tr_b16 v[230:231], v191 offset:41984
	ds_read_b64_tr_b16 v[232:233], v191 offset:46080
	s_waitcnt lgkmcnt(6)
	v_mfma_f32_16x16x32_bf16 v[10:13], v[218:221], v[134:137], v[10:13]
	v_exp_f32_e32 v84, v84
	v_mfma_f32_16x16x32_bf16 v[14:17], v[218:221], v[142:145], v[14:17]
	v_exp_f32_e32 v85, v85
	ds_read_b64_tr_b16 v[234:235], v192 offset:41984
	ds_read_b64_tr_b16 v[236:237], v192 offset:46080
	s_waitcnt lgkmcnt(6)
	v_mfma_f32_16x16x32_bf16 v[18:21], v[222:225], v[134:137], v[18:21]
	v_exp_f32_e32 v86, v86
	v_mfma_f32_16x16x32_bf16 v[22:25], v[222:225], v[142:145], v[22:25]
	v_exp_f32_e32 v87, v87
	ds_read_b64_tr_b16 v[238:239], v191 offset:42496
	ds_read_b64_tr_b16 v[240:241], v191 offset:46592
	s_waitcnt lgkmcnt(6)
	v_mfma_f32_16x16x32_bf16 v[26:29], v[226:229], v[134:137], v[26:29]
	v_exp_f32_e32 v88, v88
	v_mfma_f32_16x16x32_bf16 v[30:33], v[226:229], v[142:145], v[30:33]
	v_exp_f32_e32 v89, v89
	v_mfma_f32_16x16x32_bf16 v[246:249], v[194:197], v[134:137], v[246:249]
	ds_read_b64_tr_b16 v[242:243], v192 offset:42496
	ds_read_b64_tr_b16 v[244:245], v192 offset:46592
	s_waitcnt lgkmcnt(6)
	v_mfma_f32_16x16x32_bf16 v[34:37], v[230:233], v[134:137], v[34:37]
	v_exp_f32_e32 v90, v90
	v_mfma_f32_16x16x32_bf16 v[38:41], v[230:233], v[142:145], v[38:41]
	v_exp_f32_e32 v91, v91
	s_waitcnt lgkmcnt(4)
	v_mfma_f32_16x16x32_bf16 v[42:45], v[234:237], v[134:137], v[42:45]
	v_exp_f32_e32 v92, v92
	v_mfma_f32_16x16x32_bf16 v[46:49], v[234:237], v[142:145], v[46:49]
	v_exp_f32_e32 v93, v93
	s_waitcnt lgkmcnt(2)
	v_mfma_f32_16x16x32_bf16 v[50:53], v[238:241], v[134:137], v[50:53]
	v_exp_f32_e32 v94, v94
	v_mfma_f32_16x16x32_bf16 v[54:57], v[238:241], v[142:145], v[54:57]
	v_exp_f32_e32 v95, v95
	s_waitcnt lgkmcnt(0)
	v_mfma_f32_16x16x32_bf16 v[58:61], v[242:245], v[134:137], v[58:61]
	v_exp_f32_e32 v96, v96
	v_mfma_f32_16x16x32_bf16 v[62:65], v[242:245], v[142:145], v[62:65]
	v_exp_f32_e32 v97, v97
	v_mfma_f32_16x16x32_bf16 v[252:255], v[194:197], v[142:145], v[252:255]
	s_cmp_ge_u32 s97, 131
	s_cbranch_scc1 .Lf16_se_L1
	s_waitcnt vmcnt(0) lgkmcnt(0)
	s_barrier
	s_cmp_ge_u32 s97, 130
	s_cbranch_scc1 .Lf16_se_L1
	s_add_i32 s6, s96, 0x0
	s_mov_b32 m0, s6
	s_nop 0
	global_load_lds_dwordx4 v170, s[2:3]
	s_add_i32 m0, s6, 0x2000
	s_nop 0
	global_load_lds_dwordx4 v172, s[2:3]
	s_add_i32 m0, s6, 0x4000
	s_nop 0
	global_load_lds_dwordx4 v171, s[4:5]
	s_add_i32 m0, s6, 0x6000
	s_nop 0
	global_load_lds_dwordx4 v173, s[4:5]
	s_add_u32 s2, s2, 0x4000
	s_addc_u32 s3, s3, 0
	s_add_u32 s4, s4, 0x4000
	s_addc_u32 s5, s5, 0
; #define SBAR() __builtin_amdgcn_sched_barrier(0)
; #define RESC(a) do { if (__any((a) < 1.f)) { if (hi == 0) al_l[r32] = (a); asm volatile("s_waitcnt lgkmcnt(0)" ::: "memory"); \
;     for (int d = 0; d < 4; ++d) for (int r = 0; r < 16; ++r) o[d][r] *= al_l[crow(r, hi)]; } } while (0)
; #define ATT_SYNC(jn) do { ATT_WAIT_BAR(); if ((jn) < NT) ATT_DMA((jn), (jn) & 3); } while (0)
; template <int D0> __device__ __forceinline__ void pv_rd(s16x4 (&r)[8], int vb) {
;   r[0] = tr_read<v_rd_off(D0, 0, 0)>(vb); r[1] = tr_read<v_rd_off(D0, 0, 1)>(vb); r[2] = tr_read<v_rd_off(D0, 1, 0)>(vb); r[3] = tr_read<v_rd_off(D0, 1, 1)>(vb);
;   r[4] = tr_read<v_rd_off(D0, 2, 0)>(vb); r[5] = tr_read<v_rd_off(D0, 2, 1)>(vb); r[6] = tr_read<v_rd_off(D0, 3, 0)>(vb); r[7] = tr_read<v_rd_off(D0, 3, 1)>(vb);
; }
; __device__ __forceinline__ void pv_mm(f32x16& od, const s16x4 (&r)[8], bf16x8 pa0, bf16x8 pa1, bf16x8 pa2, bf16x8 pa3) {
;     ...
;   od = __builtin_amdgcn_mfma_f32_32x32x16_bf16(pa0, PK(r[0], r[1]), od, 0, 0, 0);
;   od = __builtin_amdgcn_mfma_f32_32x32x16_bf16(pa1, PK(r[2], r[3]), od, 0, 0, 0);
;   od = __builtin_amdgcn_mfma_f32_32x32x16_bf16(pa2, PK(r[4], r[5]), od, 0, 0, 0);
;   od = __builtin_amdgcn_mfma_f32_32x32x16_bf16(pa3, PK(r[6], r[7]), od, 0, 0, 0);
;     ...
; }
; __device__ __forceinline__ void attn_dma_body(const bf16_t* __restrict__ Qb, int ldq, int tpos0, const float* __restrict__ rope, const float* __restrict__ qgain, ...
;     ...
;   for (int j = 1; j + 1 < NT; j += 2) {
;     { SBAR(); qkt(pB0, pB1, (const bf16_t*)(lds + (j & 3) * SHM_SLOT), qr, r32, hi);
;       finishSM(pA0, pA1, alA, l_reg, pa0, pa1, pa2, pa3); s16x4 va[8]; pv_rd<0>(va, vb0 + ((j - 1) & 3) * (int)SHM_SLOT); SBAR();
;       if (!lead) ATT_SYNC(j + 2);
;       pv_d0_pre(o, vb0 + ((j - 1) & 3) * (int)SHM_SLOT, va, pa0, pa1, pa2, pa3); partialSM(pB0, pB1, m_reg, mnB, alB);
;       if (lead) ATT_SYNC(j + 2);
;       RESC(alB); }
;     { SBAR(); qkt(pA0, pA1, (const bf16_t*)(lds + ((j + 1) & 3) * SHM_SLOT), qr, r32, hi);
;       finishSM(pB0, pB1, alB, l_reg, pa0, pa1, pa2, pa3); s16x4 va[8]; pv_rd<0>(va, vb0 + (j & 3) * (int)SHM_SLOT); SBAR();
;       if (!lead) ATT_SYNC(j + 3);
;       pv_d0_pre(o, vb0 + (j & 3) * (int)SHM_SLOT, va, pa0, pa1, pa2, pa3); partialSM(pA0, pA1, m_reg, mnA, alA);
;       if (lead) ATT_SYNC(j + 3);
;       RESC(alA); }
;   }
.Lf16_se_L1:
	v_cvt_pk_bf16_f32 v130, v66, v67
	v_cvt_pk_bf16_f32 v131, v68, v69
	v_cvt_pk_bf16_f32 v132, v74, v75
	v_cvt_pk_bf16_f32 v133, v76, v77
	v_cvt_pk_bf16_f32 v134, v82, v83
	v_cvt_pk_bf16_f32 v135, v84, v85
	v_cvt_pk_bf16_f32 v136, v90, v91
	v_cvt_pk_bf16_f32 v137, v92, v93
	v_cvt_pk_bf16_f32 v138, v70, v71
	v_cvt_pk_bf16_f32 v139, v72, v73
	v_cvt_pk_bf16_f32 v140, v78, v79
	v_cvt_pk_bf16_f32 v141, v80, v81
	v_cvt_pk_bf16_f32 v142, v86, v87
	v_cvt_pk_bf16_f32 v143, v88, v89
	v_cvt_pk_bf16_f32 v144, v94, v95
	v_cvt_pk_bf16_f32 v145, v96, v97
	s_add_i32 s97, s97, 1
	s_cmp_lt_u32 s97, 132
	s_cbranch_scc0 .Lf16_done
	ds_read_b128 v[146:149], v187 offset:32768
	ds_read_b128 v[150:153], v187 offset:36864
	ds_read_b128 v[154:157], v187 offset:40960
	ds_read_b128 v[158:161], v187 offset:45056
	ds_read_b128 v[198:201], v188 offset:32768
	ds_read_b128 v[202:205], v188 offset:36864
	ds_read_b128 v[206:209], v188 offset:40960
	ds_read_b128 v[210:213], v188 offset:45056
	s_waitcnt lgkmcnt(7)
	v_mfma_f32_16x16x32_bf16 v[66:69], v[146:149], v[98:101], 0
	v_mfma_f32_16x16x32_bf16 v[70:73], v[146:149], v[114:117], 0
	ds_read_b128 v[146:149], v189 offset:32768
	s_waitcnt lgkmcnt(7)
	v_mfma_f32_16x16x32_bf16 v[74:77], v[150:153], v[98:101], 0
	v_mfma_f32_16x16x32_bf16 v[78:81], v[150:153], v[114:117], 0
	ds_read_b128 v[150:153], v189 offset:36864
	s_waitcnt lgkmcnt(7)
	v_mfma_f32_16x16x32_bf16 v[82:85], v[154:157], v[98:101], 0
	v_mfma_f32_16x16x32_bf16 v[86:89], v[154:157], v[114:117], 0
	ds_read_b128 v[154:157], v189 offset:40960
	s_waitcnt lgkmcnt(7)
	v_mfma_f32_16x16x32_bf16 v[90:93], v[158:161], v[98:101], 0
	v_mfma_f32_16x16x32_bf16 v[94:97], v[158:161], v[114:117], 0
	ds_read_b128 v[158:161], v189 offset:45056
	s_waitcnt lgkmcnt(7)
	v_mfma_f32_16x16x32_bf16 v[66:69], v[198:201], v[102:105], v[66:69]
	v_mfma_f32_16x16x32_bf16 v[70:73], v[198:201], v[118:121], v[70:73]
	ds_read_b128 v[198:201], v190 offset:32768
	s_waitcnt lgkmcnt(7)
	v_mfma_f32_16x16x32_bf16 v[74:77], v[202:205], v[102:105], v[74:77]
	v_mfma_f32_16x16x32_bf16 v[78:81], v[202:205], v[118:121], v[78:81]
	ds_read_b128 v[202:205], v190 offset:36864
	s_waitcnt lgkmcnt(7)
	v_mfma_f32_16x16x32_bf16 v[82:85], v[206:209], v[102:105], v[82:85]
	v_mfma_f32_16x16x32_bf16 v[86:89], v[206:209], v[118:121], v[86:89]
	ds_read_b128 v[206:209], v190 offset:40960
	s_waitcnt lgkmcnt(7)
	v_mfma_f32_16x16x32_bf16 v[90:93], v[210:213], v[102:105], v[90:93]
	v_mfma_f32_16x16x32_bf16 v[94:97], v[210:213], v[118:121], v[94:97]
	ds_read_b128 v[210:213], v190 offset:45056
	s_waitcnt lgkmcnt(7)
	v_mfma_f32_16x16x32_bf16 v[66:69], v[146:149], v[106:109], v[66:69]
	v_mfma_f32_16x16x32_bf16 v[70:73], v[146:149], v[122:125], v[70:73]
	s_waitcnt lgkmcnt(6)
	v_mfma_f32_16x16x32_bf16 v[74:77], v[150:153], v[106:109], v[74:77]
	v_mfma_f32_16x16x32_bf16 v[78:81], v[150:153], v[122:125], v[78:81]
	s_waitcnt lgkmcnt(5)
	v_mfma_f32_16x16x32_bf16 v[82:85], v[154:157], v[106:109], v[82:85]
	v_mfma_f32_16x16x32_bf16 v[86:89], v[154:157], v[122:125], v[86:89]
	s_waitcnt lgkmcnt(4)
	v_mfma_f32_16x16x32_bf16 v[90:93], v[158:161], v[106:109], v[90:93]
	v_mfma_f32_16x16x32_bf16 v[94:97], v[158:161], v[122:125], v[94:97]
	s_waitcnt lgkmcnt(3)
	v_mfma_f32_16x16x32_bf16 v[66:69], v[198:201], v[110:113], v[66:69]
	v_mfma_f32_16x16x32_bf16 v[70:73], v[198:201], v[126:129], v[70:73]
	ds_read_b64_tr_b16 v[214:215], v180 offset:0
	ds_read_b64_tr_b16 v[216:217], v180 offset:4096
	ds_read_b64_tr_b16 v[218:219], v181 offset:0
	ds_read_b64_tr_b16 v[220:221], v181 offset:4096
	ds_read_b64_tr_b16 v[222:223], v180 offset:512
	ds_read_b64_tr_b16 v[224:225], v180 offset:4608
	ds_read_b64_tr_b16 v[226:227], v181 offset:512
	ds_read_b64_tr_b16 v[228:229], v181 offset:4608
	s_waitcnt lgkmcnt(10)
	v_mfma_f32_16x16x32_bf16 v[74:77], v[202:205], v[110:113], v[74:77]
	v_mfma_f32_16x16x32_bf16 v[78:81], v[202:205], v[126:129], v[78:81]
	s_waitcnt lgkmcnt(9)
	v_mfma_f32_16x16x32_bf16 v[82:85], v[206:209], v[110:113], v[82:85]
	v_mfma_f32_16x16x32_bf16 v[86:89], v[206:209], v[126:129], v[86:89]
	s_waitcnt lgkmcnt(8)
	v_mfma_f32_16x16x32_bf16 v[90:93], v[210:213], v[110:113], v[90:93]
	v_mfma_f32_16x16x32_bf16 v[94:97], v[210:213], v[126:129], v[94:97]
	s_waitcnt lgkmcnt(6)
	v_mfma_f32_16x16x32_bf16 v[2:5], v[214:217], v[130:133], v[2:5]
	v_exp_f32_e32 v66, v66
	v_mfma_f32_16x16x32_bf16 v[6:9], v[214:217], v[138:141], v[6:9]
	v_exp_f32_e32 v67, v67
	ds_read_b64_tr_b16 v[230:231], v180 offset:1024
	ds_read_b64_tr_b16 v[232:233], v180 offset:5120
	s_waitcnt lgkmcnt(6)
	v_mfma_f32_16x16x32_bf16 v[10:13], v[218:221], v[130:133], v[10:13]
	v_exp_f32_e32 v68, v68
	v_mfma_f32_16x16x32_bf16 v[14:17], v[218:221], v[138:141], v[14:17]
	v_exp_f32_e32 v69, v69
	ds_read_b64_tr_b16 v[234:235], v181 offset:1024
	ds_read_b64_tr_b16 v[236:237], v181 offset:5120
	s_waitcnt lgkmcnt(6)
	v_mfma_f32_16x16x32_bf16 v[18:21], v[222:225], v[130:133], v[18:21]
	v_exp_f32_e32 v70, v70
	v_mfma_f32_16x16x32_bf16 v[22:25], v[222:225], v[138:141], v[22:25]
	v_exp_f32_e32 v71, v71
	ds_read_b64_tr_b16 v[238:239], v180 offset:1536
	ds_read_b64_tr_b16 v[240:241], v180 offset:5632
	s_waitcnt lgkmcnt(6)
	v_mfma_f32_16x16x32_bf16 v[26:29], v[226:229], v[130:133], v[26:29]
	v_exp_f32_e32 v72, v72
	v_mfma_f32_16x16x32_bf16 v[30:33], v[226:229], v[138:141], v[30:33]
	v_exp_f32_e32 v73, v73
	v_mfma_f32_16x16x32_bf16 v[246:249], v[194:197], v[130:133], v[246:249]
	ds_read_b64_tr_b16 v[242:243], v181 offset:1536
	ds_read_b64_tr_b16 v[244:245], v181 offset:5632
	s_waitcnt lgkmcnt(6)
; #define SBAR() __builtin_amdgcn_sched_barrier(0)
; #define RESC(a) do { if (__any((a) < 1.f)) { if (hi == 0) al_l[r32] = (a); asm volatile("s_waitcnt lgkmcnt(0)" ::: "memory"); \
;     for (int d = 0; d < 4; ++d) for (int r = 0; r < 16; ++r) o[d][r] *= al_l[crow(r, hi)]; } } while (0)
; #define RESC(a) do { if (__any((a) < 1.f)) { if (hi == 0) al_l[r32] = (a); asm volatile("s_waitcnt lgkmcnt(0)" ::: "memory"); \
;     for (int d = 0; d < 4; ++d) for (int r = 0; r < 16; ++r) o[d][r] *= al_l[crow(r, hi)]; } } while (0)
; #define ATT_SYNC(jn) do { ATT_WAIT_BAR(); if ((jn) < NT) ATT_DMA((jn), (jn) & 3); } while (0)
; __device__ __forceinline__ void finishSM(f32x16& p0, f32x16& p1, float alpha, float& l_reg, bf16x8& pa0, bf16x8& pa1, bf16x8& pa2, bf16x8& pa3) {
;   for (int r = 0; r < 16; ++r) p1[r] = __builtin_amdgcn_exp2f(p1[r]);
;   float ps = 0; for (int r = 0; r < 16; ++r) ps += p0[r]; for (int r = 0; r < 16; ++r) ps += p1[r];
;   { auto rr = __builtin_amdgcn_permlane32_swap(__float_as_uint(ps), __float_as_uint(ps), false, false);
;     ps = __uint_as_float(rr[0]) + __uint_as_float(rr[1]); }
;   l_reg = l_reg * alpha + ps;
;     ...
;   PK4(p0, 0, pa0); PK4(p0, 8, pa1); PK4(p1, 0, pa2); PK4(p1, 8, pa3);
; __device__ __forceinline__ void attn_dma_body(const bf16_t* __restrict__ Qb, int ldq, int tpos0, const float* __restrict__ rope, const float* __restrict__ qgain, ...
;     ...
;   for (int j = 1; j + 1 < NT; j += 2) {
;     { SBAR(); qkt(pB0, pB1, (const bf16_t*)(lds + (j & 3) * SHM_SLOT), qr, r32, hi);
;       finishSM(pA0, pA1, alA, l_reg, pa0, pa1, pa2, pa3); s16x4 va[8]; pv_rd<0>(va, vb0 + ((j - 1) & 3) * (int)SHM_SLOT); SBAR();
;       if (!lead) ATT_SYNC(j + 2);
;       pv_d0_pre(o, vb0 + ((j - 1) & 3) * (int)SHM_SLOT, va, pa0, pa1, pa2, pa3); partialSM(pB0, pB1, m_reg, mnB, alB);
;       if (lead) ATT_SYNC(j + 2);
;       RESC(alB); }
;     { SBAR(); qkt(pA0, pA1, (const bf16_t*)(lds + ((j + 1) & 3) * SHM_SLOT), qr, r32, hi);
;       finishSM(pB0, pB1, alB, l_reg, pa0, pa1, pa2, pa3); s16x4 va[8]; pv_rd<0>(va, vb0 + (j & 3) * (int)SHM_SLOT); SBAR();
;       if (!lead) ATT_SYNC(j + 3);
;       pv_d0_pre(o, vb0 + (j & 3) * (int)SHM_SLOT, va, pa0, pa1, pa2, pa3); partialSM(pA0, pA1, m_reg, mnA, alA);
;       if (lead) ATT_SYNC(j + 3);
;       RESC(alA); }
;   }
	v_mfma_f32_16x16x32_bf16 v[34:37], v[230:233], v[130:133], v[34:37]
	v_exp_f32_e32 v74, v74
	v_mfma_f32_16x16x32_bf16 v[38:41], v[230:233], v[138:141], v[38:41]
	v_exp_f32_e32 v75, v75
	ds_read_b64_tr_b16 v[214:215], v180 offset:8192
	ds_read_b64_tr_b16 v[216:217], v180 offset:12288
	s_waitcnt lgkmcnt(6)
	v_mfma_f32_16x16x32_bf16 v[42:45], v[234:237], v[130:133], v[42:45]
	v_exp_f32_e32 v76, v76
	v_mfma_f32_16x16x32_bf16 v[46:49], v[234:237], v[138:141], v[46:49]
	v_exp_f32_e32 v77, v77
	ds_read_b64_tr_b16 v[218:219], v181 offset:8192
	ds_read_b64_tr_b16 v[220:221], v181 offset:12288
	s_waitcnt lgkmcnt(6)
	v_mfma_f32_16x16x32_bf16 v[50:53], v[238:241], v[130:133], v[50:53]
	v_exp_f32_e32 v78, v78
	v_mfma_f32_16x16x32_bf16 v[54:57], v[238:241], v[138:141], v[54:57]
	v_exp_f32_e32 v79, v79
	ds_read_b64_tr_b16 v[222:223], v180 offset:8704
	ds_read_b64_tr_b16 v[224:225], v180 offset:12800
	s_waitcnt lgkmcnt(6)
	v_mfma_f32_16x16x32_bf16 v[58:61], v[242:245], v[130:133], v[58:61]
	v_exp_f32_e32 v80, v80
	v_mfma_f32_16x16x32_bf16 v[62:65], v[242:245], v[138:141], v[62:65]
	v_exp_f32_e32 v81, v81
	v_mfma_f32_16x16x32_bf16 v[252:255], v[194:197], v[138:141], v[252:255]
	ds_read_b64_tr_b16 v[226:227], v181 offset:8704
	ds_read_b64_tr_b16 v[228:229], v181 offset:12800
	s_waitcnt lgkmcnt(6)
	v_mfma_f32_16x16x32_bf16 v[2:5], v[214:217], v[134:137], v[2:5]
	v_exp_f32_e32 v82, v82
	v_mfma_f32_16x16x32_bf16 v[6:9], v[214:217], v[142:145], v[6:9]
	v_exp_f32_e32 v83, v83
	ds_read_b64_tr_b16 v[230:231], v180 offset:9216
	ds_read_b64_tr_b16 v[232:233], v180 offset:13312
	s_waitcnt lgkmcnt(6)
	v_mfma_f32_16x16x32_bf16 v[10:13], v[218:221], v[134:137], v[10:13]
	v_exp_f32_e32 v84, v84
	v_mfma_f32_16x16x32_bf16 v[14:17], v[218:221], v[142:145], v[14:17]
	v_exp_f32_e32 v85, v85
	ds_read_b64_tr_b16 v[234:235], v181 offset:9216
	ds_read_b64_tr_b16 v[236:237], v181 offset:13312
	s_waitcnt lgkmcnt(6)
	v_mfma_f32_16x16x32_bf16 v[18:21], v[222:225], v[134:137], v[18:21]
	v_exp_f32_e32 v86, v86
	v_mfma_f32_16x16x32_bf16 v[22:25], v[222:225], v[142:145], v[22:25]
	v_exp_f32_e32 v87, v87
	ds_read_b64_tr_b16 v[238:239], v180 offset:9728
	ds_read_b64_tr_b16 v[240:241], v180 offset:13824
	s_waitcnt lgkmcnt(6)
	v_mfma_f32_16x16x32_bf16 v[26:29], v[226:229], v[134:137], v[26:29]
	v_exp_f32_e32 v88, v88
	v_mfma_f32_16x16x32_bf16 v[30:33], v[226:229], v[142:145], v[30:33]
	v_exp_f32_e32 v89, v89
	v_mfma_f32_16x16x32_bf16 v[246:249], v[194:197], v[134:137], v[246:249]
	ds_read_b64_tr_b16 v[242:243], v181 offset:9728
	ds_read_b64_tr_b16 v[244:245], v181 offset:13824
	s_waitcnt lgkmcnt(6)
	v_mfma_f32_16x16x32_bf16 v[34:37], v[230:233], v[134:137], v[34:37]
	v_exp_f32_e32 v90, v90
	v_mfma_f32_16x16x32_bf16 v[38:41], v[230:233], v[142:145], v[38:41]
	v_exp_f32_e32 v91, v91
	s_waitcnt lgkmcnt(4)
	v_mfma_f32_16x16x32_bf16 v[42:45], v[234:237], v[134:137], v[42:45]
	v_exp_f32_e32 v92, v92
	v_mfma_f32_16x16x32_bf16 v[46:49], v[234:237], v[142:145], v[46:49]
	v_exp_f32_e32 v93, v93
	s_waitcnt lgkmcnt(2)
	v_mfma_f32_16x16x32_bf16 v[50:53], v[238:241], v[134:137], v[50:53]
	v_exp_f32_e32 v94, v94
	v_mfma_f32_16x16x32_bf16 v[54:57], v[238:241], v[142:145], v[54:57]
	v_exp_f32_e32 v95, v95
	s_waitcnt lgkmcnt(0)
	v_mfma_f32_16x16x32_bf16 v[58:61], v[242:245], v[134:137], v[58:61]
	v_exp_f32_e32 v96, v96
	v_mfma_f32_16x16x32_bf16 v[62:65], v[242:245], v[142:145], v[62:65]
	v_exp_f32_e32 v97, v97
	v_mfma_f32_16x16x32_bf16 v[252:255], v[194:197], v[142:145], v[252:255]
	s_cmp_ge_u32 s97, 131
	s_cbranch_scc1 .Lf16_se_L2
	s_waitcnt vmcnt(0) lgkmcnt(0)
	s_barrier
	s_cmp_ge_u32 s97, 130
	s_cbranch_scc1 .Lf16_se_L2
	s_add_i32 s6, s96, 0x8000
	s_mov_b32 m0, s6
	s_nop 0
	global_load_lds_dwordx4 v170, s[2:3]
	s_add_i32 m0, s6, 0x2000
	s_nop 0
	global_load_lds_dwordx4 v172, s[2:3]
	s_add_i32 m0, s6, 0x4000
	s_nop 0
	global_load_lds_dwordx4 v171, s[4:5]
	s_add_i32 m0, s6, 0x6000
	s_nop 0
	global_load_lds_dwordx4 v173, s[4:5]
	s_add_u32 s2, s2, 0x4000
	s_addc_u32 s3, s3, 0
	s_add_u32 s4, s4, 0x4000
	s_addc_u32 s5, s5, 0
.Lf16_se_L2:
	v_cvt_pk_bf16_f32 v130, v66, v67
	v_cvt_pk_bf16_f32 v131, v68, v69
	v_cvt_pk_bf16_f32 v132, v74, v75
	v_cvt_pk_bf16_f32 v133, v76, v77
	v_cvt_pk_bf16_f32 v134, v82, v83
	v_cvt_pk_bf16_f32 v135, v84, v85
	v_cvt_pk_bf16_f32 v136, v90, v91
	v_cvt_pk_bf16_f32 v137, v92, v93
	v_cvt_pk_bf16_f32 v138, v70, v71
	v_cvt_pk_bf16_f32 v139, v72, v73
	v_cvt_pk_bf16_f32 v140, v78, v79
	v_cvt_pk_bf16_f32 v141, v80, v81
	v_cvt_pk_bf16_f32 v142, v86, v87
	v_cvt_pk_bf16_f32 v143, v88, v89
	v_cvt_pk_bf16_f32 v144, v94, v95
	v_cvt_pk_bf16_f32 v145, v96, v97
	s_add_i32 s97, s97, 1
	s_cmp_lt_u32 s97, 132
	s_cbranch_scc0 .Lf16_done
; #define SBAR() __builtin_amdgcn_sched_barrier(0)
; #define RESC(a) do { if (__any((a) < 1.f)) { if (hi == 0) al_l[r32] = (a); asm volatile("s_waitcnt lgkmcnt(0)" ::: "memory"); \
;     for (int d = 0; d < 4; ++d) for (int r = 0; r < 16; ++r) o[d][r] *= al_l[crow(r, hi)]; } } while (0)
; #define ATT_SYNC(jn) do { ATT_WAIT_BAR(); if ((jn) < NT) ATT_DMA((jn), (jn) & 3); } while (0)
; template <int D0> __device__ __forceinline__ void pv_rd(s16x4 (&r)[8], int vb) {
;   r[0] = tr_read<v_rd_off(D0, 0, 0)>(vb); r[1] = tr_read<v_rd_off(D0, 0, 1)>(vb); r[2] = tr_read<v_rd_off(D0, 1, 0)>(vb); r[3] = tr_read<v_rd_off(D0, 1, 1)>(vb);
;   r[4] = tr_read<v_rd_off(D0, 2, 0)>(vb); r[5] = tr_read<v_rd_off(D0, 2, 1)>(vb); r[6] = tr_read<v_rd_off(D0, 3, 0)>(vb); r[7] = tr_read<v_rd_off(D0, 3, 1)>(vb);
; }
; __device__ __forceinline__ void pv_mm(f32x16& od, const s16x4 (&r)[8], bf16x8 pa0, bf16x8 pa1, bf16x8 pa2, bf16x8 pa3) {
;     ...
;   od = __builtin_amdgcn_mfma_f32_32x32x16_bf16(pa0, PK(r[0], r[1]), od, 0, 0, 0);
;   od = __builtin_amdgcn_mfma_f32_32x32x16_bf16(pa1, PK(r[2], r[3]), od, 0, 0, 0);
;   od = __builtin_amdgcn_mfma_f32_32x32x16_bf16(pa2, PK(r[4], r[5]), od, 0, 0, 0);
;   od = __builtin_amdgcn_mfma_f32_32x32x16_bf16(pa3, PK(r[6], r[7]), od, 0, 0, 0);
;     ...
; }
; __device__ __forceinline__ void attn_dma_body(const bf16_t* __restrict__ Qb, int ldq, int tpos0, const float* __restrict__ rope, const float* __restrict__ qgain, ...
;     ...
;   for (int j = 1; j + 1 < NT; j += 2) {
;     { SBAR(); qkt(pB0, pB1, (const bf16_t*)(lds + (j & 3) * SHM_SLOT), qr, r32, hi);
;       finishSM(pA0, pA1, alA, l_reg, pa0, pa1, pa2, pa3); s16x4 va[8]; pv_rd<0>(va, vb0 + ((j - 1) & 3) * (int)SHM_SLOT); SBAR();
;       if (!lead) ATT_SYNC(j + 2);
;       pv_d0_pre(o, vb0 + ((j - 1) & 3) * (int)SHM_SLOT, va, pa0, pa1, pa2, pa3); partialSM(pB0, pB1, m_reg, mnB, alB);
;       if (lead) ATT_SYNC(j + 2);
;       RESC(alB); }
;     { SBAR(); qkt(pA0, pA1, (const bf16_t*)(lds + ((j + 1) & 3) * SHM_SLOT), qr, r32, hi);
;       finishSM(pB0, pB1, alB, l_reg, pa0, pa1, pa2, pa3); s16x4 va[8]; pv_rd<0>(va, vb0 + (j & 3) * (int)SHM_SLOT); SBAR();
;       if (!lead) ATT_SYNC(j + 3);
;       pv_d0_pre(o, vb0 + (j & 3) * (int)SHM_SLOT, va, pa0, pa1, pa2, pa3); partialSM(pA0, pA1, m_reg, mnA, alA);
;       if (lead) ATT_SYNC(j + 3);
;       RESC(alA); }
;   }
	ds_read_b128 v[146:149], v183 offset:0
	ds_read_b128 v[150:153], v183 offset:4096
	ds_read_b128 v[154:157], v183 offset:8192
	ds_read_b128 v[158:161], v183 offset:12288
	ds_read_b128 v[198:201], v184 offset:0
	ds_read_b128 v[202:205], v184 offset:4096
	ds_read_b128 v[206:209], v184 offset:8192
	ds_read_b128 v[210:213], v184 offset:12288
	s_waitcnt lgkmcnt(7)
	v_mfma_f32_16x16x32_bf16 v[66:69], v[146:149], v[98:101], 0
	v_mfma_f32_16x16x32_bf16 v[70:73], v[146:149], v[114:117], 0
	ds_read_b128 v[146:149], v185 offset:0
	s_waitcnt lgkmcnt(7)
	v_mfma_f32_16x16x32_bf16 v[74:77], v[150:153], v[98:101], 0
	v_mfma_f32_16x16x32_bf16 v[78:81], v[150:153], v[114:117], 0
	ds_read_b128 v[150:153], v185 offset:4096
	s_waitcnt lgkmcnt(7)
	v_mfma_f32_16x16x32_bf16 v[82:85], v[154:157], v[98:101], 0
	v_mfma_f32_16x16x32_bf16 v[86:89], v[154:157], v[114:117], 0
	ds_read_b128 v[154:157], v185 offset:8192
	s_waitcnt lgkmcnt(7)
	v_mfma_f32_16x16x32_bf16 v[90:93], v[158:161], v[98:101], 0
	v_mfma_f32_16x16x32_bf16 v[94:97], v[158:161], v[114:117], 0
	ds_read_b128 v[158:161], v185 offset:12288
	s_waitcnt lgkmcnt(7)
	v_mfma_f32_16x16x32_bf16 v[66:69], v[198:201], v[102:105], v[66:69]
	v_mfma_f32_16x16x32_bf16 v[70:73], v[198:201], v[118:121], v[70:73]
	ds_read_b128 v[198:201], v186 offset:0
	s_waitcnt lgkmcnt(7)
	v_mfma_f32_16x16x32_bf16 v[74:77], v[202:205], v[102:105], v[74:77]
	v_mfma_f32_16x16x32_bf16 v[78:81], v[202:205], v[118:121], v[78:81]
	ds_read_b128 v[202:205], v186 offset:4096
	s_waitcnt lgkmcnt(7)
	v_mfma_f32_16x16x32_bf16 v[82:85], v[206:209], v[102:105], v[82:85]
	v_mfma_f32_16x16x32_bf16 v[86:89], v[206:209], v[118:121], v[86:89]
	ds_read_b128 v[206:209], v186 offset:8192
	s_waitcnt lgkmcnt(7)
	v_mfma_f32_16x16x32_bf16 v[90:93], v[210:213], v[102:105], v[90:93]
	v_mfma_f32_16x16x32_bf16 v[94:97], v[210:213], v[118:121], v[94:97]
	ds_read_b128 v[210:213], v186 offset:12288
	s_waitcnt lgkmcnt(7)
	v_mfma_f32_16x16x32_bf16 v[66:69], v[146:149], v[106:109], v[66:69]
	v_mfma_f32_16x16x32_bf16 v[70:73], v[146:149], v[122:125], v[70:73]
	s_waitcnt lgkmcnt(6)
	v_mfma_f32_16x16x32_bf16 v[74:77], v[150:153], v[106:109], v[74:77]
	v_mfma_f32_16x16x32_bf16 v[78:81], v[150:153], v[122:125], v[78:81]
	s_waitcnt lgkmcnt(5)
	v_mfma_f32_16x16x32_bf16 v[82:85], v[154:157], v[106:109], v[82:85]
	v_mfma_f32_16x16x32_bf16 v[86:89], v[154:157], v[122:125], v[86:89]
	s_waitcnt lgkmcnt(4)
	v_mfma_f32_16x16x32_bf16 v[90:93], v[158:161], v[106:109], v[90:93]
	v_mfma_f32_16x16x32_bf16 v[94:97], v[158:161], v[122:125], v[94:97]
	s_waitcnt lgkmcnt(3)
	v_mfma_f32_16x16x32_bf16 v[66:69], v[198:201], v[110:113], v[66:69]
	v_mfma_f32_16x16x32_bf16 v[70:73], v[198:201], v[126:129], v[70:73]
	ds_read_b64_tr_b16 v[214:215], v180 offset:32768
	ds_read_b64_tr_b16 v[216:217], v180 offset:36864
	ds_read_b64_tr_b16 v[218:219], v181 offset:32768
	ds_read_b64_tr_b16 v[220:221], v181 offset:36864
	ds_read_b64_tr_b16 v[222:223], v180 offset:33280
	ds_read_b64_tr_b16 v[224:225], v180 offset:37376
	ds_read_b64_tr_b16 v[226:227], v181 offset:33280
	ds_read_b64_tr_b16 v[228:229], v181 offset:37376
	s_waitcnt lgkmcnt(10)
	v_mfma_f32_16x16x32_bf16 v[74:77], v[202:205], v[110:113], v[74:77]
	v_mfma_f32_16x16x32_bf16 v[78:81], v[202:205], v[126:129], v[78:81]
	s_waitcnt lgkmcnt(9)
	v_mfma_f32_16x16x32_bf16 v[82:85], v[206:209], v[110:113], v[82:85]
	v_mfma_f32_16x16x32_bf16 v[86:89], v[206:209], v[126:129], v[86:89]
	s_waitcnt lgkmcnt(8)
	v_mfma_f32_16x16x32_bf16 v[90:93], v[210:213], v[110:113], v[90:93]
	v_mfma_f32_16x16x32_bf16 v[94:97], v[210:213], v[126:129], v[94:97]
	s_waitcnt lgkmcnt(6)
	v_mfma_f32_16x16x32_bf16 v[2:5], v[214:217], v[130:133], v[2:5]
	v_exp_f32_e32 v66, v66
	v_mfma_f32_16x16x32_bf16 v[6:9], v[214:217], v[138:141], v[6:9]
	v_exp_f32_e32 v67, v67
	ds_read_b64_tr_b16 v[230:231], v180 offset:33792
	ds_read_b64_tr_b16 v[232:233], v180 offset:37888
	s_waitcnt lgkmcnt(6)
	v_mfma_f32_16x16x32_bf16 v[10:13], v[218:221], v[130:133], v[10:13]
	v_exp_f32_e32 v68, v68
	v_mfma_f32_16x16x32_bf16 v[14:17], v[218:221], v[138:141], v[14:17]
	v_exp_f32_e32 v69, v69
	ds_read_b64_tr_b16 v[234:235], v181 offset:33792
	ds_read_b64_tr_b16 v[236:237], v181 offset:37888
	s_waitcnt lgkmcnt(6)
	v_mfma_f32_16x16x32_bf16 v[18:21], v[222:225], v[130:133], v[18:21]
	v_exp_f32_e32 v70, v70
	v_mfma_f32_16x16x32_bf16 v[22:25], v[222:225], v[138:141], v[22:25]
	v_exp_f32_e32 v71, v71
	ds_read_b64_tr_b16 v[238:239], v180 offset:34304
	ds_read_b64_tr_b16 v[240:241], v180 offset:38400
	s_waitcnt lgkmcnt(6)
	v_mfma_f32_16x16x32_bf16 v[26:29], v[226:229], v[130:133], v[26:29]
	v_exp_f32_e32 v72, v72
	v_mfma_f32_16x16x32_bf16 v[30:33], v[226:229], v[138:141], v[30:33]
	v_exp_f32_e32 v73, v73
	v_mfma_f32_16x16x32_bf16 v[246:249], v[194:197], v[130:133], v[246:249]
	ds_read_b64_tr_b16 v[242:243], v181 offset:34304
	ds_read_b64_tr_b16 v[244:245], v181 offset:38400
	s_waitcnt lgkmcnt(6)
	v_mfma_f32_16x16x32_bf16 v[34:37], v[230:233], v[130:133], v[34:37]
	v_exp_f32_e32 v74, v74
	v_mfma_f32_16x16x32_bf16 v[38:41], v[230:233], v[138:141], v[38:41]
	v_exp_f32_e32 v75, v75
	ds_read_b64_tr_b16 v[214:215], v180 offset:40960
	ds_read_b64_tr_b16 v[216:217], v180 offset:45056
	s_waitcnt lgkmcnt(6)
	v_mfma_f32_16x16x32_bf16 v[42:45], v[234:237], v[130:133], v[42:45]
	v_exp_f32_e32 v76, v76
	v_mfma_f32_16x16x32_bf16 v[46:49], v[234:237], v[138:141], v[46:49]
	v_exp_f32_e32 v77, v77
	ds_read_b64_tr_b16 v[218:219], v181 offset:40960
	ds_read_b64_tr_b16 v[220:221], v181 offset:45056
	s_waitcnt lgkmcnt(6)
; #define SBAR() __builtin_amdgcn_sched_barrier(0)
; #define RESC(a) do { if (__any((a) < 1.f)) { if (hi == 0) al_l[r32] = (a); asm volatile("s_waitcnt lgkmcnt(0)" ::: "memory"); \
;     for (int d = 0; d < 4; ++d) for (int r = 0; r < 16; ++r) o[d][r] *= al_l[crow(r, hi)]; } } while (0)
; #define RESC(a) do { if (__any((a) < 1.f)) { if (hi == 0) al_l[r32] = (a); asm volatile("s_waitcnt lgkmcnt(0)" ::: "memory"); \
;     for (int d = 0; d < 4; ++d) for (int r = 0; r < 16; ++r) o[d][r] *= al_l[crow(r, hi)]; } } while (0)
; #define ATT_SYNC(jn) do { ATT_WAIT_BAR(); if ((jn) < NT) ATT_DMA((jn), (jn) & 3); } while (0)
; __device__ __forceinline__ void attn_dma_body(const bf16_t* __restrict__ Qb, int ldq, int tpos0, const float* __restrict__ rope, const float* __restrict__ qgain, ...
;     ...
;   for (int j = 1; j + 1 < NT; j += 2) {
;     { SBAR(); qkt(pB0, pB1, (const bf16_t*)(lds + (j & 3) * SHM_SLOT), qr, r32, hi);
;       finishSM(pA0, pA1, alA, l_reg, pa0, pa1, pa2, pa3); s16x4 va[8]; pv_rd<0>(va, vb0 + ((j - 1) & 3) * (int)SHM_SLOT); SBAR();
;       if (!lead) ATT_SYNC(j + 2);
;       pv_d0_pre(o, vb0 + ((j - 1) & 3) * (int)SHM_SLOT, va, pa0, pa1, pa2, pa3); partialSM(pB0, pB1, m_reg, mnB, alB);
;       if (lead) ATT_SYNC(j + 2);
;       RESC(alB); }
;     { SBAR(); qkt(pA0, pA1, (const bf16_t*)(lds + ((j + 1) & 3) * SHM_SLOT), qr, r32, hi);
;       finishSM(pB0, pB1, alB, l_reg, pa0, pa1, pa2, pa3); s16x4 va[8]; pv_rd<0>(va, vb0 + (j & 3) * (int)SHM_SLOT); SBAR();
;       if (!lead) ATT_SYNC(j + 3);
;       pv_d0_pre(o, vb0 + (j & 3) * (int)SHM_SLOT, va, pa0, pa1, pa2, pa3); partialSM(pA0, pA1, m_reg, mnA, alA);
;       if (lead) ATT_SYNC(j + 3);
;       RESC(alA); }
;   }
;     ...
;   { SBAR(); qkt(pB0, pB1, (const bf16_t*)(lds + ((NT - 1) & 3) * SHM_SLOT), qr, r32, hi);
;     finishSM(pA0, pA1, alA, l_reg, pa0, pa1, pa2, pa3); SBAR();
;     pv_d0(o, vb0 + ((NT - 2) & 3) * (int)SHM_SLOT, pa0, pa1, pa2, pa3); partialSM(pB0, pB1, m_reg, mnB, alB);
;     RESC(alB);
;     finishSM(pB0, pB1, alB, l_reg, pa0, pa1, pa2, pa3); SBAR();
;     pv_d0(o, vb0 + ((NT - 1) & 3) * (int)SHM_SLOT, pa0, pa1, pa2, pa3); }
	v_mfma_f32_16x16x32_bf16 v[50:53], v[238:241], v[130:133], v[50:53]
	v_exp_f32_e32 v78, v78
	v_mfma_f32_16x16x32_bf16 v[54:57], v[238:241], v[138:141], v[54:57]
	v_exp_f32_e32 v79, v79
	ds_read_b64_tr_b16 v[222:223], v180 offset:41472
	ds_read_b64_tr_b16 v[224:225], v180 offset:45568
	s_waitcnt lgkmcnt(6)
	v_mfma_f32_16x16x32_bf16 v[58:61], v[242:245], v[130:133], v[58:61]
	v_exp_f32_e32 v80, v80
	v_mfma_f32_16x16x32_bf16 v[62:65], v[242:245], v[138:141], v[62:65]
	v_exp_f32_e32 v81, v81
	v_mfma_f32_16x16x32_bf16 v[252:255], v[194:197], v[138:141], v[252:255]
	ds_read_b64_tr_b16 v[226:227], v181 offset:41472
	ds_read_b64_tr_b16 v[228:229], v181 offset:45568
	s_waitcnt lgkmcnt(6)
	v_mfma_f32_16x16x32_bf16 v[2:5], v[214:217], v[134:137], v[2:5]
	v_exp_f32_e32 v82, v82
	v_mfma_f32_16x16x32_bf16 v[6:9], v[214:217], v[142:145], v[6:9]
	v_exp_f32_e32 v83, v83
	ds_read_b64_tr_b16 v[230:231], v180 offset:41984
	ds_read_b64_tr_b16 v[232:233], v180 offset:46080
	s_waitcnt lgkmcnt(6)
	v_mfma_f32_16x16x32_bf16 v[10:13], v[218:221], v[134:137], v[10:13]
	v_exp_f32_e32 v84, v84
	v_mfma_f32_16x16x32_bf16 v[14:17], v[218:221], v[142:145], v[14:17]
	v_exp_f32_e32 v85, v85
	ds_read_b64_tr_b16 v[234:235], v181 offset:41984
	ds_read_b64_tr_b16 v[236:237], v181 offset:46080
	s_waitcnt lgkmcnt(6)
	v_mfma_f32_16x16x32_bf16 v[18:21], v[222:225], v[134:137], v[18:21]
	v_exp_f32_e32 v86, v86
	v_mfma_f32_16x16x32_bf16 v[22:25], v[222:225], v[142:145], v[22:25]
	v_exp_f32_e32 v87, v87
	ds_read_b64_tr_b16 v[238:239], v180 offset:42496
	ds_read_b64_tr_b16 v[240:241], v180 offset:46592
	s_waitcnt lgkmcnt(6)
	v_mfma_f32_16x16x32_bf16 v[26:29], v[226:229], v[134:137], v[26:29]
	v_exp_f32_e32 v88, v88
	v_mfma_f32_16x16x32_bf16 v[30:33], v[226:229], v[142:145], v[30:33]
	v_exp_f32_e32 v89, v89
	v_mfma_f32_16x16x32_bf16 v[246:249], v[194:197], v[134:137], v[246:249]
	ds_read_b64_tr_b16 v[242:243], v181 offset:42496
	ds_read_b64_tr_b16 v[244:245], v181 offset:46592
	s_waitcnt lgkmcnt(6)
	v_mfma_f32_16x16x32_bf16 v[34:37], v[230:233], v[134:137], v[34:37]
	v_exp_f32_e32 v90, v90
	v_mfma_f32_16x16x32_bf16 v[38:41], v[230:233], v[142:145], v[38:41]
	v_exp_f32_e32 v91, v91
	s_waitcnt lgkmcnt(4)
	v_mfma_f32_16x16x32_bf16 v[42:45], v[234:237], v[134:137], v[42:45]
	v_exp_f32_e32 v92, v92
	v_mfma_f32_16x16x32_bf16 v[46:49], v[234:237], v[142:145], v[46:49]
	v_exp_f32_e32 v93, v93
	s_waitcnt lgkmcnt(2)
	v_mfma_f32_16x16x32_bf16 v[50:53], v[238:241], v[134:137], v[50:53]
	v_exp_f32_e32 v94, v94
	v_mfma_f32_16x16x32_bf16 v[54:57], v[238:241], v[142:145], v[54:57]
	v_exp_f32_e32 v95, v95
	s_waitcnt lgkmcnt(0)
	v_mfma_f32_16x16x32_bf16 v[58:61], v[242:245], v[134:137], v[58:61]
	v_exp_f32_e32 v96, v96
	v_mfma_f32_16x16x32_bf16 v[62:65], v[242:245], v[142:145], v[62:65]
	v_exp_f32_e32 v97, v97
	v_mfma_f32_16x16x32_bf16 v[252:255], v[194:197], v[142:145], v[252:255]
	s_cmp_ge_u32 s97, 131
	s_cbranch_scc1 .Lf16_se_L3
	s_waitcnt vmcnt(0) lgkmcnt(0)
	s_barrier
	s_cmp_ge_u32 s97, 130
	s_cbranch_scc1 .Lf16_se_L3
	s_add_i32 s6, s96, 0x10000
	s_mov_b32 m0, s6
	s_nop 0
	global_load_lds_dwordx4 v170, s[2:3]
	s_add_i32 m0, s6, 0x2000
	s_nop 0
	global_load_lds_dwordx4 v172, s[2:3]
	s_add_i32 m0, s6, 0x4000
	s_nop 0
	global_load_lds_dwordx4 v171, s[4:5]
	s_add_i32 m0, s6, 0x6000
	s_nop 0
	global_load_lds_dwordx4 v173, s[4:5]
	s_add_u32 s2, s2, 0x4000
	s_addc_u32 s3, s3, 0
	s_add_u32 s4, s4, 0x4000
	s_addc_u32 s5, s5, 0
.Lf16_se_L3:
	v_cvt_pk_bf16_f32 v130, v66, v67
	v_cvt_pk_bf16_f32 v131, v68, v69
	v_cvt_pk_bf16_f32 v132, v74, v75
	v_cvt_pk_bf16_f32 v133, v76, v77
	v_cvt_pk_bf16_f32 v134, v82, v83
	v_cvt_pk_bf16_f32 v135, v84, v85
	v_cvt_pk_bf16_f32 v136, v90, v91
	v_cvt_pk_bf16_f32 v137, v92, v93
	v_cvt_pk_bf16_f32 v138, v70, v71
	v_cvt_pk_bf16_f32 v139, v72, v73
	v_cvt_pk_bf16_f32 v140, v78, v79
	v_cvt_pk_bf16_f32 v141, v80, v81
	v_cvt_pk_bf16_f32 v142, v86, v87
	v_cvt_pk_bf16_f32 v143, v88, v89
	v_cvt_pk_bf16_f32 v144, v94, v95
	v_cvt_pk_bf16_f32 v145, v96, v97
	s_add_i32 s97, s97, 1
	s_cmp_lt_u32 s97, 132
	s_cbranch_scc0 .Lf16_done
	s_branch .Lf16_L_loop
.Lf16_done:
	s_mov_b32 s37, 0x18000
	ds_read_b64_tr_b16 v[214:215], v180 offset:32768
	ds_read_b64_tr_b16 v[216:217], v180 offset:36864
	ds_read_b64_tr_b16 v[218:219], v181 offset:32768
	ds_read_b64_tr_b16 v[220:221], v181 offset:36864
	ds_read_b64_tr_b16 v[222:223], v180 offset:33280
	ds_read_b64_tr_b16 v[224:225], v180 offset:37376
	ds_read_b64_tr_b16 v[226:227], v181 offset:33280
	ds_read_b64_tr_b16 v[228:229], v181 offset:37376
	s_waitcnt lgkmcnt(6)
	v_mfma_f32_16x16x32_bf16 v[2:5], v[214:217], v[130:133], v[2:5]
	v_mfma_f32_16x16x32_bf16 v[6:9], v[214:217], v[138:141], v[6:9]
	ds_read_b64_tr_b16 v[230:231], v180 offset:33792
	ds_read_b64_tr_b16 v[232:233], v180 offset:37888
	s_waitcnt lgkmcnt(6)
	v_mfma_f32_16x16x32_bf16 v[10:13], v[218:221], v[130:133], v[10:13]
	v_mfma_f32_16x16x32_bf16 v[14:17], v[218:221], v[138:141], v[14:17]
	ds_read_b64_tr_b16 v[234:235], v181 offset:33792
	ds_read_b64_tr_b16 v[236:237], v181 offset:37888
	s_waitcnt lgkmcnt(6)
	v_mfma_f32_16x16x32_bf16 v[18:21], v[222:225], v[130:133], v[18:21]
	v_mfma_f32_16x16x32_bf16 v[22:25], v[222:225], v[138:141], v[22:25]
	ds_read_b64_tr_b16 v[238:239], v180 offset:34304
	ds_read_b64_tr_b16 v[240:241], v180 offset:38400
	s_waitcnt lgkmcnt(6)
	v_mfma_f32_16x16x32_bf16 v[26:29], v[226:229], v[130:133], v[26:29]
	v_mfma_f32_16x16x32_bf16 v[30:33], v[226:229], v[138:141], v[30:33]
	v_mfma_f32_16x16x32_bf16 v[246:249], v[194:197], v[130:133], v[246:249]
	ds_read_b64_tr_b16 v[242:243], v181 offset:34304
	ds_read_b64_tr_b16 v[244:245], v181 offset:38400
	s_waitcnt lgkmcnt(6)
; #define SBAR() __builtin_amdgcn_sched_barrier(0)
; __device__ __forceinline__ int crow(int r, int hi) { return (r & 3) + 8 * (r >> 2) + 4 * hi; }
; #define RESC(a) do { if (__any((a) < 1.f)) { if (hi == 0) al_l[r32] = (a); asm volatile("s_waitcnt lgkmcnt(0)" ::: "memory"); \
;     for (int d = 0; d < 4; ++d) for (int r = 0; r < 16; ++r) o[d][r] *= al_l[crow(r, hi)]; } } while (0)
; #define RESC(a) do { if (__any((a) < 1.f)) { if (hi == 0) al_l[r32] = (a); asm volatile("s_waitcnt lgkmcnt(0)" ::: "memory"); \
;     for (int d = 0; d < 4; ++d) for (int r = 0; r < 16; ++r) o[d][r] *= al_l[crow(r, hi)]; } } while (0)
; __device__ __forceinline__ void attn_dma_body(const bf16_t* __restrict__ Qb, int ldq, int tpos0, const float* __restrict__ rope, const float* __restrict__ qgain, ...
;     ...
;   { SBAR(); qkt(pB0, pB1, (const bf16_t*)(lds + ((NT - 1) & 3) * SHM_SLOT), qr, r32, hi);
;     finishSM(pA0, pA1, alA, l_reg, pa0, pa1, pa2, pa3); SBAR();
;     pv_d0(o, vb0 + ((NT - 2) & 3) * (int)SHM_SLOT, pa0, pa1, pa2, pa3); partialSM(pB0, pB1, m_reg, mnB, alB);
;     RESC(alB);
;     finishSM(pB0, pB1, alB, l_reg, pa0, pa1, pa2, pa3); SBAR();
;     pv_d0(o, vb0 + ((NT - 1) & 3) * (int)SHM_SLOT, pa0, pa1, pa2, pa3); }
;   if (hi == 0) li_l[r32] = l_reg; asm volatile("s_waitcnt lgkmcnt(0)" ::: "memory");
;   float rli[16];
; #pragma unroll
;   for (int r = 0; r < 16; ++r) rli[r] = __builtin_amdgcn_rcpf(li_l[crow(r, hi)]);
;   bf16_t* Ow = Ob + (long)(wid * QBLK) * LDO;
;   asm volatile("s_waitcnt lgkmcnt(0)\n\ts_barrier" ::: "memory");
	v_mfma_f32_16x16x32_bf16 v[34:37], v[230:233], v[130:133], v[34:37]
	v_mfma_f32_16x16x32_bf16 v[38:41], v[230:233], v[138:141], v[38:41]
	ds_read_b64_tr_b16 v[214:215], v180 offset:40960
	ds_read_b64_tr_b16 v[216:217], v180 offset:45056
	s_waitcnt lgkmcnt(6)
	v_mfma_f32_16x16x32_bf16 v[42:45], v[234:237], v[130:133], v[42:45]
	v_mfma_f32_16x16x32_bf16 v[46:49], v[234:237], v[138:141], v[46:49]
	ds_read_b64_tr_b16 v[218:219], v181 offset:40960
	ds_read_b64_tr_b16 v[220:221], v181 offset:45056
	s_waitcnt lgkmcnt(6)
	v_mfma_f32_16x16x32_bf16 v[50:53], v[238:241], v[130:133], v[50:53]
	v_mfma_f32_16x16x32_bf16 v[54:57], v[238:241], v[138:141], v[54:57]
	ds_read_b64_tr_b16 v[222:223], v180 offset:41472
	ds_read_b64_tr_b16 v[224:225], v180 offset:45568
	s_waitcnt lgkmcnt(6)
	v_mfma_f32_16x16x32_bf16 v[58:61], v[242:245], v[130:133], v[58:61]
	v_mfma_f32_16x16x32_bf16 v[62:65], v[242:245], v[138:141], v[62:65]
	v_mfma_f32_16x16x32_bf16 v[252:255], v[194:197], v[138:141], v[252:255]
	ds_read_b64_tr_b16 v[226:227], v181 offset:41472
	ds_read_b64_tr_b16 v[228:229], v181 offset:45568
	s_waitcnt lgkmcnt(6)
	v_mfma_f32_16x16x32_bf16 v[2:5], v[214:217], v[134:137], v[2:5]
	v_mfma_f32_16x16x32_bf16 v[6:9], v[214:217], v[142:145], v[6:9]
	ds_read_b64_tr_b16 v[230:231], v180 offset:41984
	ds_read_b64_tr_b16 v[232:233], v180 offset:46080
	s_waitcnt lgkmcnt(6)
	v_mfma_f32_16x16x32_bf16 v[10:13], v[218:221], v[134:137], v[10:13]
	v_mfma_f32_16x16x32_bf16 v[14:17], v[218:221], v[142:145], v[14:17]
	ds_read_b64_tr_b16 v[234:235], v181 offset:41984
	ds_read_b64_tr_b16 v[236:237], v181 offset:46080
	s_waitcnt lgkmcnt(6)
	v_mfma_f32_16x16x32_bf16 v[18:21], v[222:225], v[134:137], v[18:21]
	v_mfma_f32_16x16x32_bf16 v[22:25], v[222:225], v[142:145], v[22:25]
	ds_read_b64_tr_b16 v[238:239], v180 offset:42496
	ds_read_b64_tr_b16 v[240:241], v180 offset:46592
	s_waitcnt lgkmcnt(6)
	v_mfma_f32_16x16x32_bf16 v[26:29], v[226:229], v[134:137], v[26:29]
	v_mfma_f32_16x16x32_bf16 v[30:33], v[226:229], v[142:145], v[30:33]
	v_mfma_f32_16x16x32_bf16 v[246:249], v[194:197], v[134:137], v[246:249]
	ds_read_b64_tr_b16 v[242:243], v181 offset:42496
	ds_read_b64_tr_b16 v[244:245], v181 offset:46592
	s_waitcnt lgkmcnt(6)
	v_mfma_f32_16x16x32_bf16 v[34:37], v[230:233], v[134:137], v[34:37]
	v_mfma_f32_16x16x32_bf16 v[38:41], v[230:233], v[142:145], v[38:41]
	s_waitcnt lgkmcnt(4)
	v_mfma_f32_16x16x32_bf16 v[42:45], v[234:237], v[134:137], v[42:45]
	v_mfma_f32_16x16x32_bf16 v[46:49], v[234:237], v[142:145], v[46:49]
	s_waitcnt lgkmcnt(2)
	v_mfma_f32_16x16x32_bf16 v[50:53], v[238:241], v[134:137], v[50:53]
	v_mfma_f32_16x16x32_bf16 v[54:57], v[238:241], v[142:145], v[54:57]
	s_waitcnt lgkmcnt(0)
	v_mfma_f32_16x16x32_bf16 v[58:61], v[242:245], v[134:137], v[58:61]
	v_mfma_f32_16x16x32_bf16 v[62:65], v[242:245], v[142:145], v[62:65]
	v_mfma_f32_16x16x32_bf16 v[252:255], v[194:197], v[142:145], v[252:255]
	s_nop 7
	s_nop 7
	v_mov_b32_e32 v182, v246
	v_mov_b32_e32 v195, v252
	v_rcp_f32_e32 v182, v182
	v_rcp_f32_e32 v195, v195
	s_waitcnt lgkmcnt(0)
	s_barrier
; __device__ __forceinline__ unsigned f2bf(float f) { unsigned u = __builtin_bit_cast(unsigned, f); return (u + 0x7fffu + ((u >> 16) & 1u)) >> 16; }
; __device__ __forceinline__ int crow(int r, int hi) { return (r & 3) + 8 * (r >> 2) + 4 * hi; }
; #define ATT_WAIT_BAR() asm volatile("s_waitcnt vmcnt(0) lgkmcnt(0)\n\ts_barrier" ::: "memory")
; __device__ __forceinline__ void attn_dma_body(const bf16_t* __restrict__ Qb, int ldq, int tpos0, const float* __restrict__ rope, const float* __restrict__ qgain, ...
;     ...
;   if (hi == 0) li_l[r32] = l_reg; asm volatile("s_waitcnt lgkmcnt(0)" ::: "memory");
;   float rli[16];
; #pragma unroll
;   for (int r = 0; r < 16; ++r) rli[r] = __builtin_amdgcn_rcpf(li_l[crow(r, hi)]);
;   bf16_t* Ow = Ob + (long)(wid * QBLK) * LDO;
;   asm volatile("s_waitcnt lgkmcnt(0)\n\ts_barrier" ::: "memory");
;   { char* st = lds + wid * 8704;
; #pragma unroll
;     for (int r = 0; r < 16; ++r) { const int orow = crow(r, hi);
; #pragma unroll
;       for (int d0 = 0; d0 < 4; ++d0) *(bf16_t*)(st + orow * 272 + (d0 * 32 + r32) * 2) = (bf16_t)f2bf(o[d0][r] * rli[r]); }
;     asm volatile("s_waitcnt lgkmcnt(0)" ::: "memory");
; #pragma unroll
;     for (int i = 0; i < 8; ++i) { const int c = i * 64 + lane, row = c >> 4, cc = c & 15; const u32x4 v = *(const u32x4*)(st + row * 272 + cc * 16);
;       const bf16_t* gp = Ow + (long)row * LDO + cc * 8;
;       asm volatile("global_store_dwordx4 %0, %1, off sc1\n\ts_nop 1" :: "v"(gp), "v"(v) : "memory"); } }
;   ATT_WAIT_BAR();
	v_mul_u32_u24_e32 v84, 0x2200, v179
	v_and_b32_e32 v246, 15, v167
	v_lshrrev_b32_e32 v247, 4, v167
	v_mul_u32_u24_e32 v248, 0x110, v246
	v_add_u32_e32 v248, v248, v84
	v_lshl_add_u32 v248, v247, 3, v248
	v_mul_f32_e32 v2, v2, v182
	v_mul_f32_e32 v3, v3, v182
	v_mul_f32_e32 v4, v4, v182
	v_mul_f32_e32 v5, v5, v182
	v_cvt_pk_bf16_f32 v252, v2, v3
	v_cvt_pk_bf16_f32 v253, v4, v5
	ds_write_b64 v248, v[252:253] offset:0
	v_mul_f32_e32 v6, v6, v195
	v_mul_f32_e32 v7, v7, v195
	v_mul_f32_e32 v8, v8, v195
	v_mul_f32_e32 v9, v9, v195
	v_cvt_pk_bf16_f32 v254, v6, v7
	v_cvt_pk_bf16_f32 v255, v8, v9
	ds_write_b64 v248, v[254:255] offset:4352
	v_mul_f32_e32 v10, v10, v182
	v_mul_f32_e32 v11, v11, v182
	v_mul_f32_e32 v12, v12, v182
	v_mul_f32_e32 v13, v13, v182
	v_cvt_pk_bf16_f32 v252, v10, v11
	v_cvt_pk_bf16_f32 v253, v12, v13
	ds_write_b64 v248, v[252:253] offset:32
	v_mul_f32_e32 v14, v14, v195
	v_mul_f32_e32 v15, v15, v195
	v_mul_f32_e32 v16, v16, v195
	v_mul_f32_e32 v17, v17, v195
	v_cvt_pk_bf16_f32 v254, v14, v15
	v_cvt_pk_bf16_f32 v255, v16, v17
	ds_write_b64 v248, v[254:255] offset:4384
	v_mul_f32_e32 v18, v18, v182
	v_mul_f32_e32 v19, v19, v182
	v_mul_f32_e32 v20, v20, v182
	v_mul_f32_e32 v21, v21, v182
	v_cvt_pk_bf16_f32 v252, v18, v19
	v_cvt_pk_bf16_f32 v253, v20, v21
	ds_write_b64 v248, v[252:253] offset:64
	v_mul_f32_e32 v22, v22, v195
	v_mul_f32_e32 v23, v23, v195
	v_mul_f32_e32 v24, v24, v195
	v_mul_f32_e32 v25, v25, v195
	v_cvt_pk_bf16_f32 v254, v22, v23
	v_cvt_pk_bf16_f32 v255, v24, v25
	ds_write_b64 v248, v[254:255] offset:4416
	v_mul_f32_e32 v26, v26, v182
	v_mul_f32_e32 v27, v27, v182
	v_mul_f32_e32 v28, v28, v182
	v_mul_f32_e32 v29, v29, v182
	v_cvt_pk_bf16_f32 v252, v26, v27
	v_cvt_pk_bf16_f32 v253, v28, v29
	ds_write_b64 v248, v[252:253] offset:96
	v_mul_f32_e32 v30, v30, v195
	v_mul_f32_e32 v31, v31, v195
	v_mul_f32_e32 v32, v32, v195
	v_mul_f32_e32 v33, v33, v195
	v_cvt_pk_bf16_f32 v254, v30, v31
	v_cvt_pk_bf16_f32 v255, v32, v33
	ds_write_b64 v248, v[254:255] offset:4448
	v_mul_f32_e32 v34, v34, v182
	v_mul_f32_e32 v35, v35, v182
	v_mul_f32_e32 v36, v36, v182
	v_mul_f32_e32 v37, v37, v182
	v_cvt_pk_bf16_f32 v252, v34, v35
	v_cvt_pk_bf16_f32 v253, v36, v37
	ds_write_b64 v248, v[252:253] offset:128
	v_mul_f32_e32 v38, v38, v195
	v_mul_f32_e32 v39, v39, v195
	v_mul_f32_e32 v40, v40, v195
	v_mul_f32_e32 v41, v41, v195
	v_cvt_pk_bf16_f32 v254, v38, v39
	v_cvt_pk_bf16_f32 v255, v40, v41
	ds_write_b64 v248, v[254:255] offset:4480
	v_mul_f32_e32 v42, v42, v182
	v_mul_f32_e32 v43, v43, v182
	v_mul_f32_e32 v44, v44, v182
	v_mul_f32_e32 v45, v45, v182
	v_cvt_pk_bf16_f32 v252, v42, v43
	v_cvt_pk_bf16_f32 v253, v44, v45
	ds_write_b64 v248, v[252:253] offset:160
	v_mul_f32_e32 v46, v46, v195
	v_mul_f32_e32 v47, v47, v195
	v_mul_f32_e32 v48, v48, v195
	v_mul_f32_e32 v49, v49, v195
	v_cvt_pk_bf16_f32 v254, v46, v47
	v_cvt_pk_bf16_f32 v255, v48, v49
	ds_write_b64 v248, v[254:255] offset:4512
	v_mul_f32_e32 v50, v50, v182
	v_mul_f32_e32 v51, v51, v182
	v_mul_f32_e32 v52, v52, v182
	v_mul_f32_e32 v53, v53, v182
	v_cvt_pk_bf16_f32 v252, v50, v51
	v_cvt_pk_bf16_f32 v253, v52, v53
	ds_write_b64 v248, v[252:253] offset:192
	v_mul_f32_e32 v54, v54, v195
	v_mul_f32_e32 v55, v55, v195
	v_mul_f32_e32 v56, v56, v195
	v_mul_f32_e32 v57, v57, v195
	v_cvt_pk_bf16_f32 v254, v54, v55
	v_cvt_pk_bf16_f32 v255, v56, v57
	ds_write_b64 v248, v[254:255] offset:4544
	v_mul_f32_e32 v58, v58, v182
	v_mul_f32_e32 v59, v59, v182
	v_mul_f32_e32 v60, v60, v182
	v_mul_f32_e32 v61, v61, v182
	v_cvt_pk_bf16_f32 v252, v58, v59
	v_cvt_pk_bf16_f32 v253, v60, v61
	ds_write_b64 v248, v[252:253] offset:224
	v_mul_f32_e32 v62, v62, v195
	v_mul_f32_e32 v63, v63, v195
	v_mul_f32_e32 v64, v64, v195
	v_mul_f32_e32 v65, v65, v195
	v_cvt_pk_bf16_f32 v254, v62, v63
	v_cvt_pk_bf16_f32 v255, v64, v65
	ds_write_b64 v248, v[254:255] offset:4576
	s_waitcnt lgkmcnt(0)
	s_lshl_b64 s[6:7], s[70:71], 12
	s_add_u32 s6, s23, s6
	s_addc_u32 s7, s94, s7
	s_add_u32 s6, s6, s44
	s_addc_u32 s7, s7, s45
	v_ashrrev_i32_e32 v165, 31, v164
	v_lshlrev_b64 v[66:67], 12, v[164:165]
	v_lshl_add_u64 v[6:7], s[6:7], 0, v[66:67]
	v_lshlrev_b32_e32 v162, 4, v246
	v_lshl_add_u64 v[6:7], v[6:7], 0, v[162:163]
	v_lshlrev_b32_e32 v162, 12, v247
	v_lshl_add_u64 v[6:7], v[6:7], 0, v[162:163]
	v_mul_u32_u24_e32 v249, 0x110, v247
	v_add_u32_e32 v249, v249, v84
	v_lshl_add_u32 v249, v246, 4, v249
	ds_read_b128 v[10:13], v249 offset:0
	s_mov_b64 s[8:9], 0x0
	v_lshl_add_u64 v[8:9], v[6:7], 0, s[8:9]
	s_waitcnt lgkmcnt(0)
	global_store_dwordx4 v[8:9], v[10:13], off sc1
	s_nop 1
	ds_read_b128 v[14:17], v249 offset:1088
	s_mov_b64 s[8:9], 0x4000
	v_lshl_add_u64 v[8:9], v[6:7], 0, s[8:9]
	s_waitcnt lgkmcnt(0)
	global_store_dwordx4 v[8:9], v[14:17], off sc1
	s_nop 1
	ds_read_b128 v[10:13], v249 offset:2176
	s_mov_b64 s[8:9], 0x8000
	v_lshl_add_u64 v[8:9], v[6:7], 0, s[8:9]
	s_waitcnt lgkmcnt(0)
	global_store_dwordx4 v[8:9], v[10:13], off sc1
	s_nop 1
	ds_read_b128 v[14:17], v249 offset:3264
	s_mov_b64 s[8:9], 0xc000
	v_lshl_add_u64 v[8:9], v[6:7], 0, s[8:9]
	s_waitcnt lgkmcnt(0)
	global_store_dwordx4 v[8:9], v[14:17], off sc1
	s_nop 1
	ds_read_b128 v[10:13], v249 offset:4352
	s_mov_b64 s[8:9], 0x10000
	v_lshl_add_u64 v[8:9], v[6:7], 0, s[8:9]
	s_waitcnt lgkmcnt(0)
	global_store_dwordx4 v[8:9], v[10:13], off sc1
	s_nop 1
	ds_read_b128 v[14:17], v249 offset:5440
	s_mov_b64 s[8:9], 0x14000
	v_lshl_add_u64 v[8:9], v[6:7], 0, s[8:9]
	s_waitcnt lgkmcnt(0)
	global_store_dwordx4 v[8:9], v[14:17], off sc1
	s_nop 1
	ds_read_b128 v[10:13], v249 offset:6528
	s_mov_b64 s[8:9], 0x18000
	v_lshl_add_u64 v[8:9], v[6:7], 0, s[8:9]
	s_waitcnt lgkmcnt(0)
	global_store_dwordx4 v[8:9], v[10:13], off sc1
	s_nop 1
	ds_read_b128 v[14:17], v249 offset:7616
	s_mov_b64 s[8:9], 0x1c000
	v_lshl_add_u64 v[8:9], v[6:7], 0, s[8:9]
	s_waitcnt lgkmcnt(0)
	global_store_dwordx4 v[8:9], v[14:17], off sc1
	s_nop 1
	s_waitcnt vmcnt(0) lgkmcnt(0)
	s_barrier
	v_readlane_b32 s96, v250, 4
	v_readlane_b32 s97, v250, 5
	s_setprio 0
	s_branch .LBB0_437
